# each kernel prefetches its own code into L2 with one data load per 128-byte line at entry (s_getpc), on top of 128-byte warm chains
# speedup vs baseline: 1.0378x; 1.0378x over previous
_Z7k_frontPKiS0_PiS1_PjPKfS4_S4_P15HIP_vector_typeIjLj4EES7_PKS5_IfLj4EES7_S7_:
	s_load_dword s36, s[0:1], 0x0
	s_load_dword s37, s[0:1], 0x40
	v_lshrrev_b32_e32 v1, 6, v0
	s_nop 0
	v_readfirstlane_b32 s35, v1
	s_getpc_b64 s[28:29]
	s_and_b32 s28, s28, 0xffffff00
	v_lshlrev_b32_e32 v2, 7, v0
	v_cmp_gt_u32_e32 vcc, 0x1400, v2
	s_and_saveexec_b64 s[30:31], vcc
	global_load_dword v43, v2, s[28:29]
	s_or_b64 exec, exec, s[30:31]
	s_movk_i32 s34, 0x5aa5
	s_mov_b64 exec, 0
	s_cmpk_lt_u32 s35, 8
	s_cbranch_scc1 .Lw0s0d0_16
	s_cmpk_lt_u32 s35, 12
	s_cbranch_scc1 .Lw0s0d8_16
	s_cmpk_lt_u32 s35, 14
	s_cbranch_scc1 .Lw0s0d12_16
	s_cmpk_lt_u32 s35, 15
	s_cbranch_scc1 .Lw0s0d14_16
	s_branch .Lw0t15

.Lw0b0:
	s_load_dwordx2 s[4:5], s[0:1], 0x58
	s_cmpk_gt_u32 s2, 0xce
	s_mov_b64 s[6:7], -1
	s_cbranch_scc0 .LBB0_5
	s_branch .Lmy_cvt0

.LBB0_5:
	s_andn2_b64 vcc, exec, s[6:7]
	s_cbranch_vccnz .LBB0_38
	s_add_i32 s3, s2, 0xffffff3c
	v_lshl_or_b32 v2, s3, 10, v0
	s_cmp_gt_u32 s3, 7
	s_mov_b64 s[6:7], -1
	s_cbranch_scc0 .LBB0_30
	s_load_dwordx2 s[6:7], s[0:1], 0x48
	s_cmp_gt_u32 s3, 9
	s_mov_b64 s[8:9], -1
	s_cbranch_scc0 .LBB0_27
	s_movk_i32 s8, 0x2900
	v_cmp_gt_u32_e32 vcc, s8, v2
	s_and_saveexec_b64 s[8:9], vcc
	s_cbranch_execz .LBB0_26
.Lw0t1:
	s_cbranch_execz .Lw0c1
.Lw0b1:
	s_load_dwordx2 s[10:11], s[0:1], 0x38
	v_add_u32_e32 v1, 0xffffd800, v2
	v_lshlrev_b32_e32 v4, 1, v0
	v_lshrrev_b32_e32 v1, 3, v1
	v_and_b32_e32 v4, 0x60, v4
	v_and_b32_e32 v1, 0x1ffffff8, v1
	v_and_b32_e32 v3, 15, v0
	v_add_u32_e32 v4, v1, v4
	v_cmp_gt_u32_e32 vcc, 2, v3
	v_mov_b32_e32 v1, 0
	v_lshl_or_b32 v4, v4, 1, v3
	v_mov_b32_e32 v3, 0
	s_and_saveexec_b64 s[12:13], vcc
	s_cbranch_execz .LBB0_11
	v_mov_b32_e32 v5, 0
	s_waitcnt lgkmcnt(0)
	v_lshl_add_u64 v[6:7], v[4:5], 2, s[10:11]
	global_load_dword v3, v[6:7], off
	s_waitcnt vmcnt(0)
	v_cvt_f16_f32_e32 v3, v3

.LBB0_15:
	s_or_b64 exec, exec, s[12:13]
	s_and_saveexec_b64 s[12:13], vcc
	s_cbranch_execz .LBB0_17
	v_mov_b32_e32 v5, 0
	s_waitcnt lgkmcnt(0)
	v_lshl_add_u64 v[8:9], v[4:5], 2, s[10:11]
	global_load_dword v5, v[8:9], off offset:24
	s_waitcnt vmcnt(0)
	v_cvt_f16_f32_e32 v6, v5
.LBB0_17:
.Lw0t3:
	s_cbranch_execz .Lw0c3

.LBB0_21:
	s_or_b64 exec, exec, s[12:13]
	v_mov_b32_e32 v10, 0
	v_mov_b32_e32 v11, 0
	s_and_saveexec_b64 s[12:13], vcc
	s_cbranch_execz .LBB0_23
	v_mov_b32_e32 v5, 0
	s_waitcnt lgkmcnt(0)
.Lw0t4:
	s_cbranch_execz .Lw0c4
.Lw0b4:
	v_lshl_add_u64 v[12:13], v[4:5], 2, s[10:11]
	global_load_dword v5, v[12:13], off offset:48
	s_waitcnt vmcnt(0)
	v_cvt_f16_f32_e32 v11, v5

.LBB0_25:
	s_or_b64 exec, exec, s[12:13]
	s_waitcnt lgkmcnt(0)
	s_mov_b32 s10, 0x5040100
	v_perm_b32 v11, v10, v11, s10
	v_perm_b32 v10, v8, v9, s10
	v_perm_b32 v8, v1, v3, s10
	v_mov_b32_e32 v3, 0
	v_lshl_add_u64 v[4:5], v[2:3], 4, s[6:7]
	v_add_co_u32_e32 v4, vcc, 0xfffe0000, v4
.Lw0t5:
	s_cbranch_execz .Lw0c5
.Lw0b5:
	v_perm_b32 v9, v6, v7, s10
	s_nop 0
	v_addc_co_u32_e32 v5, vcc, -1, v5, vcc
	global_store_dwordx4 v[4:5], v[8:11], off

.LBB0_27:
	s_andn2_b64 vcc, exec, s[8:9]
	s_cbranch_vccnz .LBB0_29
	s_load_dwordx2 s[8:9], s[0:1], 0x30
	v_lshlrev_b32_e32 v1, 3, v0
	v_lshrrev_b32_e32 v3, 4, v0
	v_add_u32_e32 v8, 0xffffe000, v2
	v_and_b32_e32 v1, 0x60, v1
	v_and_b32_e32 v3, 28, v3
	v_and_b32_e32 v4, 3, v0
	v_or3_b32 v1, v3, v4, v1
	v_lshlrev_b32_e32 v3, 1, v0
	v_lshrrev_b32_e32 v4, 6, v8
	v_and_b32_e32 v3, 0x60, v3
	v_and_b32_e32 v4, 0x3fffff8, v4
	v_add_u32_e32 v4, v4, v3
	v_lshlrev_b32_e32 v6, 2, v1
.Lw0t6:
	s_cbranch_execz .Lw0c6
.Lw0b6:
	v_mov_b32_e32 v7, 0
	s_waitcnt lgkmcnt(0)
	v_lshl_add_u64 v[10:11], s[8:9], 0, v[6:7]
	v_or_b32_e32 v6, 1, v4
	v_lshlrev_b64 v[14:15], 9, v[6:7]
	v_or_b32_e32 v6, 2, v4
	v_lshlrev_b64 v[16:17], 9, v[6:7]
	v_or_b32_e32 v6, 3, v4
	v_lshlrev_b64 v[18:19], 9, v[6:7]
	v_or_b32_e32 v6, 4, v4
	v_lshlrev_b64 v[20:21], 9, v[6:7]
	v_or_b32_e32 v6, 5, v4
	v_mov_b32_e32 v5, v7
	v_lshlrev_b64 v[22:23], 9, v[6:7]
	v_or_b32_e32 v6, 6, v4
	v_lshlrev_b64 v[12:13], 9, v[4:5]
	v_lshlrev_b64 v[24:25], 9, v[6:7]
	v_or_b32_e32 v6, 7, v4
	v_lshl_add_u64 v[12:13], v[10:11], 0, v[12:13]
	v_lshlrev_b64 v[4:5], 9, v[6:7]
	v_lshl_add_u64 v[14:15], v[10:11], 0, v[14:15]

.Lw0b7:
	v_lshl_add_u64 v[16:17], v[10:11], 0, v[16:17]
	v_lshl_add_u64 v[18:19], v[10:11], 0, v[18:19]
	v_lshl_add_u64 v[20:21], v[10:11], 0, v[20:21]
	v_lshl_add_u64 v[22:23], v[10:11], 0, v[22:23]
	v_lshl_add_u64 v[24:25], v[10:11], 0, v[24:25]
	v_lshl_add_u64 v[4:5], v[10:11], 0, v[4:5]
	global_load_dword v1, v[12:13], off
	global_load_dword v3, v[14:15], off
	global_load_dword v6, v[16:17], off
	global_load_dword v10, v[18:19], off
	global_load_dword v11, v[20:21], off
	global_load_dword v26, v[22:23], off
	global_load_dword v27, v[24:25], off
	global_load_dword v28, v[4:5], off
	v_mov_b32_e32 v9, v7
	v_lshl_add_u64 v[8:9], v[8:9], 4, s[6:7]

.LBB0_30:
	s_andn2_b64 vcc, exec, s[6:7]
	s_cbranch_vccnz .LBB0_32
	s_load_dwordx2 s[6:7], s[0:1], 0x28
	v_lshlrev_b32_e32 v1, 3, v0
	v_lshrrev_b32_e32 v3, 4, v2
	v_and_b32_e32 v1, 0x60, v1
	v_and_b32_e32 v4, 28, v3
	v_and_b32_e32 v5, 3, v0
	v_lshrrev_b32_e32 v6, 1, v0
	v_and_b32_e32 v6, 24, v6
	s_movk_i32 s8, 0x1e0
	v_or3_b32 v1, v1, v5, v4
.Lw0t9:
	s_cbranch_execz .Lw0c9
.Lw0b9:
	v_and_or_b32 v3, v3, s8, v6
	v_lshlrev_b32_e32 v1, 2, v1
	v_lshl_or_b32 v1, v3, 9, v1
	s_waitcnt lgkmcnt(0)
	global_load_dword v4, v1, s[6:7] offset:1024
	global_load_dword v5, v1, s[6:7] offset:1536
	global_load_dword v6, v1, s[6:7] offset:2048
	global_load_dword v7, v1, s[6:7] offset:3072
	global_load_dword v8, v1, s[6:7] offset:3584
	global_load_dword v9, v1, s[6:7] offset:2560
	global_load_dword v10, v1, s[6:7]
	global_load_dword v11, v1, s[6:7] offset:512
	s_load_dwordx2 s[6:7], s[0:1], 0x40
	v_mov_b32_e32 v3, 0
	s_waitcnt lgkmcnt(0)
	v_lshl_add_u64 v[2:3], v[2:3], 4, s[6:7]
	s_waitcnt vmcnt(6)
	v_cvt_pk_f16_f32 v5, v4, v5

.Lw0b10:
	s_waitcnt vmcnt(3)
	v_cvt_pk_f16_f32 v7, v7, v8
	s_waitcnt vmcnt(2)
	v_cvt_pk_f16_f32 v6, v6, v9
	s_waitcnt vmcnt(0)
	v_cvt_pk_f16_f32 v4, v10, v11
	global_store_dwordx4 v[2:3], v[4:7], off
.LBB0_32:
	s_cmp_eq_u32 s3, 0
	s_cselect_b64 s[6:7], -1, 0
	v_cmp_gt_u32_e32 vcc, 32, v0
	s_and_b64 s[8:9], s[6:7], vcc
	s_and_saveexec_b64 s[6:7], s[8:9]
	s_cbranch_execz .LBB0_37
	v_cmp_lt_u32_e32 vcc, 15, v0
	v_mov_b32_e32 v3, 0
	v_lshlrev_b32_e32 v2, 4, v0
	s_and_saveexec_b64 s[8:9], vcc
	s_xor_b64 s[8:9], exec, s[8:9]
	s_cbranch_execz .LBB0_35
	s_load_dwordx2 s[10:11], s[0:1], 0x60
	s_waitcnt lgkmcnt(0)
	v_lshl_add_u64 v[4:5], s[10:11], 0, v[2:3]
	v_add_co_u32_e32 v6, vcc, 0x1869000, v4
.Lw0t11:
	s_cbranch_execz .Lw0c11
.Lw0b11:
	v_mov_b32_e32 v2, v3
	s_nop 0
	v_addc_co_u32_e32 v7, vcc, 0, v5, vcc
	v_mov_b32_e32 v4, v3
	v_mov_b32_e32 v5, v3
	global_store_dwordx4 v[6:7], v[2:5], off offset:3840

.LBB0_39:
	s_andn2_b64 vcc, exec, s[4:5]
	s_cbranch_vccnz .LBB0_121
	s_mul_hi_i32 s3, s2, 0x5397829d
	s_load_dwordx4 s[4:7], s[0:1], 0x0
.Lw0t12:
	s_cbranch_execz .Lw0c12
.Lw0b12:
	s_lshr_b32 s8, s3, 31
	s_ashr_i32 s21, s3, 5
	s_add_i32 s21, s21, s8
	s_mul_i32 s3, s21, 0x62
	s_sub_i32 s25, s2, s3
	s_addk_i32 s2, 0x61
	s_cmpk_lt_u32 s2, 0xc3
	s_waitcnt lgkmcnt(0)
	s_cselect_b32 s16, s4, s6
	s_cselect_b32 s17, s5, s7
	s_add_u32 s18, s16, 0x30d400
	s_addc_u32 s19, s17, 0
	s_lshl_b32 s20, s25, 13
	s_min_i32 s24, s20, 0xc1500
	s_addk_i32 s24, 0x2000
	v_or_b32_e32 v2, s20, v0
	v_cmp_gt_i32_e32 vcc, s24, v2
	v_mov_b32_e32 v1, -1
	v_ashrrev_i32_e32 v3, 31, v2
	v_mov_b32_e32 v21, -1
	s_and_saveexec_b64 s[2:3], vcc
	s_cbranch_execz .LBB0_42
	v_lshl_add_u64 v[4:5], v[2:3], 2, s[18:19]
	global_load_dword v21, v[4:5], off nt
.LBB0_42:
	s_or_b64 exec, exec, s[2:3]
	v_or_b32_e32 v4, 0x400, v2
.Lw0t13:
	s_cbranch_execz .Lw0c13
.Lw0b13:
	v_cmp_gt_i32_e64 s[2:3], s24, v4
	v_ashrrev_i32_e32 v5, 31, v4
	s_and_saveexec_b64 s[4:5], s[2:3]
	s_cbranch_execz .LBB0_44
	v_lshl_add_u64 v[6:7], v[4:5], 2, s[18:19]
	global_load_dword v1, v[6:7], off nt

.LBB0_46:
	s_or_b64 exec, exec, s[6:7]
	v_or_b32_e32 v8, 0xc00, v2
	v_cmp_gt_i32_e64 s[6:7], s24, v8
	v_ashrrev_i32_e32 v9, 31, v8
	s_and_saveexec_b64 s[8:9], s[6:7]
.Lw0t14:
	s_cbranch_execz .Lw0c14
.Lw0b14:
	s_cbranch_execz .LBB0_48
	v_lshl_add_u64 v[10:11], v[8:9], 2, s[18:19]
	global_load_dword v18, v[10:11], off nt

.LBB0_50:
	s_or_b64 exec, exec, s[10:11]
	v_or_b32_e32 v12, 0x1400, v2
	v_cmp_gt_i32_e64 s[10:11], s24, v12
	v_ashrrev_i32_e32 v13, 31, v12
	s_and_saveexec_b64 s[12:13], s[10:11]
	s_cbranch_execz .LBB0_52
	v_lshl_add_u64 v[14:15], v[12:13], 2, s[18:19]
	global_load_dword v19, v[14:15], off nt
.LBB0_52:
.Lw0t15:
	s_cbranch_execz .Lw0c15

.LBB0_56:
	s_or_b64 exec, exec, s[22:23]
	v_mov_b32_e32 v25, 0
	v_mov_b32_e32 v27, 0
	s_and_saveexec_b64 s[18:19], vcc
	s_cbranch_execz .LBB0_58
.Lw0t16:
	s_cbranch_execz .Lw0c16
.Lw0b16:
	v_lshl_add_u64 v[2:3], v[2:3], 2, s[16:17]
	global_load_dword v27, v[2:3], off nt

.LBB0_72:
	s_or_b64 exec, exec, s[2:3]
	s_movk_i32 s2, 0xc4
	v_cmp_gt_u32_e64 s[16:17], s2, v0
.Lw0t18:
	s_cbranch_execz .Lw0c18
.Lw0b18:
	v_lshlrev_b32_e32 v2, 2, v0
	s_and_saveexec_b64 s[2:3], s[16:17]
	v_mov_b32_e32 v8, 0
	ds_write_b32 v2, v8 offset:33552
	s_or_b64 exec, exec, s[2:3]
	s_waitcnt lgkmcnt(0)
	s_waitcnt vmcnt(0)
	v_cmp_lt_i32_e32 vcc, -1, v21
	v_mov_b32_e32 v8, 0
	v_lshrrev_b32_e32 v14, 7, v21
	v_mov_b32_e32 v12, 0
	s_barrier
	s_and_saveexec_b64 s[2:3], vcc
	v_and_b32_e32 v9, 0x1fffffc, v14
	v_mov_b32_e32 v10, 1
	ds_add_rtn_u32 v12, v9, v10 offset:33552
	s_or_b64 exec, exec, s[2:3]
	v_cmp_lt_i32_e64 s[2:3], -1, v1
	v_lshrrev_b32_e32 v13, 7, v1
	s_and_saveexec_b64 s[4:5], s[2:3]
	v_and_b32_e32 v8, 0x1fffffc, v13
	v_mov_b32_e32 v9, 1
	ds_add_rtn_u32 v8, v8, v9 offset:33552
	s_or_b64 exec, exec, s[4:5]

.Lw0b19:
	v_cmp_lt_i32_e64 s[4:5], -1, v22
	v_mov_b32_e32 v9, 0
	v_lshrrev_b32_e32 v17, 7, v22
	v_mov_b32_e32 v15, 0
	s_and_saveexec_b64 s[6:7], s[4:5]
	v_and_b32_e32 v10, 0x1fffffc, v17
	v_mov_b32_e32 v11, 1
	ds_add_rtn_u32 v15, v10, v11 offset:33552
	s_or_b64 exec, exec, s[6:7]
	v_cmp_lt_i32_e64 s[6:7], -1, v18
	v_lshrrev_b32_e32 v16, 7, v18
	s_and_saveexec_b64 s[8:9], s[6:7]
	v_and_b32_e32 v9, 0x1fffffc, v16
	v_mov_b32_e32 v10, 1
	ds_add_rtn_u32 v9, v9, v10 offset:33552
	s_or_b64 exec, exec, s[8:9]
	v_cmp_lt_i32_e64 s[8:9], -1, v23
	v_mov_b32_e32 v10, 0
	v_lshrrev_b32_e32 v33, 7, v23
	v_mov_b32_e32 v28, 0
	s_and_saveexec_b64 s[10:11], s[8:9]
	v_and_b32_e32 v11, 0x1fffffc, v33
	v_mov_b32_e32 v28, 1

.Lw0b20:
	ds_add_rtn_u32 v28, v11, v28 offset:33552
	s_or_b64 exec, exec, s[10:11]
	v_cmp_lt_i32_e64 s[12:13], -1, v19
	v_lshrrev_b32_e32 v32, 7, v19
	s_and_saveexec_b64 s[10:11], s[12:13]
	v_and_b32_e32 v10, 0x1fffffc, v32
	v_mov_b32_e32 v11, 1
	ds_add_rtn_u32 v10, v10, v11 offset:33552
	s_or_b64 exec, exec, s[10:11]
	v_cmp_lt_i32_e64 s[10:11], -1, v24
	v_mov_b32_e32 v11, 0
	v_lshrrev_b32_e32 v31, 7, v24
	v_mov_b32_e32 v29, 0
	s_and_saveexec_b64 s[14:15], s[10:11]
	v_and_b32_e32 v29, 0x1fffffc, v31
	v_mov_b32_e32 v30, 1
	ds_add_rtn_u32 v29, v29, v30 offset:33552
	s_or_b64 exec, exec, s[14:15]
	v_cmp_lt_i32_e64 s[14:15], -1, v20
	v_lshrrev_b32_e32 v30, 7, v20
	s_and_saveexec_b64 s[18:19], s[14:15]
	v_and_b32_e32 v11, 0x1fffffc, v30

.Lw0b21:
	v_mov_b32_e32 v34, 1
	ds_add_rtn_u32 v11, v11, v34 offset:33552
	s_or_b64 exec, exec, s[18:19]
	v_mov_b32_e32 v34, 0
	s_waitcnt lgkmcnt(0)
	s_barrier
	s_and_saveexec_b64 s[18:19], s[16:17]
	ds_read_b32 v34, v2 offset:33552
	s_or_b64 exec, exec, s[18:19]
	s_waitcnt lgkmcnt(0)
	v_add_u32_dpp v35, v34, v34 row_shr:1 row_mask:0xf bank_mask:0xf bound_ctrl:1
	v_and_b32_e32 v36, 63, v0
	v_cmp_eq_u32_e64 s[18:19], 63, v36
	v_add_u32_dpp v35, v35, v35 row_shr:2 row_mask:0xf bank_mask:0xf bound_ctrl:1
	s_nop 1
	v_add_u32_dpp v35, v35, v35 row_shr:4 row_mask:0xf bank_mask:0xf bound_ctrl:1
	s_nop 1
	v_add_u32_dpp v35, v35, v35 row_shr:8 row_mask:0xf bank_mask:0xf bound_ctrl:1
	s_nop 1
	v_add_u32_dpp v35, v35, v35 row_bcast:15 row_mask:0xa bank_mask:0xf
	s_nop 1
	v_add_u32_dpp v35, v35, v35 row_bcast:31 row_mask:0xc bank_mask:0xf

.Lw0b22:
	s_and_saveexec_b64 s[22:23], s[18:19]
	v_lshrrev_b32_e32 v36, 4, v0
	v_and_b32_e32 v36, 60, v36
	ds_write_b32 v36, v35 offset:34336
	s_or_b64 exec, exec, s[22:23]
	s_waitcnt lgkmcnt(0)
	s_barrier
	s_and_saveexec_b64 s[18:19], s[16:17]
	s_cbranch_execz .LBB0_96
	v_mov_b32_e32 v36, 0
	ds_read_b96 v[36:38], v36 offset:34336
	s_movk_i32 s16, 0xbf
	s_movk_i32 s22, 0x7f
	v_cmp_lt_u32_e64 s[16:17], s16, v0
	v_sub_u32_e32 v35, v35, v34
	s_load_dwordx4 s[28:31], s[0:1], 0x10
	s_waitcnt lgkmcnt(0)
	v_cndmask_b32_e64 v38, 0, v38, s[16:17]
	v_cmp_lt_u32_e64 s[16:17], s22, v0
	s_nop 1
	v_cndmask_b32_e64 v37, 0, v37, s[16:17]
	v_cmp_lt_u32_e64 s[16:17], 63, v0
	s_nop 1

.Lw0b23:
	v_cndmask_b32_e64 v36, 0, v36, s[16:17]
	v_add_u32_e32 v36, v37, v36
	s_mul_i32 s16, s21, 0xc4
	v_add3_u32 v40, v38, v36, v35
	v_add_u32_e32 v35, s16, v0
	s_movk_i32 s16, 0x62
	v_mul_lo_u32 v35, v35, s16
	v_add_u32_e32 v36, s25, v35
	v_ashrrev_i32_e32 v37, 31, v36
	v_lshlrev_b64 v[36:37], 2, v[36:37]
	v_lshl_add_u64 v[38:39], s[28:29], 0, v[36:37]
	global_store_dword v[38:39], v34, off
	v_lshl_add_u64 v[34:35], s[30:31], 0, v[36:37]
	ds_write_b32 v2, v40 offset:32768
	global_store_dword v[34:35], v40, off
.LBB0_96:
	s_or_b64 exec, exec, s[18:19]
	s_waitcnt lgkmcnt(0)
	s_barrier
	s_and_saveexec_b64 s[16:17], vcc
	s_cbranch_execnz .LBB0_122
	s_or_b64 exec, exec, s[16:17]
.Lw0t24:
	s_cbranch_execz .Lw0c24
.Lw0b24:
	s_and_saveexec_b64 s[16:17], s[2:3]
	s_cbranch_execnz .LBB0_123

.LBB0_104:
	v_and_b32_e32 v1, 0x1fffffc, v30
	ds_read_b32 v1, v1 offset:32768
	v_lshlrev_b32_e32 v4, 17, v20
	s_mov_b32 s4, 0x3fe0000
	v_and_or_b32 v3, v4, s4, v3
.Lw0t25:
	s_cbranch_execz .Lw0c25
.Lw0b25:
	v_lshlrev_b32_e32 v4, 2, v11
	s_waitcnt lgkmcnt(0)
	v_lshl_add_u32 v1, v1, 2, v4
	ds_write_b32 v1, v3

.LBB0_107:
	s_or_b64 exec, exec, s[2:3]
	v_or_b32_e32 v1, 0x400, v0
.Lw0t26:
	s_cbranch_execz .Lw0c26
.Lw0b26:
	v_cmp_gt_i32_e32 vcc, s4, v1
	s_and_saveexec_b64 s[2:3], vcc
	s_cbranch_execz .LBB0_109
	ds_read_b32 v3, v2 offset:4096
	v_lshlrev_b32_e32 v1, 2, v1
	s_waitcnt lgkmcnt(0)
	global_store_dword v1, v3, s[0:1]

.LBB0_111:
	s_or_b64 exec, exec, s[2:3]
	v_or_b32_e32 v1, 0xc00, v0
	v_cmp_gt_i32_e32 vcc, s4, v1
	s_and_saveexec_b64 s[2:3], vcc
	s_cbranch_execz .LBB0_113
	ds_read_b32 v3, v2 offset:12288
	v_lshlrev_b32_e32 v1, 2, v1
	s_waitcnt lgkmcnt(0)
.Lw0t27:
	s_cbranch_execz .Lw0c27
.Lw0b27:
	global_store_dword v1, v3, s[0:1]

.LBB0_117:
	s_or_b64 exec, exec, s[2:3]
	v_or_b32_e32 v1, 0x1800, v0
	v_cmp_gt_i32_e32 vcc, s4, v1
	s_and_saveexec_b64 s[2:3], vcc
.Lw0t28:
	s_cbranch_execz .Lw0c28
.Lw0b28:
	s_cbranch_execz .LBB0_119
	ds_read_b32 v3, v2 offset:24576
	v_lshlrev_b32_e32 v1, 2, v1
	s_waitcnt lgkmcnt(0)
	global_store_dword v1, v3, s[0:1]

.LBB0_122:
	v_and_b32_e32 v14, 0x1fffffc, v14
	ds_read_b32 v14, v14 offset:32768
	v_lshlrev_b32_e32 v21, 17, v21
	s_mov_b32 s18, 0x3fe0000
	v_lshlrev_b32_e32 v12, 2, v12
	v_and_or_b32 v21, v21, s18, v27
	s_waitcnt lgkmcnt(0)
.Lw0t29:
	s_cbranch_execz .Lw0c29
.Lw0b29:
	v_lshl_add_u32 v12, v14, 2, v12
	ds_write_b32 v12, v21
	s_or_b64 exec, exec, s[16:17]
	s_and_saveexec_b64 s[16:17], s[2:3]
	s_cbranch_execz .LBB0_98

.LBB0_124:
	v_and_b32_e32 v1, 0x1fffffc, v17
	ds_read_b32 v1, v1 offset:32768
	v_lshlrev_b32_e32 v8, 17, v22
	s_mov_b32 s4, 0x3fe0000
.Lw0t30:
	s_cbranch_execz .Lw0c30
.Lw0b30:
	v_lshlrev_b32_e32 v12, 2, v15
	v_and_or_b32 v8, v8, s4, v26
	s_waitcnt lgkmcnt(0)
	v_lshl_add_u32 v1, v1, 2, v12
	ds_write_b32 v1, v8
	s_or_b64 exec, exec, s[2:3]
	s_and_saveexec_b64 s[2:3], s[6:7]
	s_cbranch_execz .LBB0_100

.Lw0b31:
	ds_read_b32 v1, v1 offset:32768
	v_lshlrev_b32_e32 v5, 17, v23
	s_mov_b32 s4, 0x3fe0000
	v_and_or_b32 v5, v5, s4, v7
	v_lshlrev_b32_e32 v7, 2, v28
	s_waitcnt lgkmcnt(0)
	v_lshl_add_u32 v1, v1, 2, v7
	ds_write_b32 v1, v5
	s_or_b64 exec, exec, s[2:3]
	s_and_saveexec_b64 s[2:3], s[12:13]
	s_cbranch_execz .LBB0_102

.Lmy_cvt0:
	s_waitcnt lgkmcnt(0)
	s_load_dwordx4 s[20:23], s[0:1], 0x50
	s_sub_i32 s3, s2, 207
	v_and_b32_e32 v1, 0x3c0, v0

.Lw0b33:
	v_and_b32_e32 v2, 63, v0
	v_lshlrev_b32_e32 v3, 5, v1
	v_lshl_or_b32 v3, v2, 4, v3
	v_and_b32_e32 v4, 1, v0
	v_lshrrev_b32_e32 v5, 1, v2
	v_lshl_or_b32 v5, v4, 5, v5
	v_add_u32_e32 v5, v5, v1
	v_lshlrev_b32_e32 v5, 4, v5
	v_cmp_eq_u32_e32 vcc, 0, v4
	s_waitcnt lgkmcnt(0)
	s_add_i32 s8, s3, 0
	s_lshl_b32 s9, s8, 10
	s_sub_i32 s9, 0x1869c0, s9
	v_cmp_ge_i32_e64 s[24:25], s9, v1
	s_add_i32 s8, s3, 0
	s_lshl_b32 s9, s8, 15
	s_add_u32 s10, s20, s9
	s_addc_u32 s11, s21, 0
	s_mov_b64 exec, s[24:25]
	global_load_dwordx4 v[8:11], v3, s[10:11] nt
	global_load_dwordx4 v[12:15], v3, s[10:11] offset:1024 nt
	s_waitcnt vmcnt(0)
	s_add_i32 s8, s3, 0
	s_lshl_b32 s9, s8, 14

.Lw0b34:
	s_add_u32 s10, s22, s9
	s_addc_u32 s11, s23, 0
	s_mov_b64 exec, s[24:25]
	v_cvt_pk_f16_f32 v8, v8, v9
	v_cvt_pk_f16_f32 v9, v10, v11
	v_cvt_pk_f16_f32 v10, v12, v13
	v_cvt_pk_f16_f32 v11, v14, v15
	v_cndmask_b32_e32 v12, v8, v10, vcc
	v_cndmask_b32_e32 v13, v9, v11, vcc
	s_nop 1
	v_mov_b32_dpp v12, v12 quad_perm:[1,0,3,2] row_mask:0xf bank_mask:0xf bound_ctrl:1
	v_mov_b32_dpp v13, v13 quad_perm:[1,0,3,2] row_mask:0xf bank_mask:0xf bound_ctrl:1
	v_cndmask_b32_e32 v8, v12, v8, vcc
	v_cndmask_b32_e32 v9, v13, v9, vcc
	v_cndmask_b32_e32 v10, v10, v12, vcc
	v_cndmask_b32_e32 v11, v11, v13, vcc
	global_store_dwordx4 v5, v[8:11], s[10:11] sc1

	.amdhsa_kernel _Z7k_frontPKiS0_PiS1_PjPKfS4_S4_P15HIP_vector_typeIjLj4EES7_PKS5_IfLj4EES7_S7_
		.amdhsa_group_segment_fixed_size 34400
		.amdhsa_private_segment_fixed_size 0
		.amdhsa_kernarg_size 104
		.amdhsa_user_sgpr_count 2
		.amdhsa_user_sgpr_dispatch_ptr 0
		.amdhsa_user_sgpr_queue_ptr 0
		.amdhsa_user_sgpr_kernarg_segment_ptr 1
		.amdhsa_user_sgpr_dispatch_id 0
		.amdhsa_user_sgpr_kernarg_preload_length 0
		.amdhsa_user_sgpr_kernarg_preload_offset 0
		.amdhsa_user_sgpr_private_segment_size 0
		.amdhsa_uses_dynamic_stack 0
		.amdhsa_enable_private_segment 0
		.amdhsa_system_sgpr_workgroup_id_x 1
		.amdhsa_system_sgpr_workgroup_id_y 0
		.amdhsa_system_sgpr_workgroup_id_z 0
		.amdhsa_system_sgpr_workgroup_info 0
		.amdhsa_system_vgpr_workitem_id 0
		.amdhsa_next_free_vgpr 44
		.amdhsa_next_free_sgpr 38
		.amdhsa_accum_offset 44
		.amdhsa_reserve_vcc 1
		.amdhsa_float_round_mode_32 0
		.amdhsa_float_round_mode_16_64 0
		.amdhsa_float_denorm_mode_32 3
		.amdhsa_float_denorm_mode_16_64 3
		.amdhsa_dx10_clamp 1
		.amdhsa_ieee_mode 1
		.amdhsa_fp16_overflow 0
		.amdhsa_tg_split 0
		.amdhsa_exception_fp_ieee_invalid_op 0
		.amdhsa_exception_fp_denorm_src 0
		.amdhsa_exception_fp_ieee_div_zero 0
		.amdhsa_exception_fp_ieee_overflow 0
		.amdhsa_exception_fp_ieee_underflow 0
		.amdhsa_exception_fp_ieee_inexact 0
		.amdhsa_exception_int_div_zero 0
	.end_amdhsa_kernel

_Z8k_bucketPKiS0_PKjPiS3_PK15HIP_vector_typeIfLj4EEPS4_IjLj4EE:
	s_load_dword s66, s[0:1], 0x0
	s_load_dword s67, s[0:1], 0x40
	v_lshrrev_b32_e32 v1, 6, v0
	s_nop 0
	v_readfirstlane_b32 s65, v1
	s_getpc_b64 s[36:37]
	s_and_b32 s36, s36, 0xffffff00
	v_lshlrev_b32_e32 v2, 7, v0
	v_cmp_gt_u32_e32 vcc, 0x3400, v2
	s_and_saveexec_b64 s[38:39], vcc
	global_load_dword v63, v2, s[36:37]
	s_or_b64 exec, exec, s[38:39]
	s_cmpk_ge_u32 s2, 585
	s_cbranch_scc1 .Lmy_cvt1_end
	s_movk_i32 s64, 0x5aa5
	s_mov_b64 exec, 0
	s_cmpk_lt_u32 s65, 8
	s_cbranch_scc1 .Lw1s0d0_16
	s_cmpk_lt_u32 s65, 12
	s_cbranch_scc1 .Lw1s0d8_16
	s_cmpk_lt_u32 s65, 14
	s_cbranch_scc1 .Lw1s0d12_16
	s_cmpk_lt_u32 s65, 15
	s_cbranch_scc1 .Lw1s0d14_16
	s_branch .Lw1t15

.Lw1b2:
	v_add_u32_dpp v3, v3, v3 row_shr:2 row_mask:0xf bank_mask:0xf bound_ctrl:1
	s_nop 1
	v_add_u32_dpp v3, v3, v3 row_shr:4 row_mask:0xf bank_mask:0xf bound_ctrl:1
	s_nop 1
	v_add_u32_dpp v4, v3, v3 row_shr:8 row_mask:0xf bank_mask:0xf bound_ctrl:1
	s_waitcnt vmcnt(0)
	v_add_u32_dpp v3, v2, v2 row_shr:1 row_mask:0xf bank_mask:0xf bound_ctrl:1
	v_add_u32_dpp v4, v4, v4 row_bcast:15 row_mask:0xa bank_mask:0xf
	s_nop 0
	v_add_u32_dpp v3, v3, v3 row_shr:2 row_mask:0xf bank_mask:0xf bound_ctrl:1
	v_mov_b32_dpp v1, v4 row_bcast:31 row_mask:0xc bank_mask:0xf
	s_nop 0
	v_add_u32_dpp v3, v3, v3 row_shr:4 row_mask:0xf bank_mask:0xf bound_ctrl:1
	s_nop 1
	v_add_u32_dpp v3, v3, v3 row_shr:8 row_mask:0xf bank_mask:0xf bound_ctrl:1
	s_nop 1
	v_add_u32_dpp v3, v3, v3 row_bcast:15 row_mask:0xa bank_mask:0xf
	s_nop 1
	v_add_u32_dpp v3, v3, v3 row_bcast:31 row_mask:0xc bank_mask:0xf
	s_and_saveexec_b64 s[6:7], s[4:5]

.Lw1b3:
	s_cbranch_execz .LBB1_7
	v_lshrrev_b32_e32 v5, 4, v0
	v_and_b32_e32 v5, 60, v5
	v_add_u32_e32 v6, 0x11b20, v5
	v_add_u32_e32 v5, 0x11b60, v5
	v_add_u32_e32 v1, v4, v1
	ds_write_b32 v5, v3
	ds_write_b32 v6, v1

.Lw1b4:
	s_waitcnt lgkmcnt(0)
	s_barrier
	ds_read_b128 v[4:7], v1
	v_mov_b32_e32 v1, 0x11b30
	ds_read_b128 v[8:11], v1
	v_mov_b32_e32 v1, 0x11b40
	s_movk_i32 s3, 0x7f
	s_waitcnt lgkmcnt(1)
	v_readfirstlane_b32 s40, v4
	v_readfirstlane_b32 s41, v5
	v_readfirstlane_b32 s42, v6
	v_readfirstlane_b32 s43, v7
	ds_read_b128 v[4:7], v1
	v_mov_b32_e32 v1, 0x11b50
	s_waitcnt lgkmcnt(1)
	v_readfirstlane_b32 s44, v8
	v_readfirstlane_b32 s45, v9
	v_readfirstlane_b32 s46, v10
	v_readfirstlane_b32 s47, v11
	ds_read_b128 v[8:11], v1
	v_mov_b32_e32 v1, 0x11b60
	s_waitcnt lgkmcnt(1)
	v_readfirstlane_b32 s48, v4

.Lw1b5:
	v_readfirstlane_b32 s49, v5
	v_readfirstlane_b32 s50, v6
	v_readfirstlane_b32 s51, v7
	s_waitcnt lgkmcnt(0)
	v_readfirstlane_b32 s52, v8
	ds_read_b128 v[4:7], v1
	v_mov_b32_e32 v8, 0x11b70
	v_readfirstlane_b32 s53, v9
	v_readfirstlane_b32 s54, v10
	v_readfirstlane_b32 s55, v11
	ds_read_b128 v[8:11], v8
	v_cmp_lt_u32_e64 s[8:9], s3, v0
	s_movk_i32 s3, 0xbf
	v_cmp_lt_u32_e64 s[10:11], s3, v0
	s_movk_i32 s3, 0xff
	v_cmp_lt_u32_e64 s[12:13], s3, v0
	s_movk_i32 s3, 0x13f
	v_cmp_gt_u32_e64 s[6:7], 64, v0
	v_cmp_lt_u32_e64 s[14:15], s3, v0
	s_movk_i32 s3, 0x17f
	s_waitcnt lgkmcnt(1)
	v_cndmask_b32_e64 v4, v4, 0, s[6:7]

.Lw1b7:
	s_movk_i32 s3, 0x23f
	v_mov_b32_e32 v8, 0x11b90
	v_cndmask_b32_e64 v11, 0, v11, s[20:21]
	ds_read_b96 v[8:10], v8
	v_cmp_lt_u32_e64 s[20:21], s3, v0
	s_movk_i32 s3, 0x27f
	s_load_dwordx2 s[24:25], s[0:1], 0x10
	s_waitcnt lgkmcnt(0)
	v_cndmask_b32_e64 v4, 0, v4, s[20:21]
	v_cmp_lt_u32_e64 s[20:21], s3, v0
	s_movk_i32 s3, 0x2bf
	v_add3_u32 v4, v11, v12, v4
	v_cndmask_b32_e64 v5, 0, v5, s[20:21]
	v_cmp_lt_u32_e64 s[20:21], s3, v0
	s_movk_i32 s3, 0x2ff
	v_lshrrev_b32_e32 v1, 6, v0
	v_cndmask_b32_e64 v6, 0, v6, s[20:21]
	v_cmp_lt_u32_e64 s[20:21], s3, v0
	s_movk_i32 s3, 0x33f

.Lw1b8:
	v_add3_u32 v4, v5, v4, v6
	v_cndmask_b32_e64 v5, 0, v7, s[20:21]
	v_cmp_lt_u32_e64 s[20:21], s3, v0
	s_movk_i32 s3, 0x37f
	s_nop 0
	v_cndmask_b32_e64 v6, 0, v8, s[20:21]
	v_cmp_lt_u32_e64 s[20:21], s3, v0
	v_add3_u32 v4, v5, v4, v6
	s_nop 0
	v_cndmask_b32_e64 v5, 0, v9, s[20:21]
	v_cmp_eq_u32_e64 s[20:21], 15, v1
	s_nop 1
	v_cndmask_b32_e64 v6, 0, v10, s[20:21]
	v_add3_u32 v4, v5, v4, v6
	s_and_saveexec_b64 s[26:27], vcc
	v_mov_b32_e32 v5, 0x11800
	v_sub_u32_e32 v2, v3, v2
	v_lshl_add_u32 v5, v0, 2, v5
	v_add_u32_e32 v2, v2, v4

.Lw1b9:
	ds_write_b32 v5, v2
	s_or_b64 exec, exec, s[26:27]
	s_movk_i32 s3, 0x61
	v_cmp_eq_u32_e32 vcc, s3, v0
	s_and_saveexec_b64 s[26:27], vcc
	v_add_u32_e32 v2, v4, v3
	v_mov_b32_e32 v3, 0x11988
	ds_write_b32 v3, v2
	s_or_b64 exec, exec, s[26:27]
	v_mov_b32_e32 v2, 0x11988
	s_waitcnt lgkmcnt(0)
	s_barrier
	ds_read_b32 v2, v2
	v_mov_b32_e32 v3, 0x11900
	s_and_b64 s[26:27], s[30:31], exec
	ds_read_b32 v5, v3
	s_cselect_b32 s26, 0xc3500, 0
	s_lshl_b32 s56, s26, 2
	s_add_u32 s28, s24, s56
	s_movk_i32 s24, 0x2001
	s_waitcnt lgkmcnt(1)
	v_cmp_gt_i32_e32 vcc, s24, v2
	v_readfirstlane_b32 s3, v2
	s_addc_u32 s29, s25, 0

.Lw1b10:
	s_mov_b64 s[34:35], -1
	s_cbranch_vccnz .LBB1_37
	s_mov_b64 s[24:25], 0
	v_mov_b32_e32 v3, 0x11880
	s_movk_i32 s36, 0x51
	s_movk_i32 s37, 0x52
	s_movk_i32 s38, 0x59
	s_movk_i32 s39, 0x5a
	s_movk_i32 s57, 0x5d
	s_movk_i32 s58, 0x5e
	s_movk_i32 s59, 0x5f
	s_movk_i32 s60, 0x60
	s_movk_i32 s61, 0x61
	v_mov_b32_e32 v4, 0x11990
	v_mov_b32_e32 v6, 1
	v_mov_b32_e32 v7, 0x11840
	v_mov_b32_e32 v8, 0x11820
	v_mov_b32_e32 v9, 0x11810
	v_mov_b32_e32 v10, 0x11808
	v_mov_b32_e32 v11, 0x11804
	v_mov_b32_e32 v12, 0x11800
	v_mov_b32_e32 v13, v0

.Lw1b11:
	s_branch .LBB1_16
.LBB1_15:
	s_or_b64 exec, exec, s[34:35]
	v_lshl_add_u32 v14, v16, 2, v4
	ds_read_b32 v14, v14
	s_waitcnt lgkmcnt(0)
	v_lshl_add_u32 v14, v16, 13, v14
	v_sub_u32_e32 v14, v14, v15
	v_add_u32_e32 v14, v13, v14
	v_ashrrev_i32_e32 v15, 31, v14
	v_lshl_add_u64 v[14:15], v[14:15], 2, s[28:29]
	global_load_dword v14, v[14:15], off
	v_add_u32_e32 v13, 0x400, v13
	v_cmp_le_i32_e32 vcc, s3, v13
	s_or_b64 s[24:25], vcc, s[24:25]
	s_waitcnt vmcnt(0)
	v_lshrrev_b32_e32 v14, 15, v14
	v_and_b32_e32 v14, 0x1fffc, v14
	v_add_u32_e32 v14, 0x10000, v14
	ds_add_u32 v14, v6
	s_andn2_b64 exec, exec, s[24:25]
	s_cbranch_execz .LBB1_36
.LBB1_16:
	s_waitcnt lgkmcnt(0)

.Lw1b12:
	v_cmp_gt_i32_e32 vcc, v5, v13
	s_nop 1
	v_cndmask_b32_e64 v14, 64, 0, vcc
	v_lshl_or_b32 v15, v14, 2, v3
	ds_read_b32 v15, v15
	v_or_b32_e32 v16, 32, v14
	s_waitcnt lgkmcnt(0)
	v_cmp_gt_i32_e32 vcc, v15, v13
	s_nop 1
	v_cndmask_b32_e32 v15, v16, v14, vcc
	v_cmp_lt_u32_e64 s[26:27], s36, v15
	v_cmp_gt_u32_e32 vcc, s37, v15
	s_and_saveexec_b64 s[34:35], vcc
	s_cbranch_execz .LBB1_18
	v_lshl_add_u32 v14, v15, 2, v7
	ds_read_b32 v16, v14
	s_andn2_b64 s[26:27], s[26:27], exec
	v_or_b32_e32 v14, 16, v15
	s_waitcnt lgkmcnt(0)
	v_cmp_gt_i32_e32 vcc, v16, v13
	s_and_b64 s[62:63], vcc, exec
	s_or_b64 s[26:27], s[26:27], s[62:63]
.LBB1_18:
	s_or_b64 exec, exec, s[34:35]
	s_and_saveexec_b64 s[34:35], s[26:27]
	v_mov_b32_e32 v14, v15

.Lw1b13:
	s_or_b64 exec, exec, s[34:35]
	v_cmp_lt_u32_e64 s[26:27], s38, v14
	v_cmp_gt_u32_e32 vcc, s39, v14
	s_and_saveexec_b64 s[34:35], vcc
	s_cbranch_execz .LBB1_22
	v_lshl_add_u32 v15, v14, 2, v8
	ds_read_b32 v16, v15
	s_andn2_b64 s[26:27], s[26:27], exec
	v_add_u32_e32 v15, 8, v14
	s_waitcnt lgkmcnt(0)
	v_cmp_gt_i32_e32 vcc, v16, v13
	s_and_b64 s[62:63], vcc, exec
	s_or_b64 s[26:27], s[26:27], s[62:63]

.LBB1_30:
	s_or_b64 exec, exec, s[34:35]
	s_and_saveexec_b64 s[34:35], s[26:27]
	v_mov_b32_e32 v14, v16
	s_or_b64 exec, exec, s[34:35]
	v_cmp_lt_u32_e64 s[26:27], s60, v14
	v_cmp_gt_u32_e32 vcc, s61, v14
	s_and_saveexec_b64 s[34:35], vcc

.Lw1b15:
	s_cbranch_execz .LBB1_34
	v_lshl_add_u32 v15, v14, 2, v11
	ds_read_b32 v15, v15
	s_andn2_b64 s[26:27], s[26:27], exec
	v_add_u32_e32 v16, 1, v14
	s_waitcnt lgkmcnt(0)
	v_cmp_gt_i32_e32 vcc, v15, v13
	s_and_b64 s[62:63], vcc, exec
	s_or_b64 s[26:27], s[26:27], s[62:63]

.LBB1_37:
	s_load_dwordx4 s[24:27], s[0:1], 0x18
	s_movk_i32 s57, 0x2000
	s_and_b64 vcc, exec, s[34:35]
	s_cbranch_vccz .LBB1_231
	s_waitcnt lgkmcnt(0)
	s_load_dwordx4 s[68:71], s[0:1], 0x28
	s_and_b64 s[36:37], s[30:31], exec
	s_cselect_b32 s72, 0xc4, 0

.Lw1b16:
	s_add_i32 s72, s72, s33
	s_addk_i32 s72, 0x190
	v_and_b32_e32 v48, 0x3c0, v0
	v_and_b32_e32 v49, 63, v0
	v_lshlrev_b32_e32 v58, 5, v48
	v_lshl_or_b32 v58, v49, 4, v58
	v_and_b32_e32 v59, 1, v0
	v_lshrrev_b32_e32 v49, 1, v49
	v_lshl_or_b32 v49, v59, 5, v49
	v_add_u32_e32 v49, v49, v48
	v_lshlrev_b32_e32 v49, 4, v49
	s_lshl_b32 s73, s72, 15
	s_waitcnt lgkmcnt(0)
	s_add_u32 s68, s68, s73
	s_addc_u32 s69, s69, 0
	s_mov_b32 s34, 0x11800
	s_movk_i32 s35, 0x62
	v_mov_b32_e32 v32, v0
	v_add_u32_e32 v33, 1024, v0
	v_add_u32_e32 v34, 2048, v0
	v_add_u32_e32 v35, 3072, v0
	v_add_u32_e32 v36, 4096, v0

.Lw1b17:
	v_add_u32_e32 v37, 5120, v0
	v_add_u32_e32 v38, 6144, v0
	v_add_u32_e32 v39, 7168, v0
	v_cmp_le_i32_e64 s[36:37], v5, v32
	v_cmp_le_i32_e64 s[38:39], v5, v33
	v_cmp_le_i32_e64 s[58:59], v5, v34
	v_cmp_le_i32_e64 s[60:61], v5, v35
	v_cndmask_b32_e64 v40, 0, 64, s[36:37]
	v_cndmask_b32_e64 v41, 0, 64, s[38:39]
	v_cndmask_b32_e64 v42, 0, 64, s[58:59]
	v_cndmask_b32_e64 v43, 0, 64, s[60:61]
	v_cmp_le_i32_e64 s[36:37], v5, v36
	v_cmp_le_i32_e64 s[38:39], v5, v37
	v_cmp_le_i32_e64 s[58:59], v5, v38
	v_cmp_le_i32_e64 s[60:61], v5, v39

.Lw1b20:
	v_cndmask_b32_e64 v41, v41, v4, s[38:39]
	v_cndmask_b32_e64 v42, v42, v6, s[58:59]
	v_cndmask_b32_e64 v43, v43, v7, s[60:61]
	s_waitcnt lgkmcnt(3)
	v_cmp_le_i32_e64 s[36:37], v15, v36
	s_waitcnt lgkmcnt(2)
	v_cmp_le_i32_e64 s[38:39], v16, v37
	s_waitcnt lgkmcnt(1)
	v_cmp_le_i32_e64 s[58:59], v17, v38
	s_waitcnt lgkmcnt(0)
	v_cmp_le_i32_e64 s[60:61], v18, v39
	v_cndmask_b32_e64 v44, v44, v8, s[36:37]
	v_cndmask_b32_e64 v45, v45, v9, s[38:39]
	v_cndmask_b32_e64 v46, v46, v10, s[58:59]
	v_cndmask_b32_e64 v47, v47, v19, s[60:61]
	v_add_u32_e32 v3, 16, v40
	v_min_u32_e32 v11, s35, v3
	v_lshl_add_u32 v11, v11, 2, s34
	ds_read_b32 v11, v11

.Lw1b21:
	v_add_u32_e32 v4, 16, v41
	v_min_u32_e32 v12, s35, v4
	v_lshl_add_u32 v12, v12, 2, s34
	ds_read_b32 v12, v12
	v_add_u32_e32 v6, 16, v42
	v_min_u32_e32 v13, s35, v6
	v_lshl_add_u32 v13, v13, 2, s34
	ds_read_b32 v13, v13
	v_add_u32_e32 v7, 16, v43
	v_min_u32_e32 v14, s35, v7
	v_lshl_add_u32 v14, v14, 2, s34
	ds_read_b32 v14, v14
	v_add_u32_e32 v8, 16, v44
	v_min_u32_e32 v15, s35, v8
	v_lshl_add_u32 v15, v15, 2, s34
	ds_read_b32 v15, v15
	v_add_u32_e32 v9, 16, v45
	v_min_u32_e32 v16, s35, v9
	v_lshl_add_u32 v16, v16, 2, s34
	ds_read_b32 v16, v16

.Lw1b22:
	v_add_u32_e32 v10, 16, v46
	v_min_u32_e32 v17, s35, v10
	v_lshl_add_u32 v17, v17, 2, s34
	ds_read_b32 v17, v17
	v_add_u32_e32 v19, 16, v47
	v_min_u32_e32 v18, s35, v19
	v_lshl_add_u32 v18, v18, 2, s34
	ds_read_b32 v18, v18
	s_waitcnt lgkmcnt(7)
	v_cmp_le_i32_e64 s[36:37], v11, v32
	s_waitcnt lgkmcnt(6)
	v_cmp_le_i32_e64 s[38:39], v12, v33
	s_waitcnt lgkmcnt(5)
	v_cmp_le_i32_e64 s[58:59], v13, v34
	s_waitcnt lgkmcnt(4)
	v_cmp_le_i32_e64 s[60:61], v14, v35
	v_cndmask_b32_e64 v40, v40, v3, s[36:37]
	v_cndmask_b32_e64 v41, v41, v4, s[38:39]
	v_cndmask_b32_e64 v42, v42, v6, s[58:59]
	v_cndmask_b32_e64 v43, v43, v7, s[60:61]

.Lw1b23:
	s_waitcnt lgkmcnt(3)
	v_cmp_le_i32_e64 s[36:37], v15, v36
	s_waitcnt lgkmcnt(2)
	v_cmp_le_i32_e64 s[38:39], v16, v37
	s_waitcnt lgkmcnt(1)
	v_cmp_le_i32_e64 s[58:59], v17, v38
	s_waitcnt lgkmcnt(0)
	v_cmp_le_i32_e64 s[60:61], v18, v39
	v_cndmask_b32_e64 v44, v44, v8, s[36:37]
	v_cndmask_b32_e64 v45, v45, v9, s[38:39]
	v_cndmask_b32_e64 v46, v46, v10, s[58:59]
	v_cndmask_b32_e64 v47, v47, v19, s[60:61]
	v_add_u32_e32 v3, 8, v40
	v_min_u32_e32 v11, s35, v3
	v_lshl_add_u32 v11, v11, 2, s34
	ds_read_b32 v11, v11
	v_add_u32_e32 v4, 8, v41
	v_min_u32_e32 v12, s35, v4
	v_lshl_add_u32 v12, v12, 2, s34

.Lw1b24:
	ds_read_b32 v12, v12
	v_add_u32_e32 v6, 8, v42
	v_min_u32_e32 v13, s35, v6
	v_lshl_add_u32 v13, v13, 2, s34
	ds_read_b32 v13, v13
	v_add_u32_e32 v7, 8, v43
	v_min_u32_e32 v14, s35, v7
	v_lshl_add_u32 v14, v14, 2, s34
	ds_read_b32 v14, v14
	v_add_u32_e32 v8, 8, v44
	v_min_u32_e32 v15, s35, v8
	v_lshl_add_u32 v15, v15, 2, s34
	ds_read_b32 v15, v15
	v_add_u32_e32 v9, 8, v45
	v_min_u32_e32 v16, s35, v9
	v_lshl_add_u32 v16, v16, 2, s34
	ds_read_b32 v16, v16
	v_add_u32_e32 v10, 8, v46
	v_min_u32_e32 v17, s35, v10
	v_lshl_add_u32 v17, v17, 2, s34
	ds_read_b32 v17, v17

.Lw1b25:
	v_add_u32_e32 v19, 8, v47
	v_min_u32_e32 v18, s35, v19
	v_lshl_add_u32 v18, v18, 2, s34
	ds_read_b32 v18, v18
	s_waitcnt lgkmcnt(7)
	v_cmp_le_i32_e64 s[36:37], v11, v32
	s_waitcnt lgkmcnt(6)
	v_cmp_le_i32_e64 s[38:39], v12, v33
	s_waitcnt lgkmcnt(5)
	v_cmp_le_i32_e64 s[58:59], v13, v34
	s_waitcnt lgkmcnt(4)
	v_cmp_le_i32_e64 s[60:61], v14, v35
	v_cndmask_b32_e64 v40, v40, v3, s[36:37]
	v_cndmask_b32_e64 v41, v41, v4, s[38:39]
	v_cndmask_b32_e64 v42, v42, v6, s[58:59]
	v_cndmask_b32_e64 v43, v43, v7, s[60:61]
	s_waitcnt lgkmcnt(3)
	v_cmp_le_i32_e64 s[36:37], v15, v36
	s_waitcnt lgkmcnt(2)

.Lw1b26:
	v_cmp_le_i32_e64 s[38:39], v16, v37
	s_waitcnt lgkmcnt(1)
	v_cmp_le_i32_e64 s[58:59], v17, v38
	s_waitcnt lgkmcnt(0)
	v_cmp_le_i32_e64 s[60:61], v18, v39
	v_cndmask_b32_e64 v44, v44, v8, s[36:37]
	v_cndmask_b32_e64 v45, v45, v9, s[38:39]
	v_cndmask_b32_e64 v46, v46, v10, s[58:59]
	v_cndmask_b32_e64 v47, v47, v19, s[60:61]
	v_add_u32_e32 v3, 4, v40
	v_min_u32_e32 v11, s35, v3
	v_lshl_add_u32 v11, v11, 2, s34
	ds_read_b32 v11, v11
	v_add_u32_e32 v4, 4, v41
	v_min_u32_e32 v12, s35, v4
	v_lshl_add_u32 v12, v12, 2, s34
	ds_read_b32 v12, v12
	v_add_u32_e32 v6, 4, v42
	v_min_u32_e32 v13, s35, v6
	v_lshl_add_u32 v13, v13, 2, s34

.Lw1b27:
	ds_read_b32 v13, v13
	v_add_u32_e32 v7, 4, v43
	v_min_u32_e32 v14, s35, v7
	v_lshl_add_u32 v14, v14, 2, s34
	ds_read_b32 v14, v14
	v_add_u32_e32 v8, 4, v44
	v_min_u32_e32 v15, s35, v8
	v_lshl_add_u32 v15, v15, 2, s34
	ds_read_b32 v15, v15
	v_add_u32_e32 v9, 4, v45
	v_min_u32_e32 v16, s35, v9
	v_lshl_add_u32 v16, v16, 2, s34
	ds_read_b32 v16, v16
	v_add_u32_e32 v10, 4, v46
	v_min_u32_e32 v17, s35, v10
	v_lshl_add_u32 v17, v17, 2, s34
	ds_read_b32 v17, v17
	v_add_u32_e32 v19, 4, v47
	v_min_u32_e32 v18, s35, v19
	v_lshl_add_u32 v18, v18, 2, s34

.Lw1b29:
	s_waitcnt lgkmcnt(0)
	v_cmp_le_i32_e64 s[60:61], v18, v39
	v_cndmask_b32_e64 v44, v44, v8, s[36:37]
	v_cndmask_b32_e64 v45, v45, v9, s[38:39]
	v_cndmask_b32_e64 v46, v46, v10, s[58:59]
	v_cndmask_b32_e64 v47, v47, v19, s[60:61]
	v_add_u32_e32 v3, 2, v40
	v_min_u32_e32 v11, s35, v3
	v_lshl_add_u32 v11, v11, 2, s34
	ds_read_b32 v11, v11
	v_add_u32_e32 v4, 2, v41
	v_min_u32_e32 v12, s35, v4
	v_lshl_add_u32 v12, v12, 2, s34
	ds_read_b32 v12, v12
	v_add_u32_e32 v6, 2, v42
	v_min_u32_e32 v13, s35, v6
	v_lshl_add_u32 v13, v13, 2, s34
	ds_read_b32 v13, v13
	v_add_u32_e32 v7, 2, v43
	v_min_u32_e32 v14, s35, v7

.Lw1b30:
	v_lshl_add_u32 v14, v14, 2, s34
	ds_read_b32 v14, v14
	v_add_u32_e32 v8, 2, v44
	v_min_u32_e32 v15, s35, v8
	v_lshl_add_u32 v15, v15, 2, s34
	ds_read_b32 v15, v15
	v_add_u32_e32 v9, 2, v45
	v_min_u32_e32 v16, s35, v9
	v_lshl_add_u32 v16, v16, 2, s34
	ds_read_b32 v16, v16
	v_add_u32_e32 v10, 2, v46
	v_min_u32_e32 v17, s35, v10
	v_lshl_add_u32 v17, v17, 2, s34
	ds_read_b32 v17, v17
	v_add_u32_e32 v19, 2, v47
	v_min_u32_e32 v18, s35, v19
	v_lshl_add_u32 v18, v18, 2, s34
	ds_read_b32 v18, v18
	s_waitcnt lgkmcnt(7)
	v_cmp_le_i32_e64 s[36:37], v11, v32

.Lw1b32:
	v_cndmask_b32_e64 v45, v45, v9, s[38:39]
	v_cndmask_b32_e64 v46, v46, v10, s[58:59]
	v_cndmask_b32_e64 v47, v47, v19, s[60:61]
	v_add_u32_e32 v3, 1, v40
	v_min_u32_e32 v11, s35, v3
	v_lshl_add_u32 v11, v11, 2, s34
	ds_read_b32 v11, v11
	v_add_u32_e32 v4, 1, v41
	v_min_u32_e32 v12, s35, v4
	v_lshl_add_u32 v12, v12, 2, s34
	ds_read_b32 v12, v12
	v_add_u32_e32 v6, 1, v42
	v_min_u32_e32 v13, s35, v6
	v_lshl_add_u32 v13, v13, 2, s34
	ds_read_b32 v13, v13
	v_add_u32_e32 v7, 1, v43
	v_min_u32_e32 v14, s35, v7
	v_lshl_add_u32 v14, v14, 2, s34
	ds_read_b32 v14, v14
	v_add_u32_e32 v8, 1, v44

.Lw1b33:
	v_min_u32_e32 v15, s35, v8
	v_lshl_add_u32 v15, v15, 2, s34
	ds_read_b32 v15, v15
	v_add_u32_e32 v9, 1, v45
	v_min_u32_e32 v16, s35, v9
	v_lshl_add_u32 v16, v16, 2, s34
	ds_read_b32 v16, v16
	v_add_u32_e32 v10, 1, v46
	v_min_u32_e32 v17, s35, v10
	v_lshl_add_u32 v17, v17, 2, s34
	ds_read_b32 v17, v17
	v_add_u32_e32 v19, 1, v47
	v_min_u32_e32 v18, s35, v19
	v_lshl_add_u32 v18, v18, 2, s34
	ds_read_b32 v18, v18
	s_waitcnt lgkmcnt(7)
	v_cmp_le_i32_e64 s[36:37], v11, v32
	s_waitcnt lgkmcnt(6)
	v_cmp_le_i32_e64 s[38:39], v12, v33
	s_waitcnt lgkmcnt(5)
	v_cmp_le_i32_e64 s[58:59], v13, v34

.Lw1b34:
	s_waitcnt lgkmcnt(4)
	v_cmp_le_i32_e64 s[60:61], v14, v35
	v_cndmask_b32_e64 v40, v40, v3, s[36:37]
	v_cndmask_b32_e64 v41, v41, v4, s[38:39]
	v_cndmask_b32_e64 v42, v42, v6, s[58:59]
	v_cndmask_b32_e64 v43, v43, v7, s[60:61]
	s_waitcnt lgkmcnt(3)
	v_cmp_le_i32_e64 s[36:37], v15, v36
	s_waitcnt lgkmcnt(2)
	v_cmp_le_i32_e64 s[38:39], v16, v37
	s_waitcnt lgkmcnt(1)
	v_cmp_le_i32_e64 s[58:59], v17, v38
	s_waitcnt lgkmcnt(0)
	v_cmp_le_i32_e64 s[60:61], v18, v39
	v_cndmask_b32_e64 v44, v44, v8, s[36:37]
	v_cndmask_b32_e64 v45, v45, v9, s[38:39]
	v_cndmask_b32_e64 v46, v46, v10, s[58:59]
	v_cndmask_b32_e64 v47, v47, v19, s[60:61]

.Lw1b35:
	v_lshl_add_u32 v11, v40, 2, s34
	ds_read_b32 v3, v11
	ds_read_b32 v11, v11 offset:400
	v_lshl_add_u32 v12, v41, 2, s34
	ds_read_b32 v4, v12
	ds_read_b32 v12, v12 offset:400
	v_lshl_add_u32 v13, v42, 2, s34
	ds_read_b32 v6, v13
	ds_read_b32 v13, v13 offset:400
	v_lshl_add_u32 v14, v43, 2, s34
	ds_read_b32 v7, v14
	ds_read_b32 v14, v14 offset:400
	v_lshl_add_u32 v15, v44, 2, s34
	ds_read_b32 v8, v15
	ds_read_b32 v15, v15 offset:400

.Lw1b36:
	v_lshl_add_u32 v16, v45, 2, s34
	ds_read_b32 v9, v16
	ds_read_b32 v16, v16 offset:400
	v_lshl_add_u32 v17, v46, 2, s34
	ds_read_b32 v10, v17
	ds_read_b32 v17, v17 offset:400
	v_lshl_add_u32 v18, v47, 2, s34
	ds_read_b32 v19, v18
	ds_read_b32 v18, v18 offset:400
	s_waitcnt lgkmcnt(14)
	v_sub_u32_e32 v3, v32, v3
	v_lshl_add_u32 v40, v40, 13, v3
	v_add_lshl_u32 v40, v40, v11, 2
	s_waitcnt lgkmcnt(12)
	v_sub_u32_e32 v4, v33, v4
	v_lshl_add_u32 v41, v41, 13, v4
	v_add_lshl_u32 v41, v41, v12, 2
	s_waitcnt lgkmcnt(10)

.Lw1b37:
	v_sub_u32_e32 v6, v34, v6
	v_lshl_add_u32 v42, v42, 13, v6
	v_add_lshl_u32 v42, v42, v13, 2
	s_waitcnt lgkmcnt(8)
	v_sub_u32_e32 v7, v35, v7
	v_lshl_add_u32 v43, v43, 13, v7
	v_add_lshl_u32 v43, v43, v14, 2
	s_waitcnt lgkmcnt(6)
	v_sub_u32_e32 v8, v36, v8
	v_lshl_add_u32 v44, v44, 13, v8
	v_add_lshl_u32 v44, v44, v15, 2
	s_waitcnt lgkmcnt(4)
	v_sub_u32_e32 v9, v37, v9
	v_lshl_add_u32 v45, v45, 13, v9
	v_add_lshl_u32 v45, v45, v16, 2
	s_waitcnt lgkmcnt(2)
	v_sub_u32_e32 v10, v38, v10
	v_lshl_add_u32 v46, v46, 13, v10
	v_add_lshl_u32 v46, v46, v17, 2
	s_waitcnt lgkmcnt(0)
	v_sub_u32_e32 v19, v39, v19

.Lw1b38:
	v_lshl_add_u32 v47, v47, 13, v19
	v_add_lshl_u32 v47, v47, v18, 2
	v_cmp_gt_i32_e64 s[36:37], s3, v32
	v_mov_b32_e32 v3, -1
	s_mov_b64 exec, s[36:37]
	global_load_dword v3, v40, s[28:29]
	s_mov_b64 exec, -1
	v_cmp_gt_i32_e64 s[38:39], s3, v33
	v_mov_b32_e32 v4, -1
	s_mov_b64 exec, s[38:39]
	global_load_dword v4, v41, s[28:29]
	s_mov_b64 exec, -1
	v_cmp_gt_i32_e64 s[58:59], s3, v34
	v_mov_b32_e32 v6, -1
	s_mov_b64 exec, s[58:59]
	global_load_dword v6, v42, s[28:29]
	s_mov_b64 exec, -1
	v_cmp_gt_i32_e64 s[60:61], s3, v35
	v_mov_b32_e32 v7, -1
	s_mov_b64 exec, s[60:61]
	global_load_dword v7, v43, s[28:29]

.Lw1b40:
	global_load_dwordx4 v[54:57], v58, s[68:69] offset:1024 nt
	v_mov_b32_e32 v19, 1
	s_waitcnt vmcnt(9)
	v_cmp_ne_u32_e64 s[36:37], -1, v3
	v_lshrrev_b32_e32 v32, 15, v3
	v_and_b32_e32 v32, 0x1fffc, v32
	v_add_u32_e32 v32, 0x10000, v32
	v_mov_b32_e32 v15, 0
	s_mov_b64 exec, s[36:37]
	ds_add_rtn_u32 v15, v32, v19
	s_mov_b64 exec, -1
	s_waitcnt vmcnt(8)
	v_cmp_ne_u32_e64 s[38:39], -1, v4
	v_lshrrev_b32_e32 v33, 15, v4
	v_and_b32_e32 v33, 0x1fffc, v33
	v_add_u32_e32 v33, 0x10000, v33
	v_mov_b32_e32 v5, 0
	s_mov_b64 exec, s[38:39]
	ds_add_rtn_u32 v5, v33, v19
	s_mov_b64 exec, -1
	s_waitcnt vmcnt(7)
	v_cmp_ne_u32_e64 s[58:59], -1, v6

.Lw1b41:
	v_lshrrev_b32_e32 v34, 15, v6
	v_and_b32_e32 v34, 0x1fffc, v34
	v_add_u32_e32 v34, 0x10000, v34
	v_mov_b32_e32 v16, 0
	s_mov_b64 exec, s[58:59]
	ds_add_rtn_u32 v16, v34, v19
	s_mov_b64 exec, -1
	s_waitcnt vmcnt(6)
	v_cmp_ne_u32_e64 s[60:61], -1, v7
	v_lshrrev_b32_e32 v35, 15, v7
	v_and_b32_e32 v35, 0x1fffc, v35
	v_add_u32_e32 v35, 0x10000, v35
	v_mov_b32_e32 v11, 0
	s_mov_b64 exec, s[60:61]
	ds_add_rtn_u32 v11, v35, v19
	s_mov_b64 exec, -1
	s_waitcnt vmcnt(5)
	v_cmp_ne_u32_e64 s[36:37], -1, v8
	v_lshrrev_b32_e32 v36, 15, v8
	v_and_b32_e32 v36, 0x1fffc, v36
	v_add_u32_e32 v36, 0x10000, v36

.Lw1b42:
	v_mov_b32_e32 v17, 0
	s_mov_b64 exec, s[36:37]
	ds_add_rtn_u32 v17, v36, v19
	s_mov_b64 exec, -1
	s_waitcnt vmcnt(4)
	v_cmp_ne_u32_e64 s[38:39], -1, v9
	v_lshrrev_b32_e32 v37, 15, v9
	v_and_b32_e32 v37, 0x1fffc, v37
	v_add_u32_e32 v37, 0x10000, v37
	v_mov_b32_e32 v12, 0
	s_mov_b64 exec, s[38:39]
	ds_add_rtn_u32 v12, v37, v19
	s_mov_b64 exec, -1
	s_waitcnt vmcnt(3)
	v_cmp_ne_u32_e64 s[58:59], -1, v10
	v_lshrrev_b32_e32 v38, 15, v10
	v_and_b32_e32 v38, 0x1fffc, v38
	v_add_u32_e32 v38, 0x10000, v38
	v_mov_b32_e32 v18, 0
	s_mov_b64 exec, s[58:59]
	ds_add_rtn_u32 v18, v38, v19

.Lw1b43:
	s_mov_b64 exec, -1
	s_waitcnt vmcnt(2)
	v_cmp_ne_u32_e64 s[60:61], -1, v13
	v_lshrrev_b32_e32 v39, 15, v13
	v_and_b32_e32 v39, 0x1fffc, v39
	v_add_u32_e32 v39, 0x10000, v39
	v_mov_b32_e32 v14, 0
	s_mov_b64 exec, s[60:61]
	ds_add_rtn_u32 v14, v39, v19
	s_mov_b64 exec, -1
	s_waitcnt vmcnt(0)
	s_lshl_b32 s73, s72, 14
	s_add_u32 s70, s70, s73
	s_addc_u32 s71, s71, 0
	v_cmp_eq_u32_e64 s[36:37], 0, v59
	v_cvt_pk_f16_f32 v50, v50, v51
	v_cvt_pk_f16_f32 v51, v52, v53
	v_cvt_pk_f16_f32 v52, v54, v55
	v_cvt_pk_f16_f32 v53, v56, v57
	v_cndmask_b32_e64 v54, v50, v52, s[36:37]
	v_cndmask_b32_e64 v55, v51, v53, s[36:37]

.Lw1b44:
	s_nop 1
	v_mov_b32_dpp v54, v54 quad_perm:[1,0,3,2] row_mask:0xf bank_mask:0xf bound_ctrl:1
	v_mov_b32_dpp v55, v55 quad_perm:[1,0,3,2] row_mask:0xf bank_mask:0xf bound_ctrl:1
	v_cndmask_b32_e64 v50, v54, v50, s[36:37]
	v_cndmask_b32_e64 v51, v55, v51, s[36:37]
	v_cndmask_b32_e64 v52, v52, v54, s[36:37]
	v_cndmask_b32_e64 v53, v53, v55, s[36:37]
	global_store_dwordx4 v49, v[50:53], s[70:71] sc1
	s_branch .LBB1_232

.LBB1_232:
	v_cmp_lt_i32_e32 vcc, s57, v2
	v_mov_b32_e32 v2, 0
	s_waitcnt lgkmcnt(0)
	s_barrier
	s_and_saveexec_b64 s[34:35], s[22:23]
	v_mov_b32_e32 v2, 0x10000

.Lw1b45:
	v_lshl_or_b32 v2, v0, 2, v2
	ds_read_b32 v2, v2
	s_or_b64 exec, exec, s[34:35]
	s_waitcnt lgkmcnt(0)
	v_add_u32_dpp v19, v2, v2 row_shr:1 row_mask:0xf bank_mask:0xf bound_ctrl:1
	s_nop 1
	v_add_u32_dpp v19, v19, v19 row_shr:2 row_mask:0xf bank_mask:0xf bound_ctrl:1
	s_nop 1
	v_add_u32_dpp v19, v19, v19 row_shr:4 row_mask:0xf bank_mask:0xf bound_ctrl:1
	s_nop 1
	v_add_u32_dpp v19, v19, v19 row_shr:8 row_mask:0xf bank_mask:0xf bound_ctrl:1
	s_nop 1
	v_add_u32_dpp v19, v19, v19 row_bcast:15 row_mask:0xa bank_mask:0xf
	s_nop 1
	v_add_u32_dpp v19, v19, v19 row_bcast:31 row_mask:0xc bank_mask:0xf
	s_and_saveexec_b64 s[34:35], s[4:5]
	v_mov_b32_e32 v20, 0x11b60
	v_lshl_add_u32 v1, v1, 2, v20
	ds_write_b32 v1, v19

.Lw1b46:
	s_or_b64 exec, exec, s[34:35]
	s_add_i32 s41, s41, s40
	s_add_i32 s42, s42, s41
	s_add_i32 s43, s43, s42
	s_add_i32 s44, s44, s43
	s_add_i32 s45, s45, s44
	s_add_i32 s46, s46, s45
	s_add_i32 s47, s47, s46
	s_add_i32 s48, s48, s47
	s_add_i32 s49, s49, s48
	s_add_i32 s50, s50, s49
	s_add_i32 s51, s51, s50
	s_add_i32 s52, s52, s51
	s_add_i32 s53, s53, s52
	s_add_i32 s54, s54, s53
	s_add_i32 s34, s55, s54
	s_waitcnt lgkmcnt(0)
	s_barrier
	s_and_saveexec_b64 s[36:37], s[22:23]
	s_cbranch_execz .LBB1_239
	v_mov_b32_e32 v1, 0x11b98
	v_mov_b32_e32 v20, 0x11b70
	ds_read_b32 v1, v1
	ds_read_b96 v[24:26], v20
	v_mov_b32_e32 v20, 0x11b60
	ds_read_b128 v[20:23], v20

.Lw1b47:
	v_sub_u32_e32 v2, v19, v2
	s_waitcnt lgkmcnt(2)
	v_cndmask_b32_e64 v1, 0, v1, s[20:21]
	s_waitcnt lgkmcnt(1)
	v_cndmask_b32_e64 v24, 0, v24, s[14:15]
	v_cndmask_b32_e64 v26, 0, v26, s[18:19]
	s_waitcnt lgkmcnt(0)
	v_cndmask_b32_e64 v22, 0, v22, s[10:11]
	v_cndmask_b32_e64 v21, 0, v21, s[8:9]
	v_cndmask_b32_e64 v20, v20, 0, s[6:7]
	v_cndmask_b32_e64 v23, 0, v23, s[12:13]
	v_add3_u32 v20, v21, v20, v22
	v_cndmask_b32_e64 v25, 0, v25, s[16:17]
	v_add3_u32 v20, v23, v20, v24
	v_add3_u32 v20, v25, v20, v26
	v_add3_u32 v1, v1, v20, v2
	v_mov_b32_e32 v2, 0x11000

.LBB1_239:
	s_or_b64 exec, exec, s[36:37]
	s_cmpk_eq_i32 s33, 0xc3
	s_cselect_b64 s[6:7], -1, 0
	v_cmp_eq_u32_e64 s[4:5], 0, v0
	s_and_b64 s[6:7], s[4:5], s[6:7]
	s_and_saveexec_b64 s[4:5], s[6:7]
	s_cbranch_execz .LBB1_241
	s_and_b64 s[6:7], s[30:31], exec
	s_cselect_b32 s6, 0x61a84, 0

.Lw1b49:
	s_add_u32 s6, s24, s6
	s_addc_u32 s7, s25, 0
	v_mov_b32_e32 v1, 0x61000
	v_mov_b32_e32 v2, 0xc3500
	global_store_dword v1, v2, s[6:7] offset:2688
.LBB1_241:
	s_or_b64 exec, exec, s[4:5]
	s_add_u32 s6, s26, s56
	s_addc_u32 s7, s27, 0
	s_ashr_i32 s35, s34, 31
	s_lshl_b64 s[4:5], s[34:35], 2
	s_add_u32 s8, s6, s4
	s_addc_u32 s9, s7, s5
	s_mov_b64 s[4:5], -1
	s_and_b64 vcc, exec, vcc
	s_waitcnt lgkmcnt(0)
	s_barrier
	s_cbranch_vccz .LBB1_265
	v_mov_b32_e32 v1, 0x11900
	ds_read_b32 v1, v1
	s_mov_b64 s[4:5], 0
	v_mov_b32_e32 v2, 0x11880
	s_movk_i32 s12, 0x51
	s_movk_i32 s13, 0x52

.Lw1b50:
	s_movk_i32 s14, 0x59
	s_movk_i32 s15, 0x5a
	s_movk_i32 s16, 0x5d
	s_movk_i32 s17, 0x5e
	s_movk_i32 s18, 0x5f
	s_movk_i32 s19, 0x60
	s_movk_i32 s20, 0x61
	v_mov_b32_e32 v19, 0x11990
	v_mov_b32_e32 v20, 1
	v_mov_b32_e32 v21, 0x11840
	v_mov_b32_e32 v22, 0x11820
	v_mov_b32_e32 v23, 0x11810
	v_mov_b32_e32 v24, 0x11808
	v_mov_b32_e32 v25, 0x11804
	v_mov_b32_e32 v26, 0x11800
	v_mov_b32_e32 v27, v0
	s_branch .LBB1_244
.LBB1_243:
	s_or_b64 exec, exec, s[10:11]
	v_lshl_add_u32 v28, v30, 2, v19
	ds_read_b32 v28, v28
	s_waitcnt lgkmcnt(0)
	v_lshl_add_u32 v28, v30, 13, v28

.Lw1b51:
	v_sub_u32_e32 v28, v28, v29
	v_add_u32_e32 v28, v27, v28
	v_ashrrev_i32_e32 v29, 31, v28
	v_lshl_add_u64 v[28:29], v[28:29], 2, s[28:29]
	global_load_dword v28, v[28:29], off
	v_add_u32_e32 v27, 0x400, v27
	v_cmp_le_i32_e32 vcc, s3, v27
	s_or_b64 s[4:5], vcc, s[4:5]
	s_waitcnt vmcnt(0)
	v_lshrrev_b32_e32 v29, 15, v28
	v_and_b32_e32 v29, 0x1fffc, v29
	v_add_u32_e32 v30, 0x11000, v29
	v_add_u32_e32 v29, 0x10800, v29
	ds_read_b32 v30, v30
	ds_add_rtn_u32 v29, v29, v20
	v_and_b32_e32 v31, 0x1fffff, v28
	s_waitcnt lgkmcnt(0)
	v_add_u32_e32 v28, v29, v30
	v_ashrrev_i32_e32 v29, 31, v28
	v_lshl_add_u64 v[28:29], v[28:29], 2, s[8:9]

.LBB1_244:
	s_waitcnt lgkmcnt(0)
	v_cmp_gt_i32_e32 vcc, v1, v27
	s_nop 1
	v_cndmask_b32_e64 v28, 64, 0, vcc
	v_lshl_or_b32 v29, v28, 2, v2
	ds_read_b32 v29, v29
	v_or_b32_e32 v30, 32, v28
	s_waitcnt lgkmcnt(0)
	v_cmp_gt_i32_e32 vcc, v29, v27
	s_nop 1
	v_cndmask_b32_e32 v29, v30, v28, vcc
	v_cmp_lt_u32_e64 s[6:7], s12, v29
	v_cmp_gt_u32_e32 vcc, s13, v29
	s_and_saveexec_b64 s[10:11], vcc
	s_cbranch_execz .LBB1_246
	v_lshl_add_u32 v28, v29, 2, v21
	ds_read_b32 v30, v28
	s_andn2_b64 s[6:7], s[6:7], exec
	v_or_b32_e32 v28, 16, v29
	s_waitcnt lgkmcnt(0)
	v_cmp_gt_i32_e32 vcc, v30, v27

.LBB1_250:
	s_or_b64 exec, exec, s[10:11]
	s_and_saveexec_b64 s[10:11], s[6:7]
	v_mov_b32_e32 v29, v28
	s_or_b64 exec, exec, s[10:11]
	v_cmp_lt_u32_e64 s[6:7], s16, v29
	v_cmp_gt_u32_e32 vcc, s17, v29
	s_and_saveexec_b64 s[10:11], vcc
	s_cbranch_execz .LBB1_254
	v_lshl_add_u32 v28, v29, 2, v23

.Lw1b54:
	ds_read_b32 v28, v28
	s_andn2_b64 s[6:7], s[6:7], exec
	v_add_u32_e32 v30, 4, v29
	s_waitcnt lgkmcnt(0)
	v_cmp_gt_i32_e32 vcc, v28, v27
	s_and_b64 s[22:23], vcc, exec
	s_or_b64 s[6:7], s[6:7], s[22:23]

.LBB1_258:
	s_or_b64 exec, exec, s[10:11]
	s_and_saveexec_b64 s[10:11], s[6:7]
	v_mov_b32_e32 v28, v30

.Lw1b55:
	s_or_b64 exec, exec, s[10:11]
	v_cmp_lt_u32_e64 s[6:7], s19, v28
	v_cmp_gt_u32_e32 vcc, s20, v28
	s_and_saveexec_b64 s[10:11], vcc
	s_cbranch_execz .LBB1_262
	v_lshl_add_u32 v29, v28, 2, v25
	ds_read_b32 v29, v29
	s_andn2_b64 s[6:7], s[6:7], exec
	v_add_u32_e32 v30, 1, v28
	s_waitcnt lgkmcnt(0)
	v_cmp_gt_i32_e32 vcc, v29, v27
	s_and_b64 s[22:23], vcc, exec
	s_or_b64 s[6:7], s[6:7], s[22:23]

.LBB1_265:
	s_and_b64 vcc, exec, s[4:5]
	s_cbranch_vccz .LBB1_390
	v_cmp_ne_u32_e32 vcc, -1, v3
	s_and_saveexec_b64 s[4:5], vcc

.Lw1b56:
	s_cbranch_execz .LBB1_274
	v_lshrrev_b32_e32 v1, 15, v3
	v_and_b32_e32 v1, 0x1fffc, v1
	v_add_u32_e32 v1, 0x11000, v1
	ds_read_b32 v1, v1
	v_lshlrev_b32_e32 v2, 2, v15
	s_waitcnt lgkmcnt(0)
	v_lshl_add_u32 v1, v1, 2, v2
	ds_write_b32 v1, v3
	s_or_b64 exec, exec, s[4:5]
	v_cmp_ne_u32_e32 vcc, -1, v4
	s_and_saveexec_b64 s[4:5], vcc
	s_cbranch_execnz .LBB1_275

.LBB1_272:
	s_or_b64 exec, exec, s[4:5]
	v_cmp_ne_u32_e32 vcc, -1, v10

.Lw1b58:
	s_and_saveexec_b64 s[4:5], vcc
	s_cbranch_execz .LBB1_280
.LBB1_273:
	v_lshrrev_b32_e32 v1, 15, v10
	v_and_b32_e32 v1, 0x1fffc, v1
	v_add_u32_e32 v1, 0x11000, v1
	ds_read_b32 v1, v1
	v_lshlrev_b32_e32 v2, 2, v18
	s_waitcnt lgkmcnt(0)
	v_lshl_add_u32 v1, v1, 2, v2
	ds_write_b32 v1, v10
	s_or_b64 exec, exec, s[4:5]
	v_cmp_ne_u32_e32 vcc, -1, v13
	s_and_saveexec_b64 s[4:5], vcc
	s_cbranch_execnz .LBB1_281
	s_branch .LBB1_282

.LBB1_278:
.Lw1t60:
	s_cbranch_execz .Lw1c60
.Lw1b60:
	s_or_b64 exec, exec, s[4:5]
	v_cmp_ne_u32_e32 vcc, -1, v9
	s_and_saveexec_b64 s[4:5], vcc
	s_cbranch_execz .LBB1_272

.LBB1_281:
	v_lshrrev_b32_e32 v1, 15, v13
	v_and_b32_e32 v1, 0x1fffc, v1
	v_add_u32_e32 v1, 0x11000, v1
	ds_read_b32 v1, v1

.Lw1b61:
	v_lshlrev_b32_e32 v2, 2, v14
	s_waitcnt lgkmcnt(0)
	v_lshl_add_u32 v1, v1, 2, v2
	ds_write_b32 v1, v13
.LBB1_282:
	s_or_b64 exec, exec, s[4:5]
	v_mov_b32_e32 v1, 0x11ba0
	v_mov_b32_e32 v2, -1
	ds_write_b32 v1, v2
	s_cmp_lt_i32 s3, 1
	s_waitcnt lgkmcnt(0)
	s_barrier
	s_cbranch_scc1 .LBB1_332
	v_lshlrev_b32_e32 v1, 2, v0
	s_lshl_b32 s18, s3, 2
	s_mov_b32 s19, 0x1fffc
	s_mov_b32 s20, 0x10000
	v_mov_b32_e32 v7, 0x11ba0
	v_mov_b32_e32 v2, v0
	v_cmp_gt_i32_e64 s[10:11], s3, v2
	ds_read_b32 v17, v1
	v_mov_b32_e32 v16, v1

.Lw1b62:
	v_add_u32_e32 v2, 1024, v0
	v_cmp_gt_i32_e64 s[12:13], s3, v2
	ds_read_b32 v19, v1 offset:4096
	v_add_u32_e32 v18, 4096, v1
	v_add_u32_e32 v2, 2048, v0
	v_cmp_gt_i32_e64 s[14:15], s3, v2
	ds_read_b32 v21, v1 offset:8192
	v_add_u32_e32 v20, 8192, v1
	v_add_u32_e32 v2, 3072, v0
	v_cmp_gt_i32_e64 s[16:17], s3, v2
	ds_read_b32 v23, v1 offset:12288
	v_add_u32_e32 v22, 12288, v1
	s_waitcnt lgkmcnt(0)
	v_lshrrev_b32_e32 v2, 15, v17
	v_and_b32_e32 v2, s19, v2
	v_lshrrev_b32_e32 v3, 15, v19
	v_and_b32_e32 v3, s19, v3
	v_lshrrev_b32_e32 v4, 15, v21
	v_and_b32_e32 v4, s19, v4

.Lw1b63:
	v_lshrrev_b32_e32 v5, 15, v23
	v_and_b32_e32 v5, s19, v5
	v_cndmask_b32_e64 v2, 0, v2, s[10:11]
	v_add_u32_e32 v2, s20, v2
	v_cndmask_b32_e64 v3, 0, v3, s[12:13]
	v_add_u32_e32 v3, s20, v3
	v_cndmask_b32_e64 v4, 0, v4, s[14:15]
	v_add_u32_e32 v4, s20, v4
	v_cndmask_b32_e64 v5, 0, v5, s[16:17]
	v_add_u32_e32 v5, s20, v5
	ds_read_b32 v24, v2
	ds_read_b32 v28, v2 offset:4096
	ds_read_b32 v25, v3
	ds_read_b32 v29, v3 offset:4096
	ds_read_b32 v26, v4
	ds_read_b32 v30, v4 offset:4096
	ds_read_b32 v27, v5
	ds_read_b32 v31, v5 offset:4096
	s_waitcnt lgkmcnt(0)

.Lw1b64:
	v_cndmask_b32_e64 v2, 0, v24, s[10:11]
	v_lshlrev_b32_e32 v28, 2, v28
	v_mov_b32_e32 v8, v28
	v_mov_b32_e32 v24, 0
	v_cndmask_b32_e64 v3, 0, v25, s[12:13]
	v_lshlrev_b32_e32 v29, 2, v29
	v_mov_b32_e32 v10, v29
	v_mov_b32_e32 v25, 0
	v_cndmask_b32_e64 v4, 0, v26, s[14:15]
	v_lshlrev_b32_e32 v30, 2, v30
	v_mov_b32_e32 v12, v30
	v_mov_b32_e32 v26, 0
	v_cndmask_b32_e64 v5, 0, v27, s[16:17]
	v_lshlrev_b32_e32 v31, 2, v31
	v_mov_b32_e32 v14, v31
	v_mov_b32_e32 v27, 0
	v_max_u32_e32 v6, v2, v3
	v_max3_u32 v6, v6, v4, v5
	s_mov_b32 s21, 0
.Lrs0_loop:
	v_cmp_lt_u32_e32 vcc, s21, v6
	s_cbranch_vccz .Lrs0_done
	v_cmp_gt_u32_e64 s[22:23], s18, v8
	v_cmp_gt_u32_e64 s[24:25], s18, v10
	v_cmp_gt_u32_e64 s[26:27], s18, v12
.Lw1t65:
	s_cbranch_execz .Lw1c65
.Lw1b65:
	v_cmp_gt_u32_e64 s[28:29], s18, v14
	v_cndmask_b32_e64 v2, v7, v8, s[22:23]
	v_cndmask_b32_e64 v3, v7, v10, s[24:25]
	v_cndmask_b32_e64 v4, v7, v12, s[26:27]
	v_cndmask_b32_e64 v5, v7, v14, s[28:29]
	ds_read_b32 v9, v2
	ds_read_b32 v11, v3
	ds_read_b32 v13, v4
	ds_read_b32 v15, v5
	s_waitcnt lgkmcnt(3)
	v_cmp_lt_u64_e64 s[22:23], v[8:9], v[16:17]
	s_waitcnt lgkmcnt(2)
	v_cmp_lt_u64_e64 s[24:25], v[10:11], v[18:19]
	s_waitcnt lgkmcnt(1)
	v_cmp_lt_u64_e64 s[26:27], v[12:13], v[20:21]
	s_waitcnt lgkmcnt(0)
	v_cmp_lt_u64_e64 s[28:29], v[14:15], v[22:23]

.Lw1b66:
	v_addc_co_u32_e64 v24, s[4:5], 0, v24, s[22:23]
	v_addc_co_u32_e64 v25, s[4:5], 0, v25, s[24:25]
	v_addc_co_u32_e64 v26, s[4:5], 0, v26, s[26:27]
	v_addc_co_u32_e64 v27, s[4:5], 0, v27, s[28:29]
	v_add_u32_e32 v8, 4, v8
	v_add_u32_e32 v10, 4, v10
	v_add_u32_e32 v12, 4, v12
	v_add_u32_e32 v14, 4, v14
	s_add_i32 s21, s21, 1
	s_branch .Lrs0_loop
.Lrs0_done:
	v_and_b32_e32 v2, 0x1fffff, v17
	v_lshl_add_u32 v28, v24, 2, v28
	v_and_b32_e32 v3, 0x1fffff, v19
	v_lshl_add_u32 v29, v25, 2, v29
	v_and_b32_e32 v4, 0x1fffff, v21
	v_lshl_add_u32 v30, v26, 2, v30
	v_and_b32_e32 v5, 0x1fffff, v23
	v_lshl_add_u32 v31, v27, 2, v31
	s_mov_b64 exec, s[10:11]
.Lw1t67:
	s_cbranch_execz .Lw1c67
.Lw1b67:
	ds_write_b32 v28, v2 offset:32768
	s_mov_b64 exec, s[12:13]
	ds_write_b32 v29, v3 offset:32768
	s_mov_b64 exec, s[14:15]
	ds_write_b32 v30, v4 offset:32768
	s_mov_b64 exec, s[16:17]
	ds_write_b32 v31, v5 offset:32768
	s_mov_b64 exec, -1
.LBB1_332:
	s_cmpk_lt_i32 s3, 0x1001
	s_cbranch_scc1 .LBB1_382
	v_add_u32_e32 v2, 4096, v0
	v_cmp_gt_i32_e64 s[10:11], s3, v2
	ds_read_b32 v17, v1 offset:16384
	v_add_u32_e32 v16, 16384, v1
	v_add_u32_e32 v2, 5120, v0
	v_cmp_gt_i32_e64 s[12:13], s3, v2
	ds_read_b32 v19, v1 offset:20480
	v_add_u32_e32 v18, 20480, v1
	v_add_u32_e32 v2, 6144, v0

.Lw1b68:
	v_cmp_gt_i32_e64 s[14:15], s3, v2
	ds_read_b32 v21, v1 offset:24576
	v_add_u32_e32 v20, 24576, v1
	v_add_u32_e32 v2, 7168, v0
	v_cmp_gt_i32_e64 s[16:17], s3, v2
	ds_read_b32 v23, v1 offset:28672
	v_add_u32_e32 v22, 28672, v1
	s_waitcnt lgkmcnt(0)
	v_lshrrev_b32_e32 v2, 15, v17
	v_and_b32_e32 v2, s19, v2
	v_lshrrev_b32_e32 v3, 15, v19
	v_and_b32_e32 v3, s19, v3
	v_lshrrev_b32_e32 v4, 15, v21
	v_and_b32_e32 v4, s19, v4
	v_lshrrev_b32_e32 v5, 15, v23
	v_and_b32_e32 v5, s19, v5
	v_cndmask_b32_e64 v2, 0, v2, s[10:11]
	v_add_u32_e32 v2, s20, v2
	v_cndmask_b32_e64 v3, 0, v3, s[12:13]
	v_add_u32_e32 v3, s20, v3
	v_cndmask_b32_e64 v4, 0, v4, s[14:15]

.Lw1b69:
	v_add_u32_e32 v4, s20, v4
	v_cndmask_b32_e64 v5, 0, v5, s[16:17]
	v_add_u32_e32 v5, s20, v5
	ds_read_b32 v24, v2
	ds_read_b32 v28, v2 offset:4096
	ds_read_b32 v25, v3
	ds_read_b32 v29, v3 offset:4096
	ds_read_b32 v26, v4
	ds_read_b32 v30, v4 offset:4096
	ds_read_b32 v27, v5
	ds_read_b32 v31, v5 offset:4096
	s_waitcnt lgkmcnt(0)
	v_cndmask_b32_e64 v2, 0, v24, s[10:11]
	v_lshlrev_b32_e32 v28, 2, v28
	v_mov_b32_e32 v8, v28
	v_mov_b32_e32 v24, 0
	v_cndmask_b32_e64 v3, 0, v25, s[12:13]
	v_lshlrev_b32_e32 v29, 2, v29
	v_mov_b32_e32 v10, v29

.Lw1b70:
	v_mov_b32_e32 v25, 0
	v_cndmask_b32_e64 v4, 0, v26, s[14:15]
	v_lshlrev_b32_e32 v30, 2, v30
	v_mov_b32_e32 v12, v30
	v_mov_b32_e32 v26, 0
	v_cndmask_b32_e64 v5, 0, v27, s[16:17]
	v_lshlrev_b32_e32 v31, 2, v31
	v_mov_b32_e32 v14, v31
	v_mov_b32_e32 v27, 0
	v_max_u32_e32 v6, v2, v3
	v_max3_u32 v6, v6, v4, v5
	s_mov_b32 s21, 0

.Lw1b71:
	v_cndmask_b32_e64 v5, v7, v14, s[28:29]
	ds_read_b32 v9, v2
	ds_read_b32 v11, v3
	ds_read_b32 v13, v4
	ds_read_b32 v15, v5
	s_waitcnt lgkmcnt(3)
	v_cmp_lt_u64_e64 s[22:23], v[8:9], v[16:17]
	s_waitcnt lgkmcnt(2)
	v_cmp_lt_u64_e64 s[24:25], v[10:11], v[18:19]
	s_waitcnt lgkmcnt(1)
	v_cmp_lt_u64_e64 s[26:27], v[12:13], v[20:21]
	s_waitcnt lgkmcnt(0)
	v_cmp_lt_u64_e64 s[28:29], v[14:15], v[22:23]
	v_addc_co_u32_e64 v24, s[4:5], 0, v24, s[22:23]
	v_addc_co_u32_e64 v25, s[4:5], 0, v25, s[24:25]
	v_addc_co_u32_e64 v26, s[4:5], 0, v26, s[26:27]
	v_addc_co_u32_e64 v27, s[4:5], 0, v27, s[28:29]
	v_add_u32_e32 v8, 4, v8

.Lrs4_done:
	v_and_b32_e32 v2, 0x1fffff, v17
	v_lshl_add_u32 v28, v24, 2, v28
	v_and_b32_e32 v3, 0x1fffff, v19
	v_lshl_add_u32 v29, v25, 2, v29
	v_and_b32_e32 v4, 0x1fffff, v21
	v_lshl_add_u32 v30, v26, 2, v30
	v_and_b32_e32 v5, 0x1fffff, v23
	v_lshl_add_u32 v31, v27, 2, v31
	s_mov_b64 exec, s[10:11]
	ds_write_b32 v28, v2 offset:32768
	s_mov_b64 exec, s[12:13]
	ds_write_b32 v29, v3 offset:32768
	s_mov_b64 exec, s[14:15]
	ds_write_b32 v30, v4 offset:32768
	s_mov_b64 exec, s[16:17]

.Lw1b73:
	ds_write_b32 v31, v5 offset:32768
	s_mov_b64 exec, -1

.LBB1_387:
	s_or_b64 exec, exec, s[6:7]
	s_and_b32 s6, s14, -4
	s_add_i32 s6, s6, s4
	s_sub_i32 s3, s3, s6
	v_cmp_gt_i32_e32 vcc, s3, v0
	s_and_saveexec_b64 s[4:5], vcc

.Lw1b75:
	s_cbranch_execz .LBB1_389
	v_add_u32_e32 v2, s6, v0
	v_lshlrev_b32_e32 v1, 2, v2
	ds_read_b32 v1, v1 offset:32768
	v_ashrrev_i32_e32 v3, 31, v2
	v_lshl_add_u64 v[2:3], v[2:3], 2, s[8:9]
	s_waitcnt lgkmcnt(0)
	global_store_dword v[2:3], v1, off

.Lmy_cvt1:
	s_waitcnt lgkmcnt(0)
	s_load_dwordx4 s[20:23], s[0:1], 0x28
	s_sub_i32 s3, s2, 392
	s_cmp_ge_u32 s3, 193
	s_cbranch_scc1 .Lmy_cvt1_end
	v_and_b32_e32 v1, 0x3c0, v0
	v_and_b32_e32 v2, 63, v0
	v_lshlrev_b32_e32 v3, 5, v1
	v_lshl_or_b32 v3, v2, 4, v3
	v_and_b32_e32 v4, 1, v0
	v_lshrrev_b32_e32 v5, 1, v2
	v_lshl_or_b32 v5, v4, 5, v5

.Lw1b76:
	v_add_u32_e32 v5, v5, v1
	v_lshlrev_b32_e32 v5, 4, v5
	v_cmp_eq_u32_e32 vcc, 0, v4
	s_waitcnt lgkmcnt(0)
	s_add_i32 s8, s3, 792
	s_lshl_b32 s9, s8, 10
	s_sub_i32 s9, 0x1869c0, s9
	v_cmp_ge_i32_e64 s[24:25], s9, v1
	s_add_i32 s8, s3, 985
	s_lshl_b32 s9, s8, 10
	s_sub_i32 s9, 0x1869c0, s9
	v_cmp_ge_i32_e64 s[26:27], s9, v1
	s_add_i32 s8, s3, 1178
	s_lshl_b32 s9, s8, 10
	s_sub_i32 s9, 0x1869c0, s9
	v_cmp_ge_i32_e64 s[28:29], s9, v1
	s_add_i32 s8, s3, 1371
	s_lshl_b32 s9, s8, 10
	s_sub_i32 s9, 0x1869c0, s9
	v_cmp_ge_i32_e64 s[30:31], s9, v1

.Lw1b77:
	s_add_i32 s8, s3, 792
	s_lshl_b32 s9, s8, 15
	s_add_u32 s10, s20, s9
	s_addc_u32 s11, s21, 0
	s_mov_b64 exec, s[24:25]
	global_load_dwordx4 v[8:11], v3, s[10:11] nt
	global_load_dwordx4 v[12:15], v3, s[10:11] offset:1024 nt
	s_add_i32 s8, s3, 985
	s_lshl_b32 s9, s8, 15
	s_add_u32 s10, s20, s9
	s_addc_u32 s11, s21, 0
	s_mov_b64 exec, s[26:27]
	global_load_dwordx4 v[16:19], v3, s[10:11] nt
	global_load_dwordx4 v[20:23], v3, s[10:11] offset:1024 nt
	s_add_i32 s8, s3, 1178
	s_lshl_b32 s9, s8, 15
	s_add_u32 s10, s20, s9
	s_addc_u32 s11, s21, 0
	s_mov_b64 exec, s[28:29]
	global_load_dwordx4 v[24:27], v3, s[10:11] nt
	global_load_dwordx4 v[28:31], v3, s[10:11] offset:1024 nt

.Lw1b78:
	s_add_i32 s8, s3, 1371
	s_lshl_b32 s9, s8, 15
	s_add_u32 s10, s20, s9
	s_addc_u32 s11, s21, 0
	s_mov_b64 exec, s[30:31]
	global_load_dwordx4 v[32:35], v3, s[10:11] nt
	global_load_dwordx4 v[36:39], v3, s[10:11] offset:1024 nt
	s_waitcnt vmcnt(6)
	s_add_i32 s8, s3, 792
	s_lshl_b32 s9, s8, 14
	s_add_u32 s10, s22, s9
	s_addc_u32 s11, s23, 0
	s_mov_b64 exec, s[24:25]
	v_cvt_pk_f16_f32 v8, v8, v9
	v_cvt_pk_f16_f32 v9, v10, v11
	v_cvt_pk_f16_f32 v10, v12, v13
	v_cvt_pk_f16_f32 v11, v14, v15
	v_cndmask_b32_e32 v12, v8, v10, vcc
	v_cndmask_b32_e32 v13, v9, v11, vcc
	s_nop 1
	v_mov_b32_dpp v12, v12 quad_perm:[1,0,3,2] row_mask:0xf bank_mask:0xf bound_ctrl:1
	v_mov_b32_dpp v13, v13 quad_perm:[1,0,3,2] row_mask:0xf bank_mask:0xf bound_ctrl:1

.Lw1b79:
	v_cndmask_b32_e32 v8, v12, v8, vcc
	v_cndmask_b32_e32 v9, v13, v9, vcc
	v_cndmask_b32_e32 v10, v10, v12, vcc
	v_cndmask_b32_e32 v11, v11, v13, vcc
	global_store_dwordx4 v5, v[8:11], s[10:11] sc1
	s_waitcnt vmcnt(5)
	s_add_i32 s8, s3, 985
	s_lshl_b32 s9, s8, 14
	s_add_u32 s10, s22, s9
	s_addc_u32 s11, s23, 0
	s_mov_b64 exec, s[26:27]
	v_cvt_pk_f16_f32 v16, v16, v17
	v_cvt_pk_f16_f32 v17, v18, v19
	v_cvt_pk_f16_f32 v18, v20, v21
	v_cvt_pk_f16_f32 v19, v22, v23
	v_cndmask_b32_e32 v20, v16, v18, vcc
	v_cndmask_b32_e32 v21, v17, v19, vcc
	s_nop 1
	v_mov_b32_dpp v20, v20 quad_perm:[1,0,3,2] row_mask:0xf bank_mask:0xf bound_ctrl:1
	v_mov_b32_dpp v21, v21 quad_perm:[1,0,3,2] row_mask:0xf bank_mask:0xf bound_ctrl:1
	v_cndmask_b32_e32 v16, v20, v16, vcc
	v_cndmask_b32_e32 v17, v21, v17, vcc

.Lw1b80:
	v_cndmask_b32_e32 v18, v18, v20, vcc
	v_cndmask_b32_e32 v19, v19, v21, vcc
	global_store_dwordx4 v5, v[16:19], s[10:11] sc1
	s_waitcnt vmcnt(4)
	s_add_i32 s8, s3, 1178
	s_lshl_b32 s9, s8, 14
	s_add_u32 s10, s22, s9
	s_addc_u32 s11, s23, 0
	s_mov_b64 exec, s[28:29]
	v_cvt_pk_f16_f32 v24, v24, v25
	v_cvt_pk_f16_f32 v25, v26, v27
	v_cvt_pk_f16_f32 v26, v28, v29
	v_cvt_pk_f16_f32 v27, v30, v31
	v_cndmask_b32_e32 v28, v24, v26, vcc
	v_cndmask_b32_e32 v29, v25, v27, vcc
	s_nop 1
	v_mov_b32_dpp v28, v28 quad_perm:[1,0,3,2] row_mask:0xf bank_mask:0xf bound_ctrl:1
	v_mov_b32_dpp v29, v29 quad_perm:[1,0,3,2] row_mask:0xf bank_mask:0xf bound_ctrl:1
	v_cndmask_b32_e32 v24, v28, v24, vcc
	v_cndmask_b32_e32 v25, v29, v25, vcc
	v_cndmask_b32_e32 v26, v26, v28, vcc
	v_cndmask_b32_e32 v27, v27, v29, vcc
	global_store_dwordx4 v5, v[24:27], s[10:11] sc1

.Lw1b81:
	s_waitcnt vmcnt(3)
	s_add_i32 s8, s3, 1371
	s_lshl_b32 s9, s8, 14
	s_add_u32 s10, s22, s9
	s_addc_u32 s11, s23, 0
	s_mov_b64 exec, s[30:31]
	v_cvt_pk_f16_f32 v32, v32, v33
	v_cvt_pk_f16_f32 v33, v34, v35
	v_cvt_pk_f16_f32 v34, v36, v37
	v_cvt_pk_f16_f32 v35, v38, v39
	v_cndmask_b32_e32 v36, v32, v34, vcc
	v_cndmask_b32_e32 v37, v33, v35, vcc
	s_nop 1
	v_mov_b32_dpp v36, v36 quad_perm:[1,0,3,2] row_mask:0xf bank_mask:0xf bound_ctrl:1
	v_mov_b32_dpp v37, v37 quad_perm:[1,0,3,2] row_mask:0xf bank_mask:0xf bound_ctrl:1
	v_cndmask_b32_e32 v32, v36, v32, vcc
	v_cndmask_b32_e32 v33, v37, v33, vcc
	v_cndmask_b32_e32 v34, v34, v36, vcc
	v_cndmask_b32_e32 v35, v35, v37, vcc
	global_store_dwordx4 v5, v[32:35], s[10:11] sc1

	.amdhsa_kernel _Z8k_bucketPKiS0_PKjPiS3_PK15HIP_vector_typeIfLj4EEPS4_IjLj4EE
		.amdhsa_group_segment_fixed_size 72624
		.amdhsa_private_segment_fixed_size 0
		.amdhsa_kernarg_size 56
		.amdhsa_user_sgpr_count 2
		.amdhsa_user_sgpr_dispatch_ptr 0
		.amdhsa_user_sgpr_queue_ptr 0
		.amdhsa_user_sgpr_kernarg_segment_ptr 1
		.amdhsa_user_sgpr_dispatch_id 0
		.amdhsa_user_sgpr_kernarg_preload_length 0
		.amdhsa_user_sgpr_kernarg_preload_offset 0
		.amdhsa_user_sgpr_private_segment_size 0
		.amdhsa_uses_dynamic_stack 0
		.amdhsa_enable_private_segment 0
		.amdhsa_system_sgpr_workgroup_id_x 1
		.amdhsa_system_sgpr_workgroup_id_y 0
		.amdhsa_system_sgpr_workgroup_id_z 0
		.amdhsa_system_sgpr_workgroup_info 0
		.amdhsa_system_vgpr_workitem_id 0
		.amdhsa_next_free_vgpr 64
		.amdhsa_next_free_sgpr 74
		.amdhsa_accum_offset 64
		.amdhsa_reserve_vcc 1
		.amdhsa_float_round_mode_32 0
		.amdhsa_float_round_mode_16_64 0
		.amdhsa_float_denorm_mode_32 3
		.amdhsa_float_denorm_mode_16_64 3
		.amdhsa_dx10_clamp 1
		.amdhsa_ieee_mode 1
		.amdhsa_fp16_overflow 0
		.amdhsa_tg_split 0
		.amdhsa_exception_fp_ieee_invalid_op 0
		.amdhsa_exception_fp_denorm_src 0
		.amdhsa_exception_fp_ieee_div_zero 0
		.amdhsa_exception_fp_ieee_overflow 0
		.amdhsa_exception_fp_ieee_underflow 0
		.amdhsa_exception_fp_ieee_inexact 0
		.amdhsa_exception_int_div_zero 0
	.end_amdhsa_kernel

_Z10k_layer_a2ILi0ELi13EEvPKDF16_PKiS3_PK15HIP_vector_typeIjLj4EES7_PKfS9_S9_S9_S9_S9_PDF16_Pf:
	s_getpc_b64 s[58:59]

.Lw2b0:
	s_and_b32 s58, s58, 0xffffff00
	v_lshlrev_b32_e32 v36, 7, v0
	v_cmp_gt_u32_e32 vcc, 0x2c00, v36
	s_and_saveexec_b64 s[60:61], vcc
	global_load_dword v127, v36, s[58:59]
	s_or_b64 exec, exec, s[60:61]
	s_load_dwordx2 s[8:9], s[0:1], 0x18
	s_load_dwordx4 s[4:7], s[0:1], 0x28
	s_load_dwordx2 s[10:11], s[0:1], 0x38
	v_lshlrev_b32_e32 v2, 4, v0
	v_min_u32_e32 v1, 0x7f, v0
	v_lshlrev_b32_e32 v24, 2, v1
	v_readfirstlane_b32 s3, v0
	v_add_u32_e32 v28, 0x3400, v2
	v_add_u32_e32 v29, 0x6800, v2
	v_add_u32_e32 v30, 0x9c00, v2
	v_add_u32_e32 v31, 0xd00, v0
	v_min_u32_e32 v31, 0xfff, v31

.Lw2b1:
	v_lshlrev_b32_e32 v31, 4, v31
	s_waitcnt lgkmcnt(0)
	global_load_dwordx4 v[14:17], v2, s[8:9]
	global_load_dwordx4 v[6:9], v28, s[8:9]
	global_load_dwordx4 v[10:13], v29, s[8:9]
	global_load_dwordx4 v[18:21], v30, s[8:9]
	global_load_dwordx4 v[32:35], v31, s[8:9]
	global_load_dword v4, v24, s[4:5]
	global_load_dword v5, v24, s[4:5] offset:512
	global_load_dword v1, v24, s[6:7]
	global_load_dword v3, v24, s[10:11]
	s_load_dword s42, s[0:1], 0x0
	s_load_dword s43, s[0:1], 0x40
	v_lshrrev_b32_e32 v48, 6, v0
	s_nop 0
	v_readfirstlane_b32 s41, v48
	s_movk_i32 s40, 0x5aa5
	s_mov_b64 exec, 0
	s_cmpk_lt_u32 s41, 6
	s_cbranch_scc1 .Lw2s0d0_13
	s_cmpk_lt_u32 s41, 9
	s_cbranch_scc1 .Lw2s0d6_13
	s_cmpk_lt_u32 s41, 11
	s_cbranch_scc1 .Lw2s0d9_13
	s_cmpk_lt_u32 s41, 12
	s_cbranch_scc1 .Lw2s0d11_13
	s_branch .Lw2t12

.Lw2b2:
	s_waitcnt vmcnt(8)
	ds_write_b128 v2, v[14:17]
	s_waitcnt vmcnt(7)
	ds_write_b128 v2, v[6:9] offset:13312
	s_waitcnt vmcnt(6)
	ds_write_b128 v2, v[10:13] offset:26624
	s_waitcnt vmcnt(5)
	ds_write_b128 v2, v[18:21] offset:39936
	s_movk_i32 s4, 0x300
	v_cmp_gt_u32_e32 vcc, s4, v0
	s_waitcnt vmcnt(4)
	s_and_saveexec_b64 s[4:5], vcc
	ds_write_b128 v2, v[32:35] offset:53248
	s_or_b64 exec, exec, s[4:5]
	s_movk_i32 s4, 0x80
	v_cmp_gt_u32_e32 vcc, s4, v0
	s_and_saveexec_b64 s[4:5], vcc
	s_cbranch_execz .LBB2_4
	s_waitcnt vmcnt(2)
	v_add_f32_e32 v2, v4, v5
	v_mov_b32_e32 v4, 0x1dd00

.LBB2_6:
	s_or_b64 exec, exec, s[4:5]
	s_waitcnt vmcnt(1)
	v_bfe_u32 v1, v0, 4, 2
	v_bfe_u32 v2, v0, 2, 2
.Lw2t4:
	s_cbranch_execz .Lw2c4
.Lw2b4:
	v_cmp_eq_u32_e32 vcc, v1, v2
	v_and_b32_e32 v2, 3, v0
	v_cmp_eq_u32_e64 s[4:5], 0, v2
	s_waitcnt vmcnt(0)
	v_mov_b32_e32 v3, 0x3c00
	s_and_b64 s[4:5], vcc, s[4:5]
	v_cndmask_b32_e64 v4, 0, v3, s[4:5]
	v_cmp_eq_u32_e64 s[4:5], 1, v2
	s_and_b64 s[4:5], vcc, s[4:5]
	s_lshr_b32 s12, s3, 6
	v_cndmask_b32_e64 v5, 0, v3, s[4:5]
	v_cmp_eq_u32_e64 s[4:5], 2, v2
	s_and_b64 s[4:5], vcc, s[4:5]
	v_and_b32_e32 v77, 63, v0
	v_cndmask_b32_e64 v6, 0, v3, s[4:5]
	v_cmp_eq_u32_e64 s[4:5], 3, v2
	s_and_b64 vcc, vcc, s[4:5]
	v_cndmask_b32_e32 v2, 0, v3, vcc
	v_pack_b32_f16 v73, v6, v2
	v_lshlrev_b32_e32 v2, 2, v0
	s_waitcnt lgkmcnt(0)

.Lw2b5:
	s_barrier
	v_and_b32_e32 v82, 15, v0
	v_pack_b32_f16 v72, v4, v5
	s_load_dword s3, s[0:1], 0x68
	v_and_b32_e32 v84, 0xc0, v2
	s_mul_i32 s0, s12, 0x1100
	v_and_b32_e32 v2, 48, v0
	v_bfe_u32 v5, v0, 2, 4
	v_lshlrev_b32_e32 v0, 6, v0
	s_add_i32 s4, s0, 0x10000
	v_mul_u32_u24_e32 v5, 0x110, v5
	v_and_b32_e32 v0, 0xc0, v0
	v_mov_b32_e32 v3, 0
	s_movk_i32 s20, 0x110
	v_add3_u32 v85, s4, v5, v0
	v_mov_b32_e32 v0, s4
	v_lshlrev_b32_e32 v4, 7, v1
	v_mad_u32_u24 v5, v82, s20, v0
	v_lshlrev_b32_e32 v86, 5, v1
	v_lshlrev_b32_e32 v0, 6, v1
	v_mov_b32_e32 v1, v3

.Lw2b6:
	v_lshlrev_b32_e32 v83, 4, v82
	v_lshl_add_u64 v[78:79], s[14:15], 0, v[0:1]
	v_mbcnt_lo_u32_b32 v0, -1, 0
	v_cmp_eq_u32_e64 s[0:1], 0, v77
	v_lshl_add_u64 v[74:75], s[10:11], 0, v[2:3]
	v_or_b32_e32 v76, s4, v83
	v_or_b32_e32 v87, 28, v84
	v_or_b32_e32 v88, 32, v84
	v_or_b32_e32 v89, 36, v84
	v_or_b32_e32 v90, 40, v84
	v_or_b32_e32 v91, 44, v84
	v_or_b32_e32 v92, 48, v84
	v_or_b32_e32 v93, 52, v84
	v_or_b32_e32 v94, 56, v84
	v_or_b32_e32 v95, 60, v84
	v_mov_b32_e32 v96, 0x1e900
	v_add_u32_e32 v97, 0x1dd00, v4
	s_mov_b32 s21, 0x1ffff00
	v_add_u32_e32 v98, v5, v2
	v_lshrrev_b32_e32 v125, 1, v86
	v_lshrrev_b32_e32 v126, 5, v86
	v_add3_u32 v125, v98, v86, v125
	v_mad_u32_u24 v126, v126, s20, v76

.Lw2b7:
	v_mov_b32_e32 v99, 0x3727c5ac
	s_mov_b32 s22, 0x800000
	v_mov_b32_e32 v100, 0xc0135761
	v_mbcnt_hi_u32_b32 v101, -1, v0
	v_mov_b32_e32 v102, 0x1dd00
	s_mov_b32 s47, s41

.Lw2b8:
	v_pk_add_f32 v[32:33], v[32:33], v[34:35]
	v_mov_b32_e32 v34, v21
	v_mov_b32_e32 v35, v22
	v_mov_b32_e32 v37, v23
	v_pk_add_f32 v[34:35], v[34:35], v[36:37]
	v_add_f32_e32 v32, 0, v32
	v_pk_add_f32 v[34:35], v[34:35], v[34:35] op_sel:[0,1] op_sel_hi:[1,0]
	v_add_f32_e32 v32, v32, v33
	v_add_f32_e32 v36, v16, v17
	v_add_f32_e32 v38, v18, v19
	v_mov_b32_e32 v33, v12
	v_mov_b32_e32 v35, v13
	v_mov_b32_e32 v37, v14
	v_mov_b32_e32 v39, v15
	v_pk_add_f32 v[32:33], v[32:33], v[34:35]
	v_pk_add_f32 v[34:35], v[36:37], v[38:39]
	v_mov_b32_e32 v36, v8
	v_pk_add_f32 v[32:33], v[32:33], v[34:35]
	v_mov_b32_e32 v34, v9
	v_mov_b32_e32 v35, v10
	v_mov_b32_e32 v37, v11
	v_pk_add_f32 v[34:35], v[34:35], v[36:37]
	v_pk_add_f32 v[32:33], v[32:33], v[32:33] op_sel:[0,1] op_sel_hi:[1,0]

.Lw2b9:
	v_pk_add_f32 v[34:35], v[34:35], v[34:35] op_sel:[0,1] op_sel_hi:[1,0]
	v_add_f32_e32 v36, v4, v5
	v_add_f32_e32 v38, v6, v7
	v_mov_b32_e32 v33, v0
	v_mov_b32_e32 v35, v1
	v_mov_b32_e32 v37, v2
	v_mov_b32_e32 v39, v3
	v_pk_add_f32 v[32:33], v[32:33], v[34:35]
	v_pk_add_f32 v[34:35], v[36:37], v[38:39]
	s_nop 0
	v_pk_add_f32 v[32:33], v[32:33], v[34:35]
	v_and_b32_e32 v34, 64, v101
	v_add_f32_e32 v32, v32, v33
	v_xor_b32_e32 v33, 16, v101
	v_add_u32_e32 v34, 64, v34
	v_cmp_lt_i32_e32 vcc, v33, v34
	s_nop 1
	v_cndmask_b32_e32 v33, v101, v33, vcc
	v_lshlrev_b32_e32 v42, 2, v33
	ds_bpermute_b32 v33, v42, v32
	s_waitcnt lgkmcnt(0)
	v_add_f32_e32 v32, v32, v33
	v_xor_b32_e32 v33, 32, v101
	v_cmp_lt_i32_e32 vcc, v33, v34
	s_nop 1
	v_cndmask_b32_e32 v33, v101, v33, vcc

.Lw2b10:
	v_lshlrev_b32_e32 v43, 2, v33
	ds_bpermute_b32 v33, v43, v32
	s_waitcnt lgkmcnt(0)
	v_add_f32_e32 v44, v32, v33
	v_fmamk_f32 v29, v44, 0xbc000000, v29
	v_fmamk_f32 v25, v44, 0xbc000000, v25
	v_fmamk_f32 v41, v44, 0xbc000000, v31
	v_fmamk_f32 v40, v44, 0xbc000000, v30
	v_fmac_f32_e32 v28, 0xbc000000, v44
	v_fmamk_f32 v39, v44, 0xbc000000, v27
	v_fmac_f32_e32 v24, 0xbc000000, v44
	v_mov_b32_e32 v30, v29
	v_mov_b32_e32 v31, v25
	v_fmamk_f32 v38, v44, 0xbc000000, v26
	v_mov_b32_e32 v26, v28
	v_mov_b32_e32 v27, v24
	v_pk_mul_f32 v[30:31], v[30:31], v[30:31]
	v_mov_b32_e32 v32, v41
	v_mov_b32_e32 v33, v39
	v_pk_fma_f32 v[26:27], v[26:27], v[26:27], v[30:31]

.Lw2b11:
	v_mov_b32_e32 v30, v40
	v_mov_b32_e32 v31, v38
	v_pk_mul_f32 v[32:33], v[32:33], v[32:33]
	v_fmamk_f32 v37, v44, 0xbc000000, v21
	v_pk_fma_f32 v[30:31], v[30:31], v[30:31], v[32:33]
	v_fmamk_f32 v36, v44, 0xbc000000, v20
	v_fmamk_f32 v23, v44, 0xbc000000, v23
	v_fmac_f32_e32 v22, 0xbc000000, v44
	v_pk_add_f32 v[26:27], v[26:27], v[30:31]
	v_pk_mul_f32 v[20:21], v[22:23], v[22:23]
	v_pk_mul_f32 v[30:31], v[36:37], v[36:37]
	v_fmac_f32_e32 v12, 0xbc000000, v44
	v_pk_mov_b32 v[32:33], v[30:31], v[20:21] op_sel:[1,0]
	v_mov_b32_e32 v31, v21
	v_pk_add_f32 v[20:21], v[32:33], v[30:31]
	v_fmamk_f32 v34, v44, 0xbc000000, v18
	v_fmamk_f32 v31, v44, 0xbc000000, v15

.Lw2b12:
	v_fmamk_f32 v30, v44, 0xbc000000, v14
	v_fmamk_f32 v13, v44, 0xbc000000, v13
	v_mul_f32_e32 v18, v12, v12
	v_pk_add_f32 v[14:15], v[26:27], v[26:27] op_sel:[0,1] op_sel_hi:[1,0]
	v_fmamk_f32 v35, v44, 0xbc000000, v19
	v_mul_f32_e32 v32, v13, v13
	v_mov_b32_e32 v15, v18
	v_pk_add_f32 v[18:19], v[20:21], v[20:21] op_sel:[0,1] op_sel_hi:[1,0]
	v_fmamk_f32 v17, v44, 0xbc000000, v17
	v_mov_b32_e32 v19, v32
	v_fmac_f32_e32 v16, 0xbc000000, v44
	v_pk_add_f32 v[14:15], v[14:15], v[18:19]
	v_mul_f32_e32 v18, v17, v17
	v_mul_f32_e32 v20, v35, v35
	v_mul_f32_e32 v33, v30, v30
	v_mul_f32_e32 v45, v31, v31
	v_pk_fma_f32 v[18:19], v[16:17], v[16:17], v[18:19] op_sel_hi:[1,1,0]
	v_pk_fma_f32 v[20:21], v[34:35], v[34:35], v[20:21] op_sel_hi:[1,1,0]
	v_mov_b32_e32 v19, v33
	v_mov_b32_e32 v21, v45
	v_pk_add_f32 v[18:19], v[18:19], v[20:21]

.Lw2b13:
	v_fmamk_f32 v33, v44, 0xbc000000, v9
	v_fmamk_f32 v32, v44, 0xbc000000, v8
	v_fmamk_f32 v11, v44, 0xbc000000, v11
	v_fmac_f32_e32 v10, 0xbc000000, v44
	v_pk_add_f32 v[14:15], v[14:15], v[18:19]
	v_pk_mul_f32 v[8:9], v[10:11], v[10:11]
	v_pk_mul_f32 v[18:19], v[32:33], v[32:33]
	v_fmamk_f32 v1, v44, 0xbc000000, v1
	v_pk_mov_b32 v[20:21], v[18:19], v[8:9] op_sel:[1,0]
	v_mov_b32_e32 v19, v9
	v_pk_add_f32 v[8:9], v[20:21], v[18:19]
	v_fmac_f32_e32 v0, 0xbc000000, v44
	v_fmamk_f32 v19, v44, 0xbc000000, v7
	v_fmamk_f32 v18, v44, 0xbc000000, v6
	v_mul_f32_e32 v20, v0, v0
	v_mul_f32_e32 v21, v1, v1
	v_pk_add_f32 v[6:7], v[14:15], v[14:15] op_sel:[0,1] op_sel_hi:[1,0]

.Lw2b14:
	v_pk_add_f32 v[8:9], v[8:9], v[8:9] op_sel:[0,1] op_sel_hi:[1,0]
	v_fmamk_f32 v5, v44, 0xbc000000, v5
	v_mov_b32_e32 v7, v20
	v_mov_b32_e32 v9, v21
	v_fmac_f32_e32 v4, 0xbc000000, v44
	v_fmamk_f32 v3, v44, 0xbc000000, v3
	v_fmamk_f32 v2, v44, 0xbc000000, v2
	v_pk_add_f32 v[6:7], v[6:7], v[8:9]
	v_mul_f32_e32 v8, v5, v5
	v_mul_f32_e32 v14, v19, v19
	v_mul_f32_e32 v26, v2, v2
	v_mul_f32_e32 v27, v3, v3
	v_pk_fma_f32 v[8:9], v[4:5], v[4:5], v[8:9] op_sel_hi:[1,1,0]
	v_pk_fma_f32 v[14:15], v[18:19], v[18:19], v[14:15] op_sel_hi:[1,1,0]
	v_mov_b32_e32 v9, v26
	v_mov_b32_e32 v15, v27
	v_pk_add_f32 v[8:9], v[8:9], v[14:15]
	s_nop 0
	v_pk_add_f32 v[6:7], v[6:7], v[8:9]
	s_nop 0

.Lw2b15:
	v_add_f32_e32 v6, v6, v7
	ds_bpermute_b32 v7, v42, v6
	s_waitcnt lgkmcnt(0)
	v_add_f32_e32 v6, v6, v7
	ds_bpermute_b32 v7, v43, v6
	s_waitcnt lgkmcnt(0)
	v_add_f32_e32 v6, v6, v7
	v_fmamk_f32 v6, v6, 0x3c000000, v99
	v_mul_f32_e32 v7, 0x4b800000, v6
	v_cmp_gt_f32_e32 vcc, s22, v6
	s_nop 1
	v_cndmask_b32_e32 v6, v6, v7, vcc
	v_rsq_f32_e32 v14, v6
	ds_read_b128 v[6:9], v97 offset:512
	ds_read_b128 v[42:45], v97 offset:528
	ds_read_b128 v[46:49], v97 offset:1024
	ds_read_b128 v[50:53], v97 offset:1040
	v_mul_f32_e32 v15, 0x45800000, v14
	v_cndmask_b32_e32 v20, v14, v15, vcc
	v_pk_mul_f32 v[26:27], v[20:21], v[28:29] op_sel_hi:[0,1]
	s_waitcnt lgkmcnt(1)

.Lw2b16:
	v_pk_fma_f32 v[6:7], v[6:7], v[26:27], v[46:47]
	v_or_b32_e32 v14, s4, v82
	v_pk_mul_f32 v[26:27], v[6:7], v[6:7]
	v_ashrrev_i32_e32 v15, 31, v14
	v_fmamk_f32 v21, v26, 0xbdd2d3e8, v100
	v_mul_f32_e32 v21, v6, v21
	v_fmamk_f32 v26, v27, 0xbdd2d3e8, v100
	v_exp_f32_e32 v21, v21
	v_mul_f32_e32 v26, v7, v26
	v_exp_f32_e32 v26, v26
	v_lshlrev_b64 v[14:15], 8, v[14:15]
	v_add_f32_e32 v21, 1.0, v21
	v_rcp_f32_e32 v28, v21
	v_add_f32_e32 v21, 1.0, v26
	v_pk_mul_f32 v[26:27], v[20:21], v[40:41] op_sel_hi:[0,1]
	v_pk_fma_f32 v[8:9], v[8:9], v[26:27], v[48:49]
	v_rcp_f32_e32 v29, v21
	v_pk_mul_f32 v[40:41], v[8:9], v[8:9]
	v_mad_u32_u24 v104, v86, 6, v83
	s_cmp_ge_u32 s4, 0xd000
	s_cselect_b32 s47, 1, 0

.Lw2b17:
	s_lshl_b32 s12, s4, 8
	v_mov_b32_e32 v105, 0
	v_add_u32_e32 v104, s12, v104
	s_nop 0
	v_lshl_add_u64 v[104:105], v[78:79], 0, v[104:105]
	v_fmamk_f32 v21, v40, 0xbdd2d3e8, v100
	v_mul_f32_e32 v21, v8, v21
	v_exp_f32_e32 v21, v21
	v_fmamk_f32 v14, v41, 0xbdd2d3e8, v100
	v_pk_mul_f32 v[6:7], v[6:7], v[28:29]
	v_mul_f32_e32 v14, v9, v14
	v_cvt_pk_f16_f32 v6, v6, v7
	v_add_f32_e32 v7, 1.0, v21
	v_exp_f32_e32 v21, v14
	v_rcp_f32_e32 v28, v7
	v_pk_mul_f32 v[14:15], v[20:21], v[24:25] op_sel_hi:[0,1]
	s_waitcnt lgkmcnt(0)
	v_pk_fma_f32 v[14:15], v[42:43], v[14:15], v[50:51]
	v_add_f32_e32 v7, 1.0, v21
	v_pk_mul_f32 v[24:25], v[14:15], v[14:15]
	v_rcp_f32_e32 v29, v7
	v_fmamk_f32 v24, v24, 0xbdd2d3e8, v100

.Lw2b18:
	v_mul_f32_e32 v24, v14, v24
	v_exp_f32_e32 v24, v24
	v_fmamk_f32 v21, v25, 0xbdd2d3e8, v100
	v_mul_f32_e32 v21, v15, v21
	v_pk_mul_f32 v[8:9], v[8:9], v[28:29]
	v_add_f32_e32 v7, 1.0, v24
	v_pk_mul_f32 v[24:25], v[20:21], v[38:39] op_sel_hi:[0,1]
	v_pk_fma_f32 v[24:25], v[44:45], v[24:25], v[52:53]
	v_exp_f32_e32 v21, v21
	v_pk_mul_f32 v[38:39], v[24:25], v[24:25]
	v_rcp_f32_e32 v40, v7
	v_fmamk_f32 v38, v38, 0xbdd2d3e8, v100
	v_fmamk_f32 v39, v39, 0xbdd2d3e8, v100
	v_mul_f32_e32 v38, v24, v38
	v_mul_f32_e32 v39, v25, v39
	v_exp_f32_e32 v38, v38
	v_exp_f32_e32 v39, v39
	v_add_f32_e32 v7, 1.0, v21
	v_mov_b32_e32 v21, v86
	v_add_f32_e32 v38, 1.0, v38
	v_add_f32_e32 v39, 1.0, v39
	v_rcp_f32_e32 v38, v38
	v_rcp_f32_e32 v39, v39
	v_rcp_f32_e32 v41, v7

.Lw2b19:
	v_pk_mul_f32 v[24:25], v[24:25], v[38:39]
	s_nop 0
	s_nop 0
	v_lshl_add_u32 v7, v21, 2, v102
	v_add_u32_e32 v54, 0x420, v7
	v_add_u32_e32 v48, 0x428, v7
	v_add_u32_e32 v52, 0x430, v7
	ds_read2_b32 v[38:39], v7 offset0:138 offset1:139
	ds_read2_b32 v[42:43], v7 offset0:142 offset1:143
	ds_read2_b32 v[44:45], v7 offset0:140 offset1:141
	ds_read2_b32 v[46:47], v7 offset0:136 offset1:137
	v_add_u32_e32 v7, 0x438, v7
	ds_read2_b32 v[48:49], v48 offset1:1
	ds_read2_b32 v[50:51], v7 offset1:1
	ds_read2_b32 v[52:53], v52 offset1:1
	ds_read2_b32 v[54:55], v54 offset1:1
	v_cvt_pk_f16_f32 v7, v8, v9

.Lw2b20:
	v_pk_mul_f32 v[8:9], v[14:15], v[40:41]
	s_nop 0
	v_cvt_pk_f16_f32 v8, v8, v9
	v_pk_mul_f32 v[14:15], v[20:21], v[36:37] op_sel_hi:[0,1]
	s_waitcnt lgkmcnt(0)
	v_pk_fma_f32 v[14:15], v[46:47], v[14:15], v[54:55]
	v_pk_mul_f32 v[22:23], v[20:21], v[22:23] op_sel_hi:[0,1]
	v_pk_mul_f32 v[28:29], v[14:15], v[14:15]
	v_pk_fma_f32 v[22:23], v[38:39], v[22:23], v[48:49]
	v_fmamk_f32 v9, v28, 0xbdd2d3e8, v100
	v_mul_f32_e32 v9, v14, v9
	v_fmamk_f32 v28, v29, 0xbdd2d3e8, v100
	v_exp_f32_e32 v9, v9
	v_mul_f32_e32 v28, v15, v28
	v_exp_f32_e32 v29, v28
	v_pk_mul_f32 v[36:37], v[22:23], v[22:23]
	v_add_f32_e32 v9, 1.0, v9
	v_rcp_f32_e32 v28, v9
	v_add_f32_e32 v9, 1.0, v29
	v_rcp_f32_e32 v29, v9

.Lw2b21:
	v_fmamk_f32 v9, v36, 0xbdd2d3e8, v100
	v_mul_f32_e32 v9, v22, v9
	v_exp_f32_e32 v36, v9
	v_cvt_pk_f16_f32 v9, v24, v25
	v_fmamk_f32 v24, v37, 0xbdd2d3e8, v100
	v_pk_mul_f32 v[16:17], v[20:21], v[16:17] op_sel_hi:[0,1]
	v_mul_f32_e32 v24, v23, v24
	v_pk_fma_f32 v[16:17], v[44:45], v[16:17], v[52:53]
	v_pk_mul_f32 v[14:15], v[14:15], v[28:29]
	v_exp_f32_e32 v29, v24
	v_pk_mul_f32 v[24:25], v[16:17], v[16:17]
	v_cvt_pk_f16_f32 v14, v14, v15
	v_fmamk_f32 v24, v24, 0xbdd2d3e8, v100
	v_mul_f32_e32 v24, v16, v24
	v_exp_f32_e32 v24, v24
	v_add_f32_e32 v15, 1.0, v36
	v_rcp_f32_e32 v28, v15
	v_add_f32_e32 v15, 1.0, v29
	v_rcp_f32_e32 v29, v15
	v_add_f32_e32 v15, 1.0, v24
	v_fmamk_f32 v24, v25, 0xbdd2d3e8, v100

.Lw2b22:
	v_mul_f32_e32 v36, v17, v24
	v_pk_mul_f32 v[24:25], v[20:21], v[34:35] op_sel_hi:[0,1]
	v_pk_fma_f32 v[24:25], v[42:43], v[24:25], v[50:51]
	v_exp_f32_e32 v37, v36
	v_pk_mul_f32 v[34:35], v[24:25], v[24:25]
	v_rcp_f32_e32 v36, v15
	v_fmamk_f32 v34, v34, 0xbdd2d3e8, v100
	v_fmamk_f32 v35, v35, 0xbdd2d3e8, v100
	v_mul_f32_e32 v34, v24, v34
	v_mul_f32_e32 v35, v25, v35
	v_exp_f32_e32 v34, v34
	v_exp_f32_e32 v35, v35
	v_add_f32_e32 v15, 1.0, v37
	v_rcp_f32_e32 v37, v15
	v_add_f32_e32 v34, 1.0, v34
	v_add_f32_e32 v35, 1.0, v35
	v_rcp_f32_e32 v34, v34
	v_rcp_f32_e32 v35, v35
	v_pk_mul_f32 v[22:23], v[22:23], v[28:29]
	v_pk_mul_f32 v[16:17], v[16:17], v[36:37]
	v_pk_mul_f32 v[24:25], v[24:25], v[34:35]
	s_nop 0
	v_cvt_pk_f16_f32 v16, v16, v17

.Lw2b23:
	v_lshl_add_u32 v15, v21, 2, v102
	v_add_u32_e32 v50, 0x440, v15
	v_add_u32_e32 v44, 0x448, v15
	v_add_u32_e32 v48, 0x450, v15
	ds_read2_b32 v[34:35], v15 offset0:146 offset1:147
	ds_read2_b32 v[38:39], v15 offset0:150 offset1:151
	ds_read2_b32 v[40:41], v15 offset0:148 offset1:149
	ds_read2_b32 v[42:43], v15 offset0:144 offset1:145
	v_add_u32_e32 v15, 0x458, v15
	ds_read2_b32 v[44:45], v44 offset1:1
	ds_read2_b32 v[46:47], v15 offset1:1
	ds_read2_b32 v[48:49], v48 offset1:1
	ds_read2_b32 v[50:51], v50 offset1:1
	v_cvt_pk_f16_f32 v15, v22, v23
	v_pk_mul_f32 v[12:13], v[20:21], v[12:13] op_sel_hi:[0,1]

.Lw2b24:
	s_waitcnt lgkmcnt(0)
	v_pk_fma_f32 v[12:13], v[42:43], v[12:13], v[50:51]
	v_pk_mul_f32 v[28:29], v[20:21], v[30:31] op_sel_hi:[0,1]
	v_pk_mul_f32 v[22:23], v[12:13], v[12:13]
	v_pk_fma_f32 v[28:29], v[34:35], v[28:29], v[44:45]
	v_fmamk_f32 v17, v22, 0xbdd2d3e8, v100
	v_mul_f32_e32 v17, v12, v17
	v_fmamk_f32 v22, v23, 0xbdd2d3e8, v100
	v_exp_f32_e32 v17, v17
	v_mul_f32_e32 v22, v13, v22
	v_exp_f32_e32 v23, v22
	v_pk_mul_f32 v[30:31], v[28:29], v[28:29]
	v_add_f32_e32 v17, 1.0, v17
	v_rcp_f32_e32 v22, v17
	v_add_f32_e32 v17, 1.0, v23
	v_rcp_f32_e32 v23, v17
	v_fmamk_f32 v17, v30, 0xbdd2d3e8, v100
	v_mul_f32_e32 v17, v28, v17
	v_exp_f32_e32 v30, v17
	v_pk_mul_f32 v[12:13], v[12:13], v[22:23]
	v_cvt_pk_f16_f32 v17, v24, v25

.Lw2b25:
	v_cvt_pk_f16_f32 v22, v12, v13
	v_fmamk_f32 v12, v31, 0xbdd2d3e8, v100
	v_mul_f32_e32 v12, v29, v12
	v_exp_f32_e32 v31, v12
	v_pk_mul_f32 v[12:13], v[20:21], v[32:33] op_sel_hi:[0,1]
	v_pk_fma_f32 v[12:13], v[40:41], v[12:13], v[48:49]
	v_add_f32_e32 v23, 1.0, v30
	v_pk_mul_f32 v[24:25], v[12:13], v[12:13]
	v_rcp_f32_e32 v30, v23
	v_fmamk_f32 v24, v24, 0xbdd2d3e8, v100
	v_mul_f32_e32 v24, v12, v24
	v_exp_f32_e32 v24, v24
	v_add_f32_e32 v23, 1.0, v31
	v_pk_mul_f32 v[10:11], v[20:21], v[10:11] op_sel_hi:[0,1]
	v_rcp_f32_e32 v31, v23
	v_add_f32_e32 v23, 1.0, v24
	v_fmamk_f32 v24, v25, 0xbdd2d3e8, v100
	v_pk_fma_f32 v[10:11], v[38:39], v[10:11], v[46:47]
	v_mul_f32_e32 v32, v13, v24
	v_pk_mul_f32 v[24:25], v[10:11], v[10:11]
	v_exp_f32_e32 v33, v32

.Lw2b26:
	v_fmamk_f32 v24, v24, 0xbdd2d3e8, v100
	v_fmamk_f32 v25, v25, 0xbdd2d3e8, v100
	v_mul_f32_e32 v24, v10, v24
	v_mul_f32_e32 v25, v11, v25
	v_exp_f32_e32 v24, v24
	v_exp_f32_e32 v25, v25
	v_rcp_f32_e32 v32, v23
	v_add_f32_e32 v23, 1.0, v33
	v_add_f32_e32 v24, 1.0, v24
	v_add_f32_e32 v25, 1.0, v25
	v_rcp_f32_e32 v24, v24
	v_rcp_f32_e32 v25, v25
	v_rcp_f32_e32 v33, v23
	v_pk_mul_f32 v[10:11], v[10:11], v[24:25]
	s_nop 0
	v_pk_mul_f32 v[12:13], v[12:13], v[32:33]
	v_lshl_add_u32 v21, v21, 2, v102
	v_add_u32_e32 v24, 0x468, v21
	ds_read2_b32 v[34:35], v21 offset0:154 offset1:155
	ds_read2_b32 v[36:37], v21 offset0:158 offset1:159
	ds_read2_b32 v[38:39], v21 offset0:156 offset1:157
	ds_read2_b32 v[40:41], v21 offset0:152 offset1:153

.Lw2b27:
	v_add_u32_e32 v23, 0x460, v21
	v_add_u32_e32 v25, 0x470, v21
	v_add_u32_e32 v21, 0x478, v21
	ds_read2_b32 v[42:43], v24 offset1:1
	ds_read2_b32 v[44:45], v21 offset1:1
	ds_read2_b32 v[46:47], v25 offset1:1
	ds_read2_b32 v[48:49], v23 offset1:1
	v_pk_mul_f32 v[24:25], v[28:29], v[30:31]
	s_nop 0
	v_cvt_pk_f16_f32 v23, v24, v25
	v_cvt_pk_f16_f32 v24, v12, v13
	v_pk_mul_f32 v[4:5], v[20:21], v[4:5] op_sel_hi:[0,1]
	s_waitcnt lgkmcnt(0)
	v_pk_fma_f32 v[4:5], v[40:41], v[4:5], v[48:49]
	ds_write_b128 v125, v[6:9]
	v_pk_mul_f32 v[12:13], v[4:5], v[4:5]

.Lw2b28:
	v_pk_mul_f32 v[0:1], v[20:21], v[0:1] op_sel_hi:[0,1]
	v_fmamk_f32 v12, v12, 0xbdd2d3e8, v100
	v_fmamk_f32 v13, v13, 0xbdd2d3e8, v100
	v_mul_f32_e32 v12, v4, v12
	v_mul_f32_e32 v13, v5, v13
	v_exp_f32_e32 v12, v12
	v_exp_f32_e32 v13, v13
	v_pk_fma_f32 v[0:1], v[38:39], v[0:1], v[46:47]
	v_cvt_pk_f16_f32 v25, v10, v11
	v_add_f32_e32 v6, 1.0, v12
	v_add_f32_e32 v7, 1.0, v13
	v_rcp_f32_e32 v6, v6
	v_rcp_f32_e32 v7, v7
	v_pk_mul_f32 v[10:11], v[0:1], v[0:1]
	v_pk_mul_f32 v[2:3], v[20:21], v[2:3] op_sel_hi:[0,1]
	v_pk_fma_f32 v[2:3], v[36:37], v[2:3], v[44:45]
	v_pk_mul_f32 v[4:5], v[4:5], v[6:7]
	v_pk_mul_f32 v[6:7], v[20:21], v[18:19] op_sel_hi:[0,1]
	v_pk_fma_f32 v[6:7], v[34:35], v[6:7], v[42:43]
	v_cvt_pk_f16_f32 v4, v4, v5

.Lw2b29:
	v_pk_mul_f32 v[8:9], v[6:7], v[6:7]
	s_mov_b64 s[4:5], 0
	v_fmamk_f32 v8, v8, 0xbdd2d3e8, v100
	v_mul_f32_e32 v8, v6, v8
	v_fmamk_f32 v9, v9, 0xbdd2d3e8, v100
	v_exp_f32_e32 v8, v8
	v_mul_f32_e32 v9, v7, v9
	v_exp_f32_e32 v9, v9
	ds_write_b128 v125, v[14:17] offset:16
	v_add_f32_e32 v5, 1.0, v8
	v_rcp_f32_e32 v8, v5
	v_add_f32_e32 v5, 1.0, v9
	v_rcp_f32_e32 v9, v5
	v_fmamk_f32 v5, v10, 0xbdd2d3e8, v100
	v_mul_f32_e32 v5, v0, v5
	v_fmamk_f32 v10, v11, 0xbdd2d3e8, v100
	v_exp_f32_e32 v5, v5
	v_mul_f32_e32 v10, v1, v10
	v_exp_f32_e32 v10, v10
	v_pk_mul_f32 v[6:7], v[6:7], v[8:9]
	v_add_f32_e32 v5, 1.0, v5
	v_rcp_f32_e32 v8, v5
	v_add_f32_e32 v5, 1.0, v10

.Lw2b30:
	v_pk_mul_f32 v[10:11], v[2:3], v[2:3]
	ds_write_b128 v125, v[22:25] offset:32
	v_fmamk_f32 v9, v10, 0xbdd2d3e8, v100
	v_mul_f32_e32 v9, v2, v9
	v_exp_f32_e32 v10, v9
	v_fmamk_f32 v9, v11, 0xbdd2d3e8, v100
	v_mul_f32_e32 v9, v3, v9
	v_exp_f32_e32 v11, v9
	v_rcp_f32_e32 v9, v5
	v_add_f32_e32 v5, 1.0, v10
	v_rcp_f32_e32 v10, v5
	v_add_f32_e32 v5, 1.0, v11
	v_rcp_f32_e32 v11, v5
	v_pk_mul_f32 v[0:1], v[0:1], v[8:9]
	v_cvt_pk_f16_f32 v5, v6, v7
	v_cvt_pk_f16_f32 v6, v0, v1
	v_pk_mul_f32 v[0:1], v[2:3], v[10:11]
	s_nop 0
	v_cvt_pk_f16_f32 v7, v0, v1
	ds_write_b128 v125, v[4:7] offset:48
	ds_read_b128 v[4:7], v126

.Lw2b31:
	ds_read_b128 v[8:11], v126 offset:1088
	ds_read_b128 v[12:15], v126 offset:2176
	ds_read_b128 v[16:19], v126 offset:3264
	s_cmp_lg_u32 s47, 0
	s_waitcnt lgkmcnt(0)
	s_cbranch_scc1 .Lh1_wt
	global_store_dwordx4 v[104:105], v[4:7], off
	global_store_dwordx4 v[104:105], v[8:11], off offset:1024
	global_store_dwordx4 v[104:105], v[12:15], off offset:2048
	global_store_dwordx4 v[104:105], v[16:19], off offset:3072
	s_branch .LBB2_8

.LBB2_9:
	v_mov_b32_e32 v0, 0
	s_and_saveexec_b64 s[4:5], s[0:1]
.Lw2t32:
	s_cbranch_execz .Lw2c32
.Lw2b32:
	s_cbranch_execz .LBB2_13
	s_mov_b64 s[14:15], exec
	v_mbcnt_lo_u32_b32 v0, s14, 0
	v_mbcnt_hi_u32_b32 v0, s15, v0
	v_cmp_eq_u32_e32 vcc, 0, v0
	s_and_saveexec_b64 s[10:11], vcc
	s_bcnt1_i32_b64 s12, s[14:15]
	v_mov_b32_e32 v1, s12
	ds_add_rtn_u32 v1, v96, v1
	s_or_b64 exec, exec, s[10:11]
	s_waitcnt lgkmcnt(0)
	v_readfirstlane_b32 s10, v1
	s_nop 1
	v_add_u32_e32 v0, s10, v0
.LBB2_13:
	s_or_b64 exec, exec, s[4:5]
	v_readfirstlane_b32 s4, v0
	s_waitcnt lgkmcnt(0)
	s_mul_i32 s10, s4, s3
	s_add_i32 s10, s10, s2
	s_cmpk_gt_i32 s10, 0x1869
	s_mov_b64 s[4:5], -1
	s_cbranch_scc1 .LBB2_8
	ds_read_b128 v[28:31], v97
	ds_read_b128 v[24:27], v97 offset:16
	ds_read_b128 v[20:23], v97 offset:32
.Lw2t33:
	s_cbranch_execz .Lw2c33
.Lw2b33:
	ds_read_b128 v[16:19], v97 offset:48
	ds_read_b128 v[12:15], v97 offset:64
	ds_read_b128 v[8:11], v97 offset:80
	ds_read_b128 v[4:7], v97 offset:96
	ds_read_b128 v[0:3], v97 offset:112
	s_lshl_b32 s4, s10, 4
	s_ashr_i32 s5, s4, 31
	v_lshl_add_u64 v[80:81], s[4:5], 2, v[74:75]
	s_mov_b32 s5, 0
	s_mov_b64 s[18:19], -1
	s_branch .LBB2_16
.LBB2_15:
	s_or_b64 exec, exec, s[14:15]
	v_mov_b32_e32 v48, v77
	ds_read_b128 v[32:35], v98
	ds_read_b128 v[36:39], v98 offset:64
	ds_read_b128 v[40:43], v98 offset:128
	ds_read_b128 v[44:47], v98 offset:192
	s_nop 0
	v_lshlrev_b32_e32 v48, 4, v48
	v_lshl_add_u32 v103, s5, 15, v48
.Lw2t34:
	s_cbranch_execz .Lw2c34
.Lw2b34:
	ds_read_b128 v[48:51], v103
	ds_read_b128 v[52:55], v103 offset:1024
	ds_read_b128 v[56:59], v103 offset:2048
	ds_read_b128 v[60:63], v103 offset:3072
	ds_read_b128 v[64:67], v103 offset:4096
	ds_read_b128 v[68:71], v103 offset:5120
	ds_read_b128 v[104:107], v103 offset:6144
	ds_read_b128 v[108:111], v103 offset:7168
	s_waitcnt lgkmcnt(7)
	v_mfma_f32_16x16x32_f16 v[28:31], v[48:51], v[32:35], v[28:31]
	s_waitcnt lgkmcnt(6)
	v_mfma_f32_16x16x32_f16 v[24:27], v[52:55], v[32:35], v[24:27]
	s_waitcnt lgkmcnt(5)
	v_mfma_f32_16x16x32_f16 v[20:23], v[56:59], v[32:35], v[20:23]
	s_waitcnt lgkmcnt(4)
	v_mfma_f32_16x16x32_f16 v[16:19], v[60:63], v[32:35], v[16:19]
	ds_read_b128 v[48:51], v103 offset:8192
	ds_read_b128 v[52:55], v103 offset:9216

.Lw2b35:
	ds_read_b128 v[56:59], v103 offset:10240
	ds_read_b128 v[60:63], v103 offset:11264
	s_waitcnt lgkmcnt(7)
	v_mfma_f32_16x16x32_f16 v[12:15], v[64:67], v[32:35], v[12:15]
	s_waitcnt lgkmcnt(6)
	v_mfma_f32_16x16x32_f16 v[8:11], v[68:71], v[32:35], v[8:11]
	s_waitcnt lgkmcnt(5)
	v_mfma_f32_16x16x32_f16 v[4:7], v[104:107], v[32:35], v[4:7]
	s_waitcnt lgkmcnt(4)
	v_mfma_f32_16x16x32_f16 v[0:3], v[108:111], v[32:35], v[0:3]
	ds_read_b128 v[32:35], v103 offset:12288
	ds_read_b128 v[64:67], v103 offset:13312
	ds_read_b128 v[68:71], v103 offset:14336
	ds_read_b128 v[104:107], v103 offset:15360
	s_waitcnt lgkmcnt(7)
	v_mfma_f32_16x16x32_f16 v[28:31], v[48:51], v[36:39], v[28:31]
	s_waitcnt lgkmcnt(6)
	v_mfma_f32_16x16x32_f16 v[24:27], v[52:55], v[36:39], v[24:27]

.Lw2b36:
	s_waitcnt lgkmcnt(5)
	v_mfma_f32_16x16x32_f16 v[20:23], v[56:59], v[36:39], v[20:23]
	s_waitcnt lgkmcnt(4)
	v_mfma_f32_16x16x32_f16 v[16:19], v[60:63], v[36:39], v[16:19]
	ds_read_b128 v[48:51], v103 offset:16384
	ds_read_b128 v[52:55], v103 offset:17408
	ds_read_b128 v[56:59], v103 offset:18432
	ds_read_b128 v[60:63], v103 offset:19456
	s_waitcnt lgkmcnt(7)
	v_mfma_f32_16x16x32_f16 v[12:15], v[32:35], v[36:39], v[12:15]
	s_waitcnt lgkmcnt(6)
	v_mfma_f32_16x16x32_f16 v[8:11], v[64:67], v[36:39], v[8:11]
	s_waitcnt lgkmcnt(5)
	v_mfma_f32_16x16x32_f16 v[4:7], v[68:71], v[36:39], v[4:7]
	s_waitcnt lgkmcnt(4)
	v_mfma_f32_16x16x32_f16 v[0:3], v[104:107], v[36:39], v[0:3]
	ds_read_b128 v[32:35], v103 offset:20480
	ds_read_b128 v[36:39], v103 offset:21504
	ds_read_b128 v[64:67], v103 offset:22528

.Lw2b37:
	ds_read_b128 v[68:71], v103 offset:23552
	s_waitcnt lgkmcnt(7)
	v_mfma_f32_16x16x32_f16 v[28:31], v[48:51], v[40:43], v[28:31]
	s_waitcnt lgkmcnt(6)
	v_mfma_f32_16x16x32_f16 v[24:27], v[52:55], v[40:43], v[24:27]
	s_waitcnt lgkmcnt(5)
	v_mfma_f32_16x16x32_f16 v[20:23], v[56:59], v[40:43], v[20:23]
	s_waitcnt lgkmcnt(4)
	v_mfma_f32_16x16x32_f16 v[16:19], v[60:63], v[40:43], v[16:19]
	ds_read_b128 v[48:51], v103 offset:24576
	ds_read_b128 v[52:55], v103 offset:25600
	ds_read_b128 v[56:59], v103 offset:26624
	ds_read_b128 v[60:63], v103 offset:27648
	s_waitcnt lgkmcnt(7)
	v_mfma_f32_16x16x32_f16 v[12:15], v[32:35], v[40:43], v[12:15]
	s_waitcnt lgkmcnt(6)
	v_mfma_f32_16x16x32_f16 v[8:11], v[36:39], v[40:43], v[8:11]
	s_waitcnt lgkmcnt(5)
	v_mfma_f32_16x16x32_f16 v[4:7], v[64:67], v[40:43], v[4:7]

.Lw2b38:
	s_waitcnt lgkmcnt(4)
	v_mfma_f32_16x16x32_f16 v[0:3], v[68:71], v[40:43], v[0:3]
	ds_read_b128 v[32:35], v103 offset:28672
	ds_read_b128 v[36:39], v103 offset:29696
	ds_read_b128 v[40:43], v103 offset:30720
	ds_read_b128 v[64:67], v103 offset:31744
	s_waitcnt lgkmcnt(7)
	v_mfma_f32_16x16x32_f16 v[28:31], v[48:51], v[44:47], v[28:31]
	s_waitcnt lgkmcnt(6)
	v_mfma_f32_16x16x32_f16 v[24:27], v[52:55], v[44:47], v[24:27]
	s_waitcnt lgkmcnt(5)
	v_mfma_f32_16x16x32_f16 v[20:23], v[56:59], v[44:47], v[20:23]
	s_waitcnt lgkmcnt(4)
	v_mfma_f32_16x16x32_f16 v[16:19], v[60:63], v[44:47], v[16:19]
	s_waitcnt lgkmcnt(3)
	v_mfma_f32_16x16x32_f16 v[12:15], v[32:35], v[44:47], v[12:15]
	s_waitcnt lgkmcnt(2)
	v_mfma_f32_16x16x32_f16 v[8:11], v[36:39], v[44:47], v[8:11]
	s_waitcnt lgkmcnt(1)

.Lw2b39:
	v_mfma_f32_16x16x32_f16 v[4:7], v[40:43], v[44:47], v[4:7]
	s_waitcnt lgkmcnt(0)
	v_mfma_f32_16x16x32_f16 v[0:3], v[64:67], v[44:47], v[0:3]
	s_mov_b32 s5, 1
	s_mov_b64 s[18:19], 0
	s_and_b64 vcc, exec, s[10:11]
	s_cbranch_vccnz .LBB2_7
.LBB2_16:
	s_mul_i32 s12, s5, 0x186a1
	v_lshl_add_u64 v[32:33], s[12:13], 2, v[80:81]
	global_load_dword v113, v[32:33], off
	global_load_dword v103, v[32:33], off offset:16
	s_mov_b32 s14, s13
	s_mov_b32 s15, s13
	s_mul_i32 s12, s5, 0xc3500
	s_lshl_b64 s[10:11], s[12:13], 2
	s_mov_b32 s12, s13
	v_mov_b64_e32 v[34:35], s[14:15]
	v_mov_b64_e32 v[32:33], s[12:13]
	s_add_u32 s16, s6, s10
	ds_write_b128 v85, v[32:35]
	ds_write_b128 v85, v[32:35] offset:16
	ds_write_b128 v85, v[32:35] offset:32
	ds_write_b128 v85, v[32:35] offset:48
	s_addc_u32 s17, s7, s11
.Lw2t40:
	s_cbranch_execz .Lw2c40

.LBB2_19:
	s_waitcnt vmcnt(0)
	v_mov_b32_e32 v116, v114
.Lw2t41:
	s_cbranch_execz .Lw2c41

.LBB2_20:
	s_nop 2
	v_mov_b32_e32 v104, v63
	v_mov_b32_e32 v106, v62
	v_mov_b32_e32 v105, v61
	v_mov_b32_e32 v108, v60
	v_mov_b32_e32 v109, v59
	v_mov_b32_e32 v111, v58
	v_mov_b32_e32 v110, v57
	v_mov_b32_e32 v112, v56
	v_mov_b32_e32 v107, v115
	v_cmp_lt_i32_e32 vcc, v113, v103
	s_cbranch_vccz .LBB2_19
	v_or_b32_e32 v32, 4, v84
	s_waitcnt vmcnt(0)
	ds_bpermute_b32 v66, v84, v116
	ds_bpermute_b32 v123, v32, v116
	v_or_b32_e32 v32, 8, v84
	v_or_b32_e32 v34, 12, v84
	ds_bpermute_b32 v122, v32, v116
	ds_bpermute_b32 v121, v34, v116
	v_or_b32_e32 v34, 16, v84
	ds_bpermute_b32 v120, v34, v116
	v_or_b32_e32 v34, 20, v84
	ds_bpermute_b32 v119, v34, v116

.Lw2b42:
	s_waitcnt lgkmcnt(5)
	v_lshlrev_b32_e32 v32, 8, v66
	s_waitcnt lgkmcnt(4)
	v_lshlrev_b32_e32 v33, 8, v123
	v_or_b32_e32 v34, 24, v84
	v_and_or_b32 v32, v32, s21, v83
	v_and_or_b32 v33, v33, s21, v83
	ds_bpermute_b32 v118, v34, v116
	ds_bpermute_b32 v117, v87, v116
	global_load_dwordx4 v[60:63], v32, s[8:9]
	global_load_dwordx4 v[56:59], v33, s[8:9]
	s_waitcnt lgkmcnt(5)
	v_lshlrev_b32_e32 v32, 8, v122
	s_waitcnt lgkmcnt(4)
	v_lshlrev_b32_e32 v33, 8, v121
	v_and_or_b32 v32, v32, s21, v83
	v_and_or_b32 v33, v33, s21, v83
	global_load_dwordx4 v[52:55], v32, s[8:9]
	global_load_dwordx4 v[48:51], v33, s[8:9]
	s_waitcnt lgkmcnt(3)
	v_lshlrev_b32_e32 v32, 8, v120

.Lw2b43:
	s_waitcnt lgkmcnt(2)
	v_lshlrev_b32_e32 v33, 8, v119
	v_and_or_b32 v32, v32, s21, v83
	v_and_or_b32 v33, v33, s21, v83
	global_load_dwordx4 v[44:47], v32, s[8:9]
	global_load_dwordx4 v[40:43], v33, s[8:9]
	s_waitcnt lgkmcnt(1)
	v_lshlrev_b32_e32 v32, 8, v118
	s_waitcnt lgkmcnt(0)
	v_lshlrev_b32_e32 v33, 8, v117
	v_and_or_b32 v32, v32, s21, v83
	v_and_or_b32 v33, v33, s21, v83
	global_load_dwordx4 v[36:39], v32, s[8:9]
	s_nop 0
	global_load_dwordx4 v[32:35], v33, s[8:9]
	v_or_b32_e32 v64, 16, v82
	v_add_u32_e32 v64, v64, v113
	v_cmp_lt_i32_e32 vcc, v64, v103
	v_mov_b32_e32 v114, 0x3f86a0
	s_and_saveexec_b64 s[14:15], vcc
	s_cbranch_execz .LBB2_23
	v_ashrrev_i32_e32 v65, 31, v64

.Lw2b44:
	v_lshl_add_u64 v[64:65], v[64:65], 2, s[16:17]
	global_load_dword v114, v[64:65], off
.LBB2_23:
	s_or_b64 exec, exec, s[14:15]
	v_ashrrev_i32_e32 v124, 17, v66
	v_cmp_ne_u32_e32 vcc, v124, v107
	s_cmp_lg_u64 vcc, 0
	s_cselect_b64 s[14:15], -1, 0
	s_and_b64 s[18:19], s[14:15], vcc
	v_mov_b32_e32 v115, v107
	v_mov_b32_e32 v68, v112
	v_mov_b32_e32 v69, v110
	v_mov_b32_e32 v70, v111
	v_mov_b32_e32 v71, v109
	v_mov_b32_e32 v64, v108
	v_mov_b32_e32 v65, v105
	v_mov_b32_e32 v66, v106
	v_mov_b32_e32 v67, v104
	s_and_saveexec_b64 s[14:15], s[18:19]
	s_cbranch_execz .LBB2_27
	v_cmp_gt_i32_e32 vcc, 16, v107
	s_and_saveexec_b64 s[18:19], vcc
	s_cbranch_execz .LBB2_26
	v_cvt_pk_f16_f32 v67, v111, v109
	v_cvt_pk_f16_f32 v66, v112, v110
	v_cvt_pk_f16_f32 v65, v106, v104
	v_cvt_pk_f16_f32 v64, v108, v105

.LBB2_27:
	s_or_b64 exec, exec, s[14:15]
	v_ashrrev_i32_e32 v123, 17, v123
	s_waitcnt vmcnt(7)
	v_mfma_f32_16x16x16_f16 v[64:67], v[72:73], v[60:61], v[64:67]
	v_cmp_ne_u32_e32 vcc, v123, v115
	s_cmp_lg_u64 vcc, 0
	s_cselect_b64 s[14:15], -1, 0
	v_mfma_f32_16x16x16_f16 v[60:63], v[72:73], v[62:63], v[68:71]
	s_and_b64 s[18:19], s[14:15], vcc
	s_and_saveexec_b64 s[14:15], s[18:19]
	s_cbranch_execz .LBB2_31
	v_cmp_gt_i32_e32 vcc, 16, v115
	s_and_saveexec_b64 s[18:19], vcc
	s_cbranch_execz .LBB2_30
.Lw2t46:
	s_cbranch_execz .Lw2c46

.LBB2_31:
	s_or_b64 exec, exec, s[14:15]
	v_ashrrev_i32_e32 v68, 17, v122
	s_waitcnt vmcnt(6)
	v_mfma_f32_16x16x16_f16 v[64:67], v[72:73], v[56:57], v[64:67]
	v_cmp_ne_u32_e32 vcc, v68, v115
	s_cmp_lg_u64 vcc, 0
	s_cselect_b64 s[14:15], -1, 0
.Lw2t47:
	s_cbranch_execz .Lw2c47
.Lw2b47:
	v_mfma_f32_16x16x16_f16 v[56:59], v[72:73], v[58:59], v[60:63]
	s_and_b64 s[18:19], s[14:15], vcc
	s_and_saveexec_b64 s[14:15], s[18:19]
	s_cbranch_execz .LBB2_35
	v_cmp_gt_i32_e32 vcc, 16, v115
	s_and_saveexec_b64 s[18:19], vcc
	s_cbranch_execz .LBB2_34
	s_nop 1
	v_cvt_pk_f16_f32 v59, v58, v59
	v_cvt_pk_f16_f32 v58, v56, v57
	v_cvt_pk_f16_f32 v57, v66, v67
	v_cvt_pk_f16_f32 v56, v64, v65
	v_mad_u64_u32 v[60:61], s[24:25], v115, s20, v[76:77]
	ds_write_b128 v60, v[56:59]
.LBB2_34:
	s_or_b64 exec, exec, s[18:19]
	s_nop 0
	v_mov_b32_e32 v56, 0
	v_mov_b32_e32 v115, v68
	v_mov_b32_e32 v57, v56
	v_mov_b32_e32 v58, v56
	v_mov_b32_e32 v59, v56
	v_mov_b32_e32 v64, v56
	v_mov_b32_e32 v65, v56
.Lw2t48:
	s_cbranch_execz .Lw2c48

.LBB2_39:
	s_or_b64 exec, exec, s[14:15]
	v_ashrrev_i32_e32 v64, 17, v120
	s_waitcnt vmcnt(4)
	v_mfma_f32_16x16x16_f16 v[56:59], v[72:73], v[48:49], v[60:63]
	v_cmp_ne_u32_e32 vcc, v64, v115
	s_cmp_lg_u64 vcc, 0
	s_cselect_b64 s[14:15], -1, 0
	v_mfma_f32_16x16x16_f16 v[48:51], v[72:73], v[50:51], v[52:55]
	s_and_b64 s[18:19], s[14:15], vcc
	s_and_saveexec_b64 s[14:15], s[18:19]
	s_cbranch_execz .LBB2_43
	v_cmp_gt_i32_e32 vcc, 16, v115
	s_and_saveexec_b64 s[18:19], vcc
	s_cbranch_execz .LBB2_42
	s_nop 1
	v_cvt_pk_f16_f32 v51, v50, v51
	v_cvt_pk_f16_f32 v50, v48, v49
.Lw2t50:
	s_cbranch_execz .Lw2c50

.LBB2_43:
	s_or_b64 exec, exec, s[14:15]
	v_ashrrev_i32_e32 v60, 17, v119
	s_waitcnt vmcnt(3)
	v_mfma_f32_16x16x16_f16 v[52:55], v[72:73], v[44:45], v[56:59]
	v_cmp_ne_u32_e32 vcc, v60, v115
	s_cmp_lg_u64 vcc, 0
	s_cselect_b64 s[14:15], -1, 0
	v_mfma_f32_16x16x16_f16 v[44:47], v[72:73], v[46:47], v[48:51]
	s_and_b64 s[18:19], s[14:15], vcc
.Lw2t51:
	s_cbranch_execz .Lw2c51
.Lw2b51:
	s_and_saveexec_b64 s[14:15], s[18:19]
	s_cbranch_execz .LBB2_47
	v_cmp_gt_i32_e32 vcc, 16, v115
	s_and_saveexec_b64 s[18:19], vcc
	s_cbranch_execz .LBB2_46
	s_nop 1
	v_cvt_pk_f16_f32 v47, v46, v47
	v_cvt_pk_f16_f32 v46, v44, v45
	v_cvt_pk_f16_f32 v45, v54, v55
	v_cvt_pk_f16_f32 v44, v52, v53
	v_mad_u64_u32 v[48:49], s[24:25], v115, s20, v[76:77]
	ds_write_b128 v48, v[44:47]

.LBB2_47:
	s_or_b64 exec, exec, s[14:15]
	v_ashrrev_i32_e32 v56, 17, v118
.Lw2t52:
	s_cbranch_execz .Lw2c52
.Lw2b52:
	s_waitcnt vmcnt(2)
	v_mfma_f32_16x16x16_f16 v[48:51], v[72:73], v[40:41], v[52:55]
	v_cmp_ne_u32_e32 vcc, v56, v115
	s_cmp_lg_u64 vcc, 0
	s_cselect_b64 s[14:15], -1, 0
	v_mfma_f32_16x16x16_f16 v[40:43], v[72:73], v[42:43], v[44:47]
	s_and_b64 s[18:19], s[14:15], vcc
	s_and_saveexec_b64 s[14:15], s[18:19]
	s_cbranch_execz .LBB2_51
	v_cmp_gt_i32_e32 vcc, 16, v115
	s_and_saveexec_b64 s[18:19], vcc
	s_cbranch_execz .LBB2_50
	s_nop 1
	v_cvt_pk_f16_f32 v43, v42, v43
	v_cvt_pk_f16_f32 v42, v40, v41
	v_cvt_pk_f16_f32 v41, v50, v51
	v_cvt_pk_f16_f32 v40, v48, v49
	v_mad_u64_u32 v[44:45], s[24:25], v115, s20, v[76:77]
	ds_write_b128 v44, v[40:43]
.LBB2_50:
	s_or_b64 exec, exec, s[18:19]
	s_nop 0
	v_mov_b32_e32 v40, 0
	v_mov_b32_e32 v115, v56
.Lw2t53:
	s_cbranch_execz .Lw2c53
.Lw2b53:
	v_mov_b32_e32 v41, v40
	v_mov_b32_e32 v42, v40
	v_mov_b32_e32 v43, v40
	v_mov_b32_e32 v48, v40
	v_mov_b32_e32 v49, v40
	v_mov_b32_e32 v50, v40
	v_mov_b32_e32 v51, v40
.LBB2_51:
	s_or_b64 exec, exec, s[14:15]
	v_ashrrev_i32_e32 v52, 17, v117
	s_waitcnt vmcnt(1)
	v_mfma_f32_16x16x16_f16 v[44:47], v[72:73], v[36:37], v[48:51]
	v_cmp_ne_u32_e32 vcc, v52, v115
	s_cmp_lg_u64 vcc, 0
	s_cselect_b64 s[14:15], -1, 0
	v_mfma_f32_16x16x16_f16 v[36:39], v[72:73], v[38:39], v[40:43]
	s_and_b64 s[18:19], s[14:15], vcc
	s_and_saveexec_b64 s[14:15], s[18:19]
	s_cbranch_execz .LBB2_55
	v_cmp_gt_i32_e32 vcc, 16, v115
	s_and_saveexec_b64 s[18:19], vcc
	s_cbranch_execz .LBB2_54
	s_nop 1
	v_cvt_pk_f16_f32 v39, v38, v39
	v_cvt_pk_f16_f32 v38, v36, v37
	v_cvt_pk_f16_f32 v37, v46, v47
	v_cvt_pk_f16_f32 v36, v44, v45

.LBB2_54:
	s_or_b64 exec, exec, s[18:19]
	s_nop 0
	v_mov_b32_e32 v36, 0
	v_mov_b32_e32 v115, v52
	v_mov_b32_e32 v37, v36
	v_mov_b32_e32 v38, v36
	v_mov_b32_e32 v39, v36
	v_mov_b32_e32 v44, v36
	v_mov_b32_e32 v45, v36
	v_mov_b32_e32 v46, v36
	v_mov_b32_e32 v47, v36
.LBB2_55:
	s_or_b64 exec, exec, s[14:15]
	s_waitcnt vmcnt(0)
	v_mfma_f32_16x16x16_f16 v[60:63], v[72:73], v[32:33], v[44:47]
	v_add_u32_e32 v32, 8, v113
	v_cmp_lt_i32_e32 vcc, v32, v103
	v_mfma_f32_16x16x16_f16 v[56:59], v[72:73], v[34:35], v[36:39]
	s_cbranch_vccz .LBB2_89
	ds_bpermute_b32 v123, v88, v116
	ds_bpermute_b32 v122, v89, v116
	ds_bpermute_b32 v121, v90, v116

.Lw2b55:
	ds_bpermute_b32 v120, v91, v116
	ds_bpermute_b32 v119, v92, v116
	ds_bpermute_b32 v118, v93, v116
	s_waitcnt lgkmcnt(5)
	v_lshlrev_b32_e32 v32, 8, v123
	s_waitcnt lgkmcnt(4)
	v_lshlrev_b32_e32 v33, 8, v122
	v_and_or_b32 v32, v32, s21, v83
	v_and_or_b32 v33, v33, s21, v83
	ds_bpermute_b32 v117, v94, v116
	ds_bpermute_b32 v116, v95, v116
	global_load_dwordx4 v[68:71], v32, s[8:9]
	global_load_dwordx4 v[64:67], v33, s[8:9]
	s_waitcnt lgkmcnt(5)
	v_lshlrev_b32_e32 v32, 8, v121
	s_waitcnt lgkmcnt(4)
	v_lshlrev_b32_e32 v33, 8, v120
	v_and_or_b32 v32, v32, s21, v83
	v_and_or_b32 v33, v33, s21, v83
	global_load_dwordx4 v[52:55], v32, s[8:9]

.Lw2b56:
	global_load_dwordx4 v[48:51], v33, s[8:9]
	s_waitcnt lgkmcnt(3)
	v_lshlrev_b32_e32 v32, 8, v119
	s_waitcnt lgkmcnt(2)
	v_lshlrev_b32_e32 v33, 8, v118
	v_and_or_b32 v32, v32, s21, v83
	v_and_or_b32 v33, v33, s21, v83
	global_load_dwordx4 v[44:47], v32, s[8:9]
	global_load_dwordx4 v[40:43], v33, s[8:9]
	s_waitcnt lgkmcnt(1)
	v_lshlrev_b32_e32 v32, 8, v117
	s_waitcnt lgkmcnt(0)
	v_lshlrev_b32_e32 v33, 8, v116
	v_and_or_b32 v32, v32, s21, v83
	v_and_or_b32 v33, v33, s21, v83
	global_load_dwordx4 v[36:39], v32, s[8:9]
	s_nop 0
	global_load_dwordx4 v[32:35], v33, s[8:9]
	v_ashrrev_i32_e32 v123, 17, v123
	v_cmp_ne_u32_e32 vcc, v123, v115
	s_cmp_lg_u64 vcc, 0
	s_cselect_b64 s[14:15], -1, 0

.Lw2b57:
	s_and_b64 s[18:19], s[14:15], vcc
	s_and_saveexec_b64 s[14:15], s[18:19]
	s_cbranch_execz .LBB2_60
	v_cmp_gt_i32_e32 vcc, 16, v115
	s_and_saveexec_b64 s[18:19], vcc
	s_cbranch_execz .LBB2_59
	v_cvt_pk_f16_f32 v59, v58, v59
	v_cvt_pk_f16_f32 v58, v56, v57
	v_cvt_pk_f16_f32 v57, v62, v63
	v_cvt_pk_f16_f32 v56, v60, v61
	v_mad_u64_u32 v[60:61], s[24:25], v115, s20, v[76:77]
	ds_write_b128 v60, v[56:59]

.LBB2_60:
	s_or_b64 exec, exec, s[14:15]
	v_ashrrev_i32_e32 v122, 17, v122
.Lw2t58:
	s_cbranch_execz .Lw2c58
.Lw2b58:
	s_waitcnt vmcnt(7)
	v_mfma_f32_16x16x16_f16 v[60:63], v[72:73], v[68:69], v[60:63]
	v_cmp_ne_u32_e32 vcc, v122, v115
	s_cmp_lg_u64 vcc, 0
	s_cselect_b64 s[14:15], -1, 0
	v_mfma_f32_16x16x16_f16 v[56:59], v[72:73], v[70:71], v[56:59]
	s_and_b64 s[18:19], s[14:15], vcc
	s_and_saveexec_b64 s[14:15], s[18:19]
	s_cbranch_execz .LBB2_64
	v_cmp_gt_i32_e32 vcc, 16, v115
	s_and_saveexec_b64 s[18:19], vcc
	s_cbranch_execz .LBB2_63
	s_nop 1
	v_cvt_pk_f16_f32 v59, v58, v59
	v_cvt_pk_f16_f32 v58, v56, v57
	v_cvt_pk_f16_f32 v57, v62, v63
	v_cvt_pk_f16_f32 v56, v60, v61
	v_mad_u64_u32 v[60:61], s[24:25], v115, s20, v[76:77]
	ds_write_b128 v60, v[56:59]
.LBB2_63:
	s_or_b64 exec, exec, s[18:19]
	s_nop 0
	v_mov_b32_e32 v56, 0
	v_mov_b32_e32 v115, v122
.Lw2t59:
	s_cbranch_execz .Lw2c59

.LBB2_64:
	s_or_b64 exec, exec, s[14:15]
	v_ashrrev_i32_e32 v68, 17, v121
	s_waitcnt vmcnt(6)
	v_mfma_f32_16x16x16_f16 v[60:63], v[72:73], v[64:65], v[60:63]
	v_cmp_ne_u32_e32 vcc, v68, v115
	s_cmp_lg_u64 vcc, 0
	s_cselect_b64 s[14:15], -1, 0
	v_mfma_f32_16x16x16_f16 v[56:59], v[72:73], v[66:67], v[56:59]
	s_and_b64 s[18:19], s[14:15], vcc
	s_and_saveexec_b64 s[14:15], s[18:19]
	s_cbranch_execz .LBB2_68
	v_cmp_gt_i32_e32 vcc, 16, v115
	s_and_saveexec_b64 s[18:19], vcc
	s_cbranch_execz .LBB2_67
	s_nop 1
	v_cvt_pk_f16_f32 v59, v58, v59
	v_cvt_pk_f16_f32 v58, v56, v57
	v_cvt_pk_f16_f32 v57, v62, v63
	v_cvt_pk_f16_f32 v56, v60, v61

.LBB2_72:
	s_or_b64 exec, exec, s[14:15]
	v_ashrrev_i32_e32 v64, 17, v119
	s_waitcnt vmcnt(4)
	v_mfma_f32_16x16x16_f16 v[56:59], v[72:73], v[48:49], v[60:63]
	v_cmp_ne_u32_e32 vcc, v64, v115
.Lw2t62:
	s_cbranch_execz .Lw2c62
.Lw2b62:
	s_cmp_lg_u64 vcc, 0
	s_cselect_b64 s[14:15], -1, 0
	v_mfma_f32_16x16x16_f16 v[48:51], v[72:73], v[50:51], v[52:55]
	s_and_b64 s[18:19], s[14:15], vcc
	s_and_saveexec_b64 s[14:15], s[18:19]
	s_cbranch_execz .LBB2_76
	v_cmp_gt_i32_e32 vcc, 16, v115
	s_and_saveexec_b64 s[18:19], vcc
	s_cbranch_execz .LBB2_75
	s_nop 1
	v_cvt_pk_f16_f32 v51, v50, v51
	v_cvt_pk_f16_f32 v50, v48, v49
	v_cvt_pk_f16_f32 v49, v58, v59
	v_cvt_pk_f16_f32 v48, v56, v57
	v_mad_u64_u32 v[52:53], s[24:25], v115, s20, v[76:77]
	ds_write_b128 v52, v[48:51]
.LBB2_75:
	s_or_b64 exec, exec, s[18:19]
	s_nop 0
	v_mov_b32_e32 v48, 0
	v_mov_b32_e32 v115, v64
	v_mov_b32_e32 v49, v48
	v_mov_b32_e32 v50, v48
	v_mov_b32_e32 v51, v48
	v_mov_b32_e32 v56, v48
.Lw2t63:
	s_cbranch_execz .Lw2c63

.Lw2b64:
	s_or_b64 exec, exec, s[18:19]
	s_nop 0
	v_mov_b32_e32 v44, 0
	v_mov_b32_e32 v115, v60
	v_mov_b32_e32 v45, v44
	v_mov_b32_e32 v46, v44
	v_mov_b32_e32 v47, v44
	v_mov_b32_e32 v52, v44
	v_mov_b32_e32 v53, v44
	v_mov_b32_e32 v54, v44
	v_mov_b32_e32 v55, v44
.LBB2_80:
	s_or_b64 exec, exec, s[14:15]
	v_ashrrev_i32_e32 v56, 17, v117
	s_waitcnt vmcnt(2)
	v_mfma_f32_16x16x16_f16 v[48:51], v[72:73], v[40:41], v[52:55]
	v_cmp_ne_u32_e32 vcc, v56, v115
	s_cmp_lg_u64 vcc, 0
	s_cselect_b64 s[14:15], -1, 0
	v_mfma_f32_16x16x16_f16 v[40:43], v[72:73], v[42:43], v[44:47]
	s_and_b64 s[18:19], s[14:15], vcc
	s_and_saveexec_b64 s[14:15], s[18:19]
	s_cbranch_execz .LBB2_84
	v_cmp_gt_i32_e32 vcc, 16, v115
	s_and_saveexec_b64 s[18:19], vcc
	s_cbranch_execz .LBB2_83
	s_nop 1
	v_cvt_pk_f16_f32 v43, v42, v43
.Lw2t65:
	s_cbranch_execz .Lw2c65

.Lw2b66:
	s_and_b64 s[18:19], s[14:15], vcc
	s_and_saveexec_b64 s[14:15], s[18:19]
	s_cbranch_execz .LBB2_88
	v_cmp_gt_i32_e32 vcc, 16, v115
	s_and_saveexec_b64 s[18:19], vcc
	s_cbranch_execz .LBB2_87
	s_nop 1
	v_cvt_pk_f16_f32 v39, v38, v39
	v_cvt_pk_f16_f32 v38, v36, v37
	v_cvt_pk_f16_f32 v37, v46, v47
	v_cvt_pk_f16_f32 v36, v44, v45
	v_mad_u64_u32 v[40:41], s[24:25], v115, s20, v[76:77]
	ds_write_b128 v40, v[36:39]

_Z10k_layer_a2ILi1ELi13EEvPKDF16_PKiS3_PK15HIP_vector_typeIjLj4EES7_PKfS9_S9_S9_S9_S9_PDF16_Pf:
	s_getpc_b64 s[58:59]

.Lw3b0:
	s_and_b32 s58, s58, 0xffffff00
	v_lshlrev_b32_e32 v48, 7, v0
	v_cmp_gt_u32_e32 vcc, 0x3400, v48
	s_and_saveexec_b64 s[60:61], vcc
	global_load_dword v127, v48, s[58:59]
	s_or_b64 exec, exec, s[60:61]
	s_load_dwordx4 s[12:15], s[0:1], 0x38
	s_load_dwordx8 s[4:11], s[0:1], 0x18
	v_lshlrev_b32_e32 v2, 4, v0
	v_min_u32_e32 v1, 0x7f, v0
	v_lshlrev_b32_e32 v26, 2, v1
	v_readfirstlane_b32 s3, v0
	v_add_u32_e32 v28, 0x3400, v2
	v_add_u32_e32 v29, 0x6800, v2
	v_add_u32_e32 v30, 0x9c00, v2
	v_add_u32_e32 v31, 0xd00, v0
	v_min_u32_e32 v31, 0xfff, v31
	v_lshlrev_b32_e32 v31, 4, v31
	v_add_u32_e32 v27, 0x680, v0

.Lw3b1:
	v_min_u32_e32 v27, 0x8ff, v27
	v_lshlrev_b32_e32 v27, 4, v27
	s_waitcnt lgkmcnt(0)
	global_load_dwordx4 v[16:19], v2, s[4:5]
	global_load_dwordx4 v[8:11], v28, s[4:5]
	global_load_dwordx4 v[12:15], v29, s[4:5]
	global_load_dwordx4 v[20:23], v30, s[4:5]
	global_load_dwordx4 v[32:35], v31, s[4:5]
	global_load_dwordx4 v[36:39], v2, s[6:7]
	global_load_dwordx4 v[40:43], v28, s[6:7]
	global_load_dwordx4 v[44:47], v27, s[6:7]
	global_load_dword v5, v26, s[8:9]
	global_load_dword v7, v26, s[8:9] offset:512
	global_load_dword v1, v26, s[10:11]
	global_load_dword v4, v26, s[12:13]
	global_load_dword v6, v26, s[14:15]
	s_load_dword s42, s[0:1], 0x0
	s_load_dword s43, s[0:1], 0x40
	v_lshrrev_b32_e32 v48, 6, v0
	s_nop 0
	v_readfirstlane_b32 s41, v48
	s_movk_i32 s40, 0x5aa5
	s_mov_b64 exec, 0
	s_cmpk_lt_u32 s41, 6
	s_cbranch_scc1 .Lw3s0d0_13
	s_cmpk_lt_u32 s41, 9
	s_cbranch_scc1 .Lw3s0d6_13
	s_cmpk_lt_u32 s41, 11
	s_cbranch_scc1 .Lw3s0d9_13
	s_cmpk_lt_u32 s41, 12
	s_cbranch_scc1 .Lw3s0d11_13
	s_branch .Lw3t12

.Lw3b2:
	s_waitcnt vmcnt(12)
	ds_write_b128 v2, v[16:19]
	s_waitcnt vmcnt(11)
	ds_write_b128 v2, v[8:11] offset:13312
	s_waitcnt vmcnt(10)
	ds_write_b128 v2, v[12:15] offset:26624
	s_waitcnt vmcnt(9)
	ds_write_b128 v2, v[20:23] offset:39936
	s_movk_i32 s4, 0x300
	v_cmp_gt_u32_e32 vcc, s4, v0
	s_waitcnt vmcnt(8)
.Lw3t3:
	s_cbranch_execz .Lw3c3
.Lw3b3:
	s_and_saveexec_b64 s[4:5], vcc
	ds_write_b128 v2, v[32:35] offset:53248
	s_or_b64 exec, exec, s[4:5]
	v_mov_b32_e32 v3, 0x1dd00
	v_lshl_add_u32 v3, v0, 4, v3
	s_waitcnt vmcnt(7)
	ds_write_b128 v3, v[36:39]
	s_waitcnt vmcnt(6)
	ds_write_b128 v3, v[40:43] offset:13312
	s_movk_i32 s4, 0x280
	v_cmp_gt_u32_e32 vcc, s4, v0
	s_waitcnt vmcnt(5)
	s_and_saveexec_b64 s[4:5], vcc
	ds_write_b128 v3, v[44:47] offset:26624
	s_or_b64 exec, exec, s[4:5]
	s_waitcnt vmcnt(0)
	s_movk_i32 s4, 0x80
	v_cmp_gt_u32_e32 vcc, s4, v0
	s_and_saveexec_b64 s[4:5], vcc
	s_cbranch_execz .LBB3_6
	v_mov_b32_e32 v3, 0x26d00
	v_add_f32_e32 v2, v5, v7
	v_lshl_add_u32 v3, v0, 2, v3

.Lw3b4:
	ds_write2st64_b32 v3, v2, v1 offset1:2
	ds_write2st64_b32 v3, v4, v6 offset0:4 offset1:6
.LBB3_6:
	s_or_b64 exec, exec, s[4:5]
	s_load_dwordx2 s[6:7], s[0:1], 0x60
	s_load_dwordx2 s[16:17], s[0:1], 0x50
	s_load_dwordx4 s[8:11], s[0:1], 0x0
	s_load_dwordx2 s[18:19], s[0:1], 0x10
	s_mov_b32 s13, 0
	v_cmp_eq_u32_e32 vcc, 0, v0
	s_and_saveexec_b64 s[4:5], vcc
	v_mov_b32_e32 v1, 0
	v_mov_b32_e32 v2, 0x27900
	ds_write_b32 v2, v1
	s_or_b64 exec, exec, s[4:5]
	v_bfe_u32 v1, v0, 4, 2
	v_bfe_u32 v2, v0, 2, 2
	v_cmp_eq_u32_e32 vcc, v1, v2
	v_and_b32_e32 v2, 3, v0
	v_cmp_eq_u32_e64 s[4:5], 0, v2
	v_mov_b32_e32 v3, 0x3c00

.Lw3b5:
	s_and_b64 s[4:5], vcc, s[4:5]
	v_cndmask_b32_e64 v4, 0, v3, s[4:5]
	v_cmp_eq_u32_e64 s[4:5], 1, v2
	s_and_b64 s[4:5], vcc, s[4:5]
	s_lshr_b32 s12, s3, 6
	v_cndmask_b32_e64 v5, 0, v3, s[4:5]
	v_cmp_eq_u32_e64 s[4:5], 2, v2
	s_and_b64 s[4:5], vcc, s[4:5]
	v_and_b32_e32 v77, 63, v0
	v_cndmask_b32_e64 v6, 0, v3, s[4:5]
	v_cmp_eq_u32_e64 s[4:5], 3, v2
	s_and_b64 vcc, vcc, s[4:5]
	v_cndmask_b32_e32 v2, 0, v3, vcc
	v_pack_b32_f16 v73, v6, v2
	v_lshlrev_b32_e32 v2, 2, v0
	v_and_b32_e32 v82, 0xc0, v2
	v_and_b32_e32 v2, 48, v0
	v_mov_b32_e32 v3, 0
	s_waitcnt lgkmcnt(0)
	s_barrier
	v_and_b32_e32 v80, 15, v0
	s_load_dword s3, s[0:1], 0x68

.Lw3b6:
	s_mul_i32 s0, s12, 0x1100
	v_lshl_add_u64 v[74:75], s[10:11], 0, v[2:3]
	v_bfe_u32 v3, v0, 2, 4
	v_lshlrev_b32_e32 v0, 6, v0
	s_add_i32 s4, s0, 0x10000
	v_mul_u32_u24_e32 v3, 0x110, v3
	v_and_b32_e32 v0, 0xc0, v0
	s_movk_i32 s26, 0x110
	v_add3_u32 v83, s4, v3, v0
	v_mov_b32_e32 v0, s4
	v_mad_u32_u24 v0, v80, s26, v0
	v_pack_b32_f16 v72, v4, v5
	v_lshlrev_b32_e32 v81, 4, v80
	v_lshlrev_b32_e32 v4, 7, v1
	v_add_u32_e32 v97, v0, v2
	v_mbcnt_lo_u32_b32 v0, -1, 0
	v_cmp_eq_u32_e64 s[0:1], 0, v77
	v_or_b32_e32 v76, s4, v81
	v_lshlrev_b32_e32 v84, 5, v1

.Lw3b7:
	v_cmp_gt_u32_e64 s[4:5], 16, v77
	v_or_b32_e32 v85, 24, v82
	v_or_b32_e32 v86, 28, v82
	v_or_b32_e32 v87, 32, v82
	v_or_b32_e32 v88, 36, v82
	v_or_b32_e32 v89, 40, v82
	v_or_b32_e32 v90, 44, v82
	v_or_b32_e32 v91, 48, v82
	v_or_b32_e32 v92, 52, v82
	v_or_b32_e32 v93, 56, v82
	v_or_b32_e32 v94, 60, v82
	v_mov_b32_e32 v95, 0x27900
	v_add_u32_e32 v96, 0x26d00, v4
	s_mov_b32 s27, 0x1ffff00
	v_mov_b32_e32 v98, 0x3727c5ac
	s_mov_b32 s28, 0x800000
	v_mov_b32_e32 v99, 0xc0135761
	v_mbcnt_hi_u32_b32 v100, -1, v0
	v_mov_b32_e32 v101, 0x26d00
	v_mov_b32_e32 v102, 0x1dd00
	s_mov_b32 s47, s41
.Lstg3:
.Lw3t8:
	s_cbranch_execz .Lw3c8
.Lw3b8:
	s_cmp_eq_u32 s47, 0
	s_cbranch_scc1 .Lstg3d
	s_sleep 4
	s_sub_u32 s47, s47, 1
	s_branch .Lstg3

.Lw3b9:
	v_readfirstlane_b32 s10, v0
	s_waitcnt lgkmcnt(0)
	s_mul_i32 s12, s10, s3
	s_add_i32 s12, s12, s2
	s_cmpk_gt_i32 s12, 0x1869
	s_mov_b64 s[10:11], -1
	s_cbranch_scc1 .LBB3_10
	ds_read_b128 v[28:31], v96
	ds_read_b128 v[24:27], v96 offset:16
	ds_read_b128 v[20:23], v96 offset:32
	ds_read_b128 v[16:19], v96 offset:48
	ds_read_b128 v[12:15], v96 offset:64
	ds_read_b128 v[8:11], v96 offset:80
	ds_read_b128 v[4:7], v96 offset:96
	ds_read_b128 v[0:3], v96 offset:112
	s_lshl_b32 s10, s12, 4
	s_ashr_i32 s11, s10, 31
	v_lshl_add_u64 v[78:79], s[10:11], 2, v[74:75]
	s_mov_b32 s11, 0
	s_mov_b64 s[22:23], -1
	s_branch .LBB3_18

.Lw3b10:
	v_mov_b32_e32 v48, v77
	ds_read_b128 v[32:35], v97
	ds_read_b128 v[36:39], v97 offset:64
	ds_read_b128 v[40:43], v97 offset:128
	ds_read_b128 v[44:47], v97 offset:192
	s_nop 0
	v_lshlrev_b32_e32 v48, 4, v48
	v_lshl_add_u32 v103, s11, 15, v48
	ds_read_b128 v[48:51], v103
	ds_read_b128 v[52:55], v103 offset:1024
	ds_read_b128 v[56:59], v103 offset:2048
	ds_read_b128 v[60:63], v103 offset:3072
	ds_read_b128 v[64:67], v103 offset:4096
	ds_read_b128 v[68:71], v103 offset:5120
	ds_read_b128 v[104:107], v103 offset:6144
	ds_read_b128 v[108:111], v103 offset:7168
	s_waitcnt lgkmcnt(7)
	v_mfma_f32_16x16x32_f16 v[28:31], v[48:51], v[32:35], v[28:31]

.Lw3b11:
	s_waitcnt lgkmcnt(6)
	v_mfma_f32_16x16x32_f16 v[24:27], v[52:55], v[32:35], v[24:27]
	s_waitcnt lgkmcnt(5)
	v_mfma_f32_16x16x32_f16 v[20:23], v[56:59], v[32:35], v[20:23]
	s_waitcnt lgkmcnt(4)
	v_mfma_f32_16x16x32_f16 v[16:19], v[60:63], v[32:35], v[16:19]
	ds_read_b128 v[48:51], v103 offset:8192
	ds_read_b128 v[52:55], v103 offset:9216
	ds_read_b128 v[56:59], v103 offset:10240
	ds_read_b128 v[60:63], v103 offset:11264
	s_waitcnt lgkmcnt(7)
	v_mfma_f32_16x16x32_f16 v[12:15], v[64:67], v[32:35], v[12:15]
	s_waitcnt lgkmcnt(6)
	v_mfma_f32_16x16x32_f16 v[8:11], v[68:71], v[32:35], v[8:11]
	s_waitcnt lgkmcnt(5)
	v_mfma_f32_16x16x32_f16 v[4:7], v[104:107], v[32:35], v[4:7]
	s_waitcnt lgkmcnt(4)
	v_mfma_f32_16x16x32_f16 v[0:3], v[108:111], v[32:35], v[0:3]
	ds_read_b128 v[32:35], v103 offset:12288

.Lw3b12:
	ds_read_b128 v[64:67], v103 offset:13312
	ds_read_b128 v[68:71], v103 offset:14336
	ds_read_b128 v[104:107], v103 offset:15360
	s_waitcnt lgkmcnt(7)
	v_mfma_f32_16x16x32_f16 v[28:31], v[48:51], v[36:39], v[28:31]
	s_waitcnt lgkmcnt(6)
	v_mfma_f32_16x16x32_f16 v[24:27], v[52:55], v[36:39], v[24:27]
	s_waitcnt lgkmcnt(5)
	v_mfma_f32_16x16x32_f16 v[20:23], v[56:59], v[36:39], v[20:23]
	s_waitcnt lgkmcnt(4)
	v_mfma_f32_16x16x32_f16 v[16:19], v[60:63], v[36:39], v[16:19]
	ds_read_b128 v[48:51], v103 offset:16384
	ds_read_b128 v[52:55], v103 offset:17408
	ds_read_b128 v[56:59], v103 offset:18432
	ds_read_b128 v[60:63], v103 offset:19456
	s_waitcnt lgkmcnt(7)
	v_mfma_f32_16x16x32_f16 v[12:15], v[32:35], v[36:39], v[12:15]
	s_waitcnt lgkmcnt(6)

.Lw3b13:
	v_mfma_f32_16x16x32_f16 v[8:11], v[64:67], v[36:39], v[8:11]
	s_waitcnt lgkmcnt(5)
	v_mfma_f32_16x16x32_f16 v[4:7], v[68:71], v[36:39], v[4:7]
	s_waitcnt lgkmcnt(4)
	v_mfma_f32_16x16x32_f16 v[0:3], v[104:107], v[36:39], v[0:3]
	ds_read_b128 v[32:35], v103 offset:20480
	ds_read_b128 v[36:39], v103 offset:21504
	ds_read_b128 v[64:67], v103 offset:22528
	ds_read_b128 v[68:71], v103 offset:23552
	s_waitcnt lgkmcnt(7)
	v_mfma_f32_16x16x32_f16 v[28:31], v[48:51], v[40:43], v[28:31]
	s_waitcnt lgkmcnt(6)
	v_mfma_f32_16x16x32_f16 v[24:27], v[52:55], v[40:43], v[24:27]
	s_waitcnt lgkmcnt(5)
	v_mfma_f32_16x16x32_f16 v[20:23], v[56:59], v[40:43], v[20:23]
	s_waitcnt lgkmcnt(4)
	v_mfma_f32_16x16x32_f16 v[16:19], v[60:63], v[40:43], v[16:19]
	ds_read_b128 v[48:51], v103 offset:24576
	ds_read_b128 v[52:55], v103 offset:25600

.Lw3b14:
	ds_read_b128 v[56:59], v103 offset:26624
	ds_read_b128 v[60:63], v103 offset:27648
	s_waitcnt lgkmcnt(7)
	v_mfma_f32_16x16x32_f16 v[12:15], v[32:35], v[40:43], v[12:15]
	s_waitcnt lgkmcnt(6)
	v_mfma_f32_16x16x32_f16 v[8:11], v[36:39], v[40:43], v[8:11]
	s_waitcnt lgkmcnt(5)
	v_mfma_f32_16x16x32_f16 v[4:7], v[64:67], v[40:43], v[4:7]
	s_waitcnt lgkmcnt(4)
	v_mfma_f32_16x16x32_f16 v[0:3], v[68:71], v[40:43], v[0:3]
	ds_read_b128 v[32:35], v103 offset:28672
	ds_read_b128 v[36:39], v103 offset:29696
	ds_read_b128 v[40:43], v103 offset:30720
	ds_read_b128 v[64:67], v103 offset:31744
	s_waitcnt lgkmcnt(7)
	v_mfma_f32_16x16x32_f16 v[28:31], v[48:51], v[44:47], v[28:31]
	s_waitcnt lgkmcnt(6)
	v_mfma_f32_16x16x32_f16 v[24:27], v[52:55], v[44:47], v[24:27]

.Lw3b15:
	s_waitcnt lgkmcnt(5)
	v_mfma_f32_16x16x32_f16 v[20:23], v[56:59], v[44:47], v[20:23]
	s_waitcnt lgkmcnt(4)
	v_mfma_f32_16x16x32_f16 v[16:19], v[60:63], v[44:47], v[16:19]
	s_waitcnt lgkmcnt(3)
	v_mfma_f32_16x16x32_f16 v[12:15], v[32:35], v[44:47], v[12:15]
	s_waitcnt lgkmcnt(2)
	v_mfma_f32_16x16x32_f16 v[8:11], v[36:39], v[44:47], v[8:11]
	s_waitcnt lgkmcnt(1)
	v_mfma_f32_16x16x32_f16 v[4:7], v[40:43], v[44:47], v[4:7]
	s_waitcnt lgkmcnt(0)
	v_mfma_f32_16x16x32_f16 v[0:3], v[64:67], v[44:47], v[0:3]
	s_mov_b32 s11, 1
	s_mov_b64 s[22:23], 0
	s_and_b64 vcc, exec, s[14:15]
	s_cbranch_vccnz .LBB3_94

.Lw3b16:
	s_mov_b32 s15, s13
	s_mul_i32 s12, s11, 0xc3500
	s_lshl_b64 s[20:21], s[12:13], 2
	s_mov_b32 s12, s13
	v_mov_b64_e32 v[34:35], s[14:15]
	v_mov_b64_e32 v[32:33], s[12:13]
	s_add_u32 s20, s18, s20
	ds_write_b128 v83, v[32:35]
	ds_write_b128 v83, v[32:35] offset:16
	ds_write_b128 v83, v[32:35] offset:32
	ds_write_b128 v83, v[32:35] offset:48
	s_addc_u32 s21, s19, s21
	v_mov_b32_e32 v116, 0x3f86a0
	s_waitcnt vmcnt(1)
	v_add_u32_e32 v32, v113, v80
	s_waitcnt vmcnt(0)
	v_cmp_lt_i32_e32 vcc, v32, v103
	s_and_saveexec_b64 s[14:15], vcc
	s_cbranch_execz .LBB3_20
	v_ashrrev_i32_e32 v33, 31, v32
	v_lshl_add_u64 v[32:33], v[32:33], 2, s[20:21]
	global_load_dword v116, v[32:33], off

.Lw3b17:
	v_mov_b32_e32 v56, 0
	s_xor_b64 s[14:15], s[22:23], -1
	v_mov_b32_e32 v115, 31
	v_mov_b32_e32 v57, v56
	v_mov_b32_e32 v58, v56
	v_mov_b32_e32 v59, v56
	v_mov_b32_e32 v60, v56
	v_mov_b32_e32 v61, v56
	v_mov_b32_e32 v62, v56
	v_mov_b32_e32 v63, v56
	s_branch .LBB3_22

.LBB3_22:
	s_nop 2
	v_mov_b32_e32 v104, v63
	v_mov_b32_e32 v106, v62
	v_mov_b32_e32 v105, v61
	v_mov_b32_e32 v108, v60
	v_mov_b32_e32 v109, v59
	v_mov_b32_e32 v111, v58
	v_mov_b32_e32 v110, v57
	v_mov_b32_e32 v112, v56
	v_mov_b32_e32 v107, v115
	v_cmp_lt_i32_e32 vcc, v113, v103
	s_cbranch_vccz .LBB3_21
	v_or_b32_e32 v32, 4, v82
	s_waitcnt vmcnt(0)
	ds_bpermute_b32 v66, v82, v116
	ds_bpermute_b32 v123, v32, v116
.Lw3t18:
	s_cbranch_execz .Lw3c18
.Lw3b18:
	v_or_b32_e32 v32, 8, v82
	v_or_b32_e32 v34, 12, v82
	ds_bpermute_b32 v122, v32, v116
	ds_bpermute_b32 v121, v34, v116
	v_or_b32_e32 v34, 16, v82
	ds_bpermute_b32 v120, v34, v116
	v_or_b32_e32 v34, 20, v82
	ds_bpermute_b32 v119, v34, v116
	s_waitcnt lgkmcnt(5)
	v_lshlrev_b32_e32 v32, 8, v66
	s_waitcnt lgkmcnt(4)
	v_lshlrev_b32_e32 v33, 8, v123
	v_and_or_b32 v32, v32, s27, v81
	v_and_or_b32 v33, v33, s27, v81
	ds_bpermute_b32 v118, v85, v116
	ds_bpermute_b32 v117, v86, v116
	global_load_dwordx4 v[60:63], v32, s[8:9]
	global_load_dwordx4 v[56:59], v33, s[8:9]
	s_waitcnt lgkmcnt(5)
	v_lshlrev_b32_e32 v32, 8, v122

.Lw3b19:
	s_waitcnt lgkmcnt(4)
	v_lshlrev_b32_e32 v33, 8, v121
	v_and_or_b32 v32, v32, s27, v81
	v_and_or_b32 v33, v33, s27, v81
	global_load_dwordx4 v[52:55], v32, s[8:9]
	global_load_dwordx4 v[48:51], v33, s[8:9]
	s_waitcnt lgkmcnt(3)
	v_lshlrev_b32_e32 v32, 8, v120
	s_waitcnt lgkmcnt(2)
	v_lshlrev_b32_e32 v33, 8, v119
	v_and_or_b32 v32, v32, s27, v81
	v_and_or_b32 v33, v33, s27, v81
	global_load_dwordx4 v[44:47], v32, s[8:9]
	global_load_dwordx4 v[40:43], v33, s[8:9]
	s_waitcnt lgkmcnt(1)
	v_lshlrev_b32_e32 v32, 8, v118
	s_waitcnt lgkmcnt(0)
	v_lshlrev_b32_e32 v33, 8, v117
	v_and_or_b32 v32, v32, s27, v81
	v_and_or_b32 v33, v33, s27, v81
	global_load_dwordx4 v[36:39], v32, s[8:9]

.Lw3b21:
	s_and_saveexec_b64 s[22:23], s[24:25]
	s_cbranch_execz .LBB3_29
	v_cmp_gt_i32_e32 vcc, 16, v107
	s_and_saveexec_b64 s[24:25], vcc
	s_cbranch_execz .LBB3_28
	v_cvt_pk_f16_f32 v67, v111, v109
	v_cvt_pk_f16_f32 v66, v112, v110
	v_cvt_pk_f16_f32 v65, v106, v104
	v_cvt_pk_f16_f32 v64, v108, v105
	v_mad_u64_u32 v[68:69], s[30:31], v107, s26, v[76:77]
	ds_write_b128 v68, v[64:67]

.LBB3_29:
	s_or_b64 exec, exec, s[22:23]
	v_ashrrev_i32_e32 v123, 17, v123
	s_waitcnt vmcnt(7)
	v_mfma_f32_16x16x16_f16 v[64:67], v[72:73], v[60:61], v[64:67]
.Lw3t22:
	s_cbranch_execz .Lw3c22
.Lw3b22:
	v_cmp_ne_u32_e32 vcc, v123, v115
	s_cmp_lg_u64 vcc, 0
	s_cselect_b64 s[22:23], -1, 0
	v_mfma_f32_16x16x16_f16 v[60:63], v[72:73], v[62:63], v[68:71]
	s_and_b64 s[24:25], s[22:23], vcc
	s_and_saveexec_b64 s[22:23], s[24:25]
	s_cbranch_execz .LBB3_33
	v_cmp_gt_i32_e32 vcc, 16, v115
	s_and_saveexec_b64 s[24:25], vcc
	s_cbranch_execz .LBB3_32
	s_nop 1
	v_cvt_pk_f16_f32 v63, v62, v63
	v_cvt_pk_f16_f32 v62, v60, v61
	v_cvt_pk_f16_f32 v61, v66, v67
	v_cvt_pk_f16_f32 v60, v64, v65
	v_mad_u64_u32 v[64:65], s[30:31], v115, s26, v[76:77]
	ds_write_b128 v64, v[60:63]
.LBB3_32:
	s_or_b64 exec, exec, s[24:25]
	s_nop 0
	v_mov_b32_e32 v60, 0
	v_mov_b32_e32 v115, v123
	v_mov_b32_e32 v61, v60
	v_mov_b32_e32 v62, v60
.Lw3t23:
	s_cbranch_execz .Lw3c23

.LBB3_33:
	s_or_b64 exec, exec, s[22:23]
	v_ashrrev_i32_e32 v68, 17, v122
	s_waitcnt vmcnt(6)
	v_mfma_f32_16x16x16_f16 v[64:67], v[72:73], v[56:57], v[64:67]
	v_cmp_ne_u32_e32 vcc, v68, v115
	s_cmp_lg_u64 vcc, 0
	s_cselect_b64 s[22:23], -1, 0
	v_mfma_f32_16x16x16_f16 v[56:59], v[72:73], v[58:59], v[60:63]
	s_and_b64 s[24:25], s[22:23], vcc
	s_and_saveexec_b64 s[22:23], s[24:25]
	s_cbranch_execz .LBB3_37
	v_cmp_gt_i32_e32 vcc, 16, v115
	s_and_saveexec_b64 s[24:25], vcc
	s_cbranch_execz .LBB3_36
	s_nop 1
	v_cvt_pk_f16_f32 v59, v58, v59
	v_cvt_pk_f16_f32 v58, v56, v57
	v_cvt_pk_f16_f32 v57, v66, v67
	v_cvt_pk_f16_f32 v56, v64, v65
	v_mad_u64_u32 v[60:61], s[30:31], v115, s26, v[76:77]

.LBB3_37:
	s_or_b64 exec, exec, s[22:23]
	v_ashrrev_i32_e32 v68, 17, v121
	s_waitcnt vmcnt(5)
	v_mfma_f32_16x16x16_f16 v[60:63], v[72:73], v[52:53], v[64:67]
	v_cmp_ne_u32_e32 vcc, v68, v115
	s_cmp_lg_u64 vcc, 0
	s_cselect_b64 s[22:23], -1, 0
	v_mfma_f32_16x16x16_f16 v[52:55], v[72:73], v[54:55], v[56:59]
	s_and_b64 s[24:25], s[22:23], vcc
	s_and_saveexec_b64 s[22:23], s[24:25]
	s_cbranch_execz .LBB3_41
	v_cmp_gt_i32_e32 vcc, 16, v115
	s_and_saveexec_b64 s[24:25], vcc
	s_cbranch_execz .LBB3_40
	s_nop 1
.Lw3t25:
	s_cbranch_execz .Lw3c25

.Lw3b26:
	v_mfma_f32_16x16x16_f16 v[48:51], v[72:73], v[50:51], v[52:55]
	s_and_b64 s[24:25], s[22:23], vcc
	s_and_saveexec_b64 s[22:23], s[24:25]
	s_cbranch_execz .LBB3_45
	v_cmp_gt_i32_e32 vcc, 16, v115
	s_and_saveexec_b64 s[24:25], vcc
	s_cbranch_execz .LBB3_44
	s_nop 1
	v_cvt_pk_f16_f32 v51, v50, v51
	v_cvt_pk_f16_f32 v50, v48, v49
	v_cvt_pk_f16_f32 v49, v58, v59
	v_cvt_pk_f16_f32 v48, v56, v57
	v_mad_u64_u32 v[52:53], s[30:31], v115, s26, v[76:77]
	ds_write_b128 v52, v[48:51]
.LBB3_44:
	s_or_b64 exec, exec, s[24:25]
	s_nop 0
	v_mov_b32_e32 v48, 0
	v_mov_b32_e32 v115, v64
	v_mov_b32_e32 v49, v48
	v_mov_b32_e32 v50, v48
	v_mov_b32_e32 v51, v48
	v_mov_b32_e32 v56, v48
	v_mov_b32_e32 v57, v48
	v_mov_b32_e32 v58, v48
.Lw3t27:
	s_cbranch_execz .Lw3c27

.LBB3_49:
	s_or_b64 exec, exec, s[22:23]
	v_ashrrev_i32_e32 v56, 17, v118
	s_waitcnt vmcnt(2)
	v_mfma_f32_16x16x16_f16 v[48:51], v[72:73], v[40:41], v[52:55]
	v_cmp_ne_u32_e32 vcc, v56, v115
	s_cmp_lg_u64 vcc, 0
	s_cselect_b64 s[22:23], -1, 0
	v_mfma_f32_16x16x16_f16 v[40:43], v[72:73], v[42:43], v[44:47]
	s_and_b64 s[24:25], s[22:23], vcc
	s_and_saveexec_b64 s[22:23], s[24:25]
	s_cbranch_execz .LBB3_53
	v_cmp_gt_i32_e32 vcc, 16, v115
	s_and_saveexec_b64 s[24:25], vcc
	s_cbranch_execz .LBB3_52
	s_nop 1
	v_cvt_pk_f16_f32 v43, v42, v43
	v_cvt_pk_f16_f32 v42, v40, v41
.Lw3t29:
	s_cbranch_execz .Lw3c29

.LBB3_52:
	s_or_b64 exec, exec, s[24:25]
	s_nop 0
	v_mov_b32_e32 v40, 0
	v_mov_b32_e32 v115, v56
	v_mov_b32_e32 v41, v40
	v_mov_b32_e32 v42, v40
	v_mov_b32_e32 v43, v40
	v_mov_b32_e32 v48, v40
	v_mov_b32_e32 v49, v40
	v_mov_b32_e32 v50, v40
	v_mov_b32_e32 v51, v40
.LBB3_53:
	s_or_b64 exec, exec, s[22:23]
	v_ashrrev_i32_e32 v52, 17, v117
	s_waitcnt vmcnt(1)
	v_mfma_f32_16x16x16_f16 v[44:47], v[72:73], v[36:37], v[48:51]
	v_cmp_ne_u32_e32 vcc, v52, v115
	s_cmp_lg_u64 vcc, 0
	s_cselect_b64 s[22:23], -1, 0
	v_mfma_f32_16x16x16_f16 v[36:39], v[72:73], v[38:39], v[40:43]
	s_and_b64 s[24:25], s[22:23], vcc
	s_and_saveexec_b64 s[22:23], s[24:25]
.Lw3t30:
	s_cbranch_execz .Lw3c30
.Lw3b30:
	s_cbranch_execz .LBB3_57
	v_cmp_gt_i32_e32 vcc, 16, v115
	s_and_saveexec_b64 s[24:25], vcc
	s_cbranch_execz .LBB3_56
	s_nop 1
	v_cvt_pk_f16_f32 v39, v38, v39
	v_cvt_pk_f16_f32 v38, v36, v37
	v_cvt_pk_f16_f32 v37, v46, v47
	v_cvt_pk_f16_f32 v36, v44, v45
	v_mad_u64_u32 v[40:41], s[30:31], v115, s26, v[76:77]
	ds_write_b128 v40, v[36:39]

.Lw3b31:
	v_add_u32_e32 v32, 8, v113
	v_cmp_lt_i32_e32 vcc, v32, v103
	v_mfma_f32_16x16x16_f16 v[56:59], v[72:73], v[34:35], v[36:39]
	s_cbranch_vccz .LBB3_91
	ds_bpermute_b32 v123, v87, v116
	ds_bpermute_b32 v122, v88, v116
	ds_bpermute_b32 v121, v89, v116
	ds_bpermute_b32 v120, v90, v116
	ds_bpermute_b32 v119, v91, v116
	ds_bpermute_b32 v118, v92, v116
	s_waitcnt lgkmcnt(5)
	v_lshlrev_b32_e32 v32, 8, v123
	s_waitcnt lgkmcnt(4)
	v_lshlrev_b32_e32 v33, 8, v122
	v_and_or_b32 v32, v32, s27, v81
	v_and_or_b32 v33, v33, s27, v81
	ds_bpermute_b32 v117, v93, v116
	ds_bpermute_b32 v116, v94, v116
	global_load_dwordx4 v[68:71], v32, s[8:9]

.Lw3b32:
	global_load_dwordx4 v[64:67], v33, s[8:9]
	s_waitcnt lgkmcnt(5)
	v_lshlrev_b32_e32 v32, 8, v121
	s_waitcnt lgkmcnt(4)
	v_lshlrev_b32_e32 v33, 8, v120
	v_and_or_b32 v32, v32, s27, v81
	v_and_or_b32 v33, v33, s27, v81
	global_load_dwordx4 v[52:55], v32, s[8:9]
	global_load_dwordx4 v[48:51], v33, s[8:9]
	s_waitcnt lgkmcnt(3)
	v_lshlrev_b32_e32 v32, 8, v119
	s_waitcnt lgkmcnt(2)
	v_lshlrev_b32_e32 v33, 8, v118
	v_and_or_b32 v32, v32, s27, v81
	v_and_or_b32 v33, v33, s27, v81
	global_load_dwordx4 v[44:47], v32, s[8:9]
	global_load_dwordx4 v[40:43], v33, s[8:9]
	s_waitcnt lgkmcnt(1)
	v_lshlrev_b32_e32 v32, 8, v117
	s_waitcnt lgkmcnt(0)
	v_lshlrev_b32_e32 v33, 8, v116

.Lw3b33:
	v_and_or_b32 v32, v32, s27, v81
	v_and_or_b32 v33, v33, s27, v81
	global_load_dwordx4 v[36:39], v32, s[8:9]
	s_nop 0
	global_load_dwordx4 v[32:35], v33, s[8:9]
	v_ashrrev_i32_e32 v123, 17, v123
	v_cmp_ne_u32_e32 vcc, v123, v115
	s_cmp_lg_u64 vcc, 0
	s_cselect_b64 s[22:23], -1, 0
	s_and_b64 s[24:25], s[22:23], vcc
	s_and_saveexec_b64 s[22:23], s[24:25]
	s_cbranch_execz .LBB3_62
	v_cmp_gt_i32_e32 vcc, 16, v115
	s_and_saveexec_b64 s[24:25], vcc
	s_cbranch_execz .LBB3_61
	v_cvt_pk_f16_f32 v59, v58, v59
	v_cvt_pk_f16_f32 v58, v56, v57
	v_cvt_pk_f16_f32 v57, v62, v63
	v_cvt_pk_f16_f32 v56, v60, v61
	v_mad_u64_u32 v[60:61], s[30:31], v115, s26, v[76:77]
	ds_write_b128 v60, v[56:59]

.Lw3b34:
	s_or_b64 exec, exec, s[24:25]
	v_mov_b32_e32 v56, 0
	v_mov_b32_e32 v115, v123
	v_mov_b32_e32 v57, v56
	v_mov_b32_e32 v58, v56
	v_mov_b32_e32 v59, v56
	v_mov_b32_e32 v60, v56
	v_mov_b32_e32 v61, v56
	v_mov_b32_e32 v62, v56
	v_mov_b32_e32 v63, v56
.LBB3_62:
	s_or_b64 exec, exec, s[22:23]
	v_ashrrev_i32_e32 v122, 17, v122
	s_waitcnt vmcnt(7)
	v_mfma_f32_16x16x16_f16 v[60:63], v[72:73], v[68:69], v[60:63]
	v_cmp_ne_u32_e32 vcc, v122, v115
	s_cmp_lg_u64 vcc, 0
	s_cselect_b64 s[22:23], -1, 0
	v_mfma_f32_16x16x16_f16 v[56:59], v[72:73], v[70:71], v[56:59]
	s_and_b64 s[24:25], s[22:23], vcc
	s_and_saveexec_b64 s[22:23], s[24:25]
	s_cbranch_execz .LBB3_66
	v_cmp_gt_i32_e32 vcc, 16, v115
	s_and_saveexec_b64 s[24:25], vcc
	s_cbranch_execz .LBB3_65
	s_nop 1
	v_cvt_pk_f16_f32 v59, v58, v59
	v_cvt_pk_f16_f32 v58, v56, v57
.Lw3t35:
	s_cbranch_execz .Lw3c35

.Lw3b36:
	s_cbranch_execz .LBB3_70
	v_cmp_gt_i32_e32 vcc, 16, v115
	s_and_saveexec_b64 s[24:25], vcc
	s_cbranch_execz .LBB3_69
	s_nop 1
	v_cvt_pk_f16_f32 v59, v58, v59
	v_cvt_pk_f16_f32 v58, v56, v57
	v_cvt_pk_f16_f32 v57, v62, v63
	v_cvt_pk_f16_f32 v56, v60, v61
	v_mad_u64_u32 v[60:61], s[30:31], v115, s26, v[76:77]
	ds_write_b128 v60, v[56:59]

.LBB3_70:
	s_or_b64 exec, exec, s[22:23]
	v_ashrrev_i32_e32 v64, 17, v120
	s_waitcnt vmcnt(5)
.Lw3t37:
	s_cbranch_execz .Lw3c37
.Lw3b37:
	v_mfma_f32_16x16x16_f16 v[60:63], v[72:73], v[52:53], v[60:63]
	v_cmp_ne_u32_e32 vcc, v64, v115
	s_cmp_lg_u64 vcc, 0
	s_cselect_b64 s[22:23], -1, 0
	v_mfma_f32_16x16x16_f16 v[52:55], v[72:73], v[54:55], v[56:59]
	s_and_b64 s[24:25], s[22:23], vcc
	s_and_saveexec_b64 s[22:23], s[24:25]
	s_cbranch_execz .LBB3_74
	v_cmp_gt_i32_e32 vcc, 16, v115
	s_and_saveexec_b64 s[24:25], vcc
	s_cbranch_execz .LBB3_73
	s_nop 1
	v_cvt_pk_f16_f32 v55, v54, v55
	v_cvt_pk_f16_f32 v54, v52, v53
	v_cvt_pk_f16_f32 v53, v62, v63
	v_cvt_pk_f16_f32 v52, v60, v61
	v_mad_u64_u32 v[56:57], s[30:31], v115, s26, v[76:77]
	ds_write_b128 v56, v[52:55]
.LBB3_73:
	s_or_b64 exec, exec, s[24:25]
	s_nop 0
	v_mov_b32_e32 v52, 0
	v_mov_b32_e32 v115, v64
	v_mov_b32_e32 v53, v52
.Lw3t38:
	s_cbranch_execz .Lw3c38

.LBB3_74:
	s_or_b64 exec, exec, s[22:23]
	v_ashrrev_i32_e32 v64, 17, v119
	s_waitcnt vmcnt(4)
	v_mfma_f32_16x16x16_f16 v[56:59], v[72:73], v[48:49], v[60:63]
	v_cmp_ne_u32_e32 vcc, v64, v115
	s_cmp_lg_u64 vcc, 0
	s_cselect_b64 s[22:23], -1, 0
	v_mfma_f32_16x16x16_f16 v[48:51], v[72:73], v[50:51], v[52:55]
	s_and_b64 s[24:25], s[22:23], vcc
	s_and_saveexec_b64 s[22:23], s[24:25]
	s_cbranch_execz .LBB3_78
	v_cmp_gt_i32_e32 vcc, 16, v115
	s_and_saveexec_b64 s[24:25], vcc
	s_cbranch_execz .LBB3_77
	s_nop 1
	v_cvt_pk_f16_f32 v51, v50, v51
	v_cvt_pk_f16_f32 v50, v48, v49
	v_cvt_pk_f16_f32 v49, v58, v59
	v_cvt_pk_f16_f32 v48, v56, v57

.Lw3b39:
	v_mad_u64_u32 v[52:53], s[30:31], v115, s26, v[76:77]
	ds_write_b128 v52, v[48:51]
.LBB3_77:
	s_or_b64 exec, exec, s[24:25]
	s_nop 0
	v_mov_b32_e32 v48, 0
	v_mov_b32_e32 v115, v64
	v_mov_b32_e32 v49, v48
	v_mov_b32_e32 v50, v48
	v_mov_b32_e32 v51, v48
	v_mov_b32_e32 v56, v48
	v_mov_b32_e32 v57, v48
	v_mov_b32_e32 v58, v48
	v_mov_b32_e32 v59, v48
.LBB3_78:
	s_or_b64 exec, exec, s[22:23]
	v_ashrrev_i32_e32 v60, 17, v118
	s_waitcnt vmcnt(3)
	v_mfma_f32_16x16x16_f16 v[52:55], v[72:73], v[44:45], v[56:59]
	v_cmp_ne_u32_e32 vcc, v60, v115
	s_cmp_lg_u64 vcc, 0
	s_cselect_b64 s[22:23], -1, 0
	v_mfma_f32_16x16x16_f16 v[44:47], v[72:73], v[46:47], v[48:51]
	s_and_b64 s[24:25], s[22:23], vcc
	s_and_saveexec_b64 s[22:23], s[24:25]
	s_cbranch_execz .LBB3_82
	v_cmp_gt_i32_e32 vcc, 16, v115
	s_and_saveexec_b64 s[24:25], vcc
	s_cbranch_execz .LBB3_81
.Lw3t40:
	s_cbranch_execz .Lw3c40

.LBB3_82:
	s_or_b64 exec, exec, s[22:23]
	v_ashrrev_i32_e32 v56, 17, v117
	s_waitcnt vmcnt(2)
	v_mfma_f32_16x16x16_f16 v[48:51], v[72:73], v[40:41], v[52:55]
	v_cmp_ne_u32_e32 vcc, v56, v115
	s_cmp_lg_u64 vcc, 0
	s_cselect_b64 s[22:23], -1, 0
.Lw3t41:
	s_cbranch_execz .Lw3c41
.Lw3b41:
	v_mfma_f32_16x16x16_f16 v[40:43], v[72:73], v[42:43], v[44:47]
	s_and_b64 s[24:25], s[22:23], vcc
	s_and_saveexec_b64 s[22:23], s[24:25]
	s_cbranch_execz .LBB3_86
	v_cmp_gt_i32_e32 vcc, 16, v115
	s_and_saveexec_b64 s[24:25], vcc
	s_cbranch_execz .LBB3_85
	s_nop 1
	v_cvt_pk_f16_f32 v43, v42, v43
	v_cvt_pk_f16_f32 v42, v40, v41
	v_cvt_pk_f16_f32 v41, v50, v51
	v_cvt_pk_f16_f32 v40, v48, v49
	v_mad_u64_u32 v[44:45], s[30:31], v115, s26, v[76:77]
	ds_write_b128 v44, v[40:43]

.LBB3_92:
	v_cmp_gt_i32_e32 vcc, 16, v107
	s_and_saveexec_b64 s[20:21], vcc
	s_cbranch_execz .LBB3_17
	v_cvt_pk_f16_f32 v35, v111, v109
	v_cvt_pk_f16_f32 v34, v112, v110
	v_cvt_pk_f16_f32 v33, v106, v104
	v_cvt_pk_f16_f32 v32, v108, v105
.Lw3t44:
	s_cbranch_execz .Lw3c44
.Lw3b44:
	v_mad_u64_u32 v[36:37], s[22:23], v107, s26, v[76:77]
	ds_write_b128 v36, v[32:35]
	s_branch .LBB3_17
.LBB3_94:
	v_mov_b32_e32 v32, v28
	v_mov_b32_e32 v33, v24
	v_mov_b32_e32 v34, v29
	v_mov_b32_e32 v35, v25
	v_pk_add_f32 v[32:33], v[32:33], v[34:35]
	v_mov_b32_e32 v34, v30
	v_mov_b32_e32 v35, v26
	v_mov_b32_e32 v36, v31
	v_mov_b32_e32 v37, v27
	v_pk_add_f32 v[34:35], v[34:35], v[36:37]
	v_mov_b32_e32 v36, v20
	v_pk_add_f32 v[32:33], v[32:33], v[34:35]
	v_mov_b32_e32 v34, v21
	v_mov_b32_e32 v35, v22
	v_mov_b32_e32 v37, v23
	v_pk_add_f32 v[34:35], v[34:35], v[36:37]
	v_add_f32_e32 v32, 0, v32
	v_pk_add_f32 v[34:35], v[34:35], v[34:35] op_sel:[0,1] op_sel_hi:[1,0]
	v_add_f32_e32 v32, v32, v33
	v_add_f32_e32 v36, v16, v17

.Lw3b45:
	v_add_f32_e32 v38, v18, v19
	v_mov_b32_e32 v33, v12
	v_mov_b32_e32 v35, v13
	v_mov_b32_e32 v37, v14
	v_mov_b32_e32 v39, v15
	v_pk_add_f32 v[32:33], v[32:33], v[34:35]
	v_pk_add_f32 v[34:35], v[36:37], v[38:39]
	v_mov_b32_e32 v36, v8
	v_pk_add_f32 v[32:33], v[32:33], v[34:35]
	v_mov_b32_e32 v34, v9
	v_mov_b32_e32 v35, v10
	v_mov_b32_e32 v37, v11
	v_pk_add_f32 v[34:35], v[34:35], v[36:37]
	v_pk_add_f32 v[32:33], v[32:33], v[32:33] op_sel:[0,1] op_sel_hi:[1,0]
	v_pk_add_f32 v[34:35], v[34:35], v[34:35] op_sel:[0,1] op_sel_hi:[1,0]
	v_add_f32_e32 v36, v4, v5
	v_add_f32_e32 v38, v6, v7
	v_mov_b32_e32 v33, v0
	v_mov_b32_e32 v35, v1
	v_mov_b32_e32 v37, v2
	v_mov_b32_e32 v39, v3
	v_pk_add_f32 v[32:33], v[32:33], v[34:35]
	v_pk_add_f32 v[34:35], v[36:37], v[38:39]

.Lw3b46:
	s_nop 0
	v_pk_add_f32 v[32:33], v[32:33], v[34:35]
	v_and_b32_e32 v34, 64, v100
	v_add_f32_e32 v32, v32, v33
	v_xor_b32_e32 v33, 16, v100
	v_add_u32_e32 v34, 64, v34
	v_cmp_lt_i32_e32 vcc, v33, v34
	s_nop 1
	v_cndmask_b32_e32 v33, v100, v33, vcc
	v_lshlrev_b32_e32 v40, 2, v33
	ds_bpermute_b32 v33, v40, v32
	s_waitcnt lgkmcnt(0)
	v_add_f32_e32 v32, v32, v33
	v_xor_b32_e32 v33, 32, v100
	v_cmp_lt_i32_e32 vcc, v33, v34
	s_nop 1
	v_cndmask_b32_e32 v33, v100, v33, vcc
	v_lshlrev_b32_e32 v41, 2, v33
	ds_bpermute_b32 v33, v41, v32
	s_waitcnt lgkmcnt(0)
	v_add_f32_e32 v42, v32, v33
	v_fmamk_f32 v29, v42, 0xbc000000, v29
	v_fmamk_f32 v25, v42, 0xbc000000, v25
	v_fmamk_f32 v39, v42, 0xbc000000, v31
	v_fmamk_f32 v38, v42, 0xbc000000, v30

.Lw3b47:
	v_fmac_f32_e32 v28, 0xbc000000, v42
	v_fmamk_f32 v37, v42, 0xbc000000, v27
	v_fmac_f32_e32 v24, 0xbc000000, v42
	v_mov_b32_e32 v30, v29
	v_mov_b32_e32 v31, v25
	v_fmamk_f32 v36, v42, 0xbc000000, v26
	v_mov_b32_e32 v26, v28
	v_mov_b32_e32 v27, v24
	v_pk_mul_f32 v[30:31], v[30:31], v[30:31]
	v_mov_b32_e32 v32, v39
	v_mov_b32_e32 v33, v37
	v_pk_fma_f32 v[26:27], v[26:27], v[26:27], v[30:31]
	v_mov_b32_e32 v30, v38
	v_mov_b32_e32 v31, v36
	v_pk_mul_f32 v[32:33], v[32:33], v[32:33]
	v_fmamk_f32 v35, v42, 0xbc000000, v21
	v_pk_fma_f32 v[30:31], v[30:31], v[30:31], v[32:33]
	v_fmamk_f32 v34, v42, 0xbc000000, v20
	v_fmamk_f32 v23, v42, 0xbc000000, v23

.Lw3b48:
	v_fmac_f32_e32 v22, 0xbc000000, v42
	v_pk_add_f32 v[26:27], v[26:27], v[30:31]
	v_pk_mul_f32 v[20:21], v[22:23], v[22:23]
	v_pk_mul_f32 v[30:31], v[34:35], v[34:35]
	v_fmamk_f32 v13, v42, 0xbc000000, v13
	v_pk_mov_b32 v[32:33], v[30:31], v[20:21] op_sel:[1,0]
	v_mov_b32_e32 v31, v21
	v_pk_add_f32 v[20:21], v[32:33], v[30:31]
	v_fmac_f32_e32 v12, 0xbc000000, v42
	v_fmamk_f32 v33, v42, 0xbc000000, v19
	v_fmamk_f32 v32, v42, 0xbc000000, v18
	v_fmamk_f32 v19, v42, 0xbc000000, v15
	v_fmamk_f32 v18, v42, 0xbc000000, v14
	v_mul_f32_e32 v30, v12, v12
	v_mul_f32_e32 v31, v13, v13
	v_pk_add_f32 v[14:15], v[26:27], v[26:27] op_sel:[0,1] op_sel_hi:[1,0]
	v_pk_add_f32 v[20:21], v[20:21], v[20:21] op_sel:[0,1] op_sel_hi:[1,0]

.Lw3b49:
	v_fmamk_f32 v17, v42, 0xbc000000, v17
	v_mov_b32_e32 v15, v30
	v_mov_b32_e32 v21, v31
	v_fmac_f32_e32 v16, 0xbc000000, v42
	v_pk_add_f32 v[14:15], v[14:15], v[20:21]
	v_mul_f32_e32 v20, v17, v17
	v_mul_f32_e32 v26, v33, v33
	v_mul_f32_e32 v43, v18, v18
	v_mul_f32_e32 v44, v19, v19
	v_pk_fma_f32 v[20:21], v[16:17], v[16:17], v[20:21] op_sel_hi:[1,1,0]
	v_pk_fma_f32 v[26:27], v[32:33], v[32:33], v[26:27] op_sel_hi:[1,1,0]
	v_mov_b32_e32 v21, v43
	v_mov_b32_e32 v27, v44
	v_pk_add_f32 v[20:21], v[20:21], v[26:27]
	v_fmamk_f32 v11, v42, 0xbc000000, v11
	v_pk_add_f32 v[14:15], v[14:15], v[20:21]
	v_fmamk_f32 v21, v42, 0xbc000000, v9
	v_fmamk_f32 v20, v42, 0xbc000000, v8
	v_fmac_f32_e32 v10, 0xbc000000, v42
	v_pk_mul_f32 v[8:9], v[10:11], v[10:11]

.Lw3b50:
	v_pk_mul_f32 v[26:27], v[20:21], v[20:21]
	v_fmamk_f32 v1, v42, 0xbc000000, v1
	v_pk_mov_b32 v[30:31], v[26:27], v[8:9] op_sel:[1,0]
	v_mov_b32_e32 v27, v9
	v_pk_add_f32 v[8:9], v[30:31], v[26:27]
	v_fmac_f32_e32 v0, 0xbc000000, v42
	v_fmamk_f32 v27, v42, 0xbc000000, v7
	v_fmamk_f32 v26, v42, 0xbc000000, v6
	v_mul_f32_e32 v30, v0, v0
	v_mul_f32_e32 v31, v1, v1
	v_pk_add_f32 v[6:7], v[14:15], v[14:15] op_sel:[0,1] op_sel_hi:[1,0]
	v_pk_add_f32 v[8:9], v[8:9], v[8:9] op_sel:[0,1] op_sel_hi:[1,0]
	v_fmamk_f32 v5, v42, 0xbc000000, v5
	v_mov_b32_e32 v7, v30
	v_mov_b32_e32 v9, v31
	v_fmac_f32_e32 v4, 0xbc000000, v42
	v_fmamk_f32 v3, v42, 0xbc000000, v3
	v_fmamk_f32 v2, v42, 0xbc000000, v2

.Lw3b51:
	v_pk_add_f32 v[6:7], v[6:7], v[8:9]
	v_mul_f32_e32 v8, v5, v5
	v_mul_f32_e32 v14, v27, v27
	v_mul_f32_e32 v42, v2, v2
	v_mul_f32_e32 v43, v3, v3
	v_pk_fma_f32 v[8:9], v[4:5], v[4:5], v[8:9] op_sel_hi:[1,1,0]
	v_pk_fma_f32 v[14:15], v[26:27], v[26:27], v[14:15] op_sel_hi:[1,1,0]
	v_mov_b32_e32 v9, v42
	v_mov_b32_e32 v15, v43
	v_pk_add_f32 v[8:9], v[8:9], v[14:15]
	s_nop 0
	v_pk_add_f32 v[6:7], v[6:7], v[8:9]
	s_nop 0
	v_add_f32_e32 v6, v6, v7
	ds_bpermute_b32 v7, v40, v6
	s_waitcnt lgkmcnt(0)
	v_add_f32_e32 v6, v6, v7
	ds_bpermute_b32 v7, v41, v6
	s_waitcnt lgkmcnt(0)
	v_add_f32_e32 v6, v6, v7
	v_fmamk_f32 v6, v6, 0x3c000000, v98
	v_mul_f32_e32 v7, 0x4b800000, v6

.Lw3b52:
	v_cmp_gt_f32_e32 vcc, s28, v6
	s_nop 1
	v_cndmask_b32_e32 v6, v6, v7, vcc
	v_rsq_f32_e32 v14, v6
	ds_read_b128 v[6:9], v96 offset:512
	ds_read_b128 v[40:43], v96 offset:528
	ds_read_b128 v[44:47], v96 offset:1024
	ds_read_b128 v[48:51], v96 offset:1040
	v_mul_f32_e32 v15, 0x45800000, v14
	v_cndmask_b32_e32 v30, v14, v15, vcc
	v_pk_mul_f32 v[14:15], v[30:31], v[28:29] op_sel_hi:[0,1]
	s_waitcnt lgkmcnt(1)
	v_pk_fma_f32 v[6:7], v[6:7], v[14:15], v[44:45]
	v_pk_mul_f32 v[28:29], v[30:31], v[38:39] op_sel_hi:[0,1]
	v_pk_mul_f32 v[14:15], v[6:7], v[6:7]
	v_pk_fma_f32 v[8:9], v[8:9], v[28:29], v[46:47]
	v_fmamk_f32 v14, v14, 0xbdd2d3e8, v99
	v_fmamk_f32 v15, v15, 0xbdd2d3e8, v99

.Lw3b53:
	v_mul_f32_e32 v14, v6, v14
	v_mul_f32_e32 v15, v7, v15
	v_exp_f32_e32 v14, v14
	v_exp_f32_e32 v15, v15
	v_pk_mul_f32 v[28:29], v[8:9], v[8:9]
	v_add_f32_e32 v14, 1.0, v14
	v_add_f32_e32 v15, 1.0, v15
	v_rcp_f32_e32 v14, v14
	v_rcp_f32_e32 v15, v15
	v_fmamk_f32 v28, v28, 0xbdd2d3e8, v99
	v_mul_f32_e32 v28, v8, v28
	v_exp_f32_e32 v28, v28
	v_pk_mul_f32 v[6:7], v[6:7], v[14:15]
	v_fmamk_f32 v14, v29, 0xbdd2d3e8, v99
	v_mul_f32_e32 v14, v9, v14
	v_exp_f32_e32 v29, v14
	v_pk_mul_f32 v[14:15], v[30:31], v[24:25] op_sel_hi:[0,1]
	s_waitcnt lgkmcnt(0)
	v_pk_fma_f32 v[14:15], v[40:41], v[14:15], v[48:49]
	v_cvt_pk_f16_f32 v6, v6, v7
	v_pk_mul_f32 v[24:25], v[14:15], v[14:15]
	v_add_f32_e32 v7, 1.0, v28
	v_fmamk_f32 v24, v24, 0xbdd2d3e8, v99

.Lw3b54:
	v_mul_f32_e32 v24, v14, v24
	v_exp_f32_e32 v24, v24
	v_rcp_f32_e32 v28, v7
	v_add_f32_e32 v7, 1.0, v29
	v_rcp_f32_e32 v29, v7
	v_add_f32_e32 v7, 1.0, v24
	v_fmamk_f32 v24, v25, 0xbdd2d3e8, v99
	v_mul_f32_e32 v31, v15, v24
	v_pk_mul_f32 v[24:25], v[30:31], v[36:37] op_sel_hi:[0,1]
	v_pk_fma_f32 v[24:25], v[42:43], v[24:25], v[50:51]
	v_exp_f32_e32 v31, v31
	v_pk_mul_f32 v[36:37], v[24:25], v[24:25]
	v_rcp_f32_e32 v38, v7
	v_fmamk_f32 v36, v36, 0xbdd2d3e8, v99
	v_fmamk_f32 v37, v37, 0xbdd2d3e8, v99
	v_mul_f32_e32 v36, v24, v36
	v_mul_f32_e32 v37, v25, v37
	v_exp_f32_e32 v36, v36
	v_exp_f32_e32 v37, v37
	v_add_f32_e32 v7, 1.0, v31
	v_mov_b32_e32 v31, v84
	v_add_f32_e32 v36, 1.0, v36
	v_add_f32_e32 v37, 1.0, v37
	v_rcp_f32_e32 v36, v36

.Lw3b55:
	v_rcp_f32_e32 v37, v37
	v_rcp_f32_e32 v39, v7
	v_pk_mul_f32 v[8:9], v[8:9], v[28:29]
	v_pk_mul_f32 v[24:25], v[24:25], v[36:37]
	s_nop 0
	s_nop 0
	v_lshl_add_u32 v7, v31, 2, v101
	v_add_u32_e32 v52, 0x420, v7
	v_add_u32_e32 v46, 0x428, v7
	v_add_u32_e32 v50, 0x430, v7
	ds_read2_b32 v[36:37], v7 offset0:138 offset1:139
	ds_read2_b32 v[40:41], v7 offset0:142 offset1:143
	ds_read2_b32 v[42:43], v7 offset0:140 offset1:141
	ds_read2_b32 v[44:45], v7 offset0:136 offset1:137
	v_add_u32_e32 v7, 0x438, v7
	ds_read2_b32 v[46:47], v46 offset1:1
	ds_read2_b32 v[48:49], v7 offset1:1
	ds_read2_b32 v[50:51], v50 offset1:1

.Lw3b56:
	ds_read2_b32 v[52:53], v52 offset1:1
	v_cvt_pk_f16_f32 v7, v8, v9
	v_pk_mul_f32 v[8:9], v[14:15], v[38:39]
	s_nop 0
	v_cvt_pk_f16_f32 v8, v8, v9
	v_pk_mul_f32 v[14:15], v[30:31], v[34:35] op_sel_hi:[0,1]
	s_waitcnt lgkmcnt(0)
	v_pk_fma_f32 v[14:15], v[44:45], v[14:15], v[52:53]
	v_pk_mul_f32 v[22:23], v[30:31], v[22:23] op_sel_hi:[0,1]
	v_pk_mul_f32 v[28:29], v[14:15], v[14:15]
	v_pk_fma_f32 v[22:23], v[36:37], v[22:23], v[46:47]
	v_fmamk_f32 v9, v28, 0xbdd2d3e8, v99
	v_mul_f32_e32 v9, v14, v9
	v_fmamk_f32 v28, v29, 0xbdd2d3e8, v99
	v_exp_f32_e32 v9, v9
	v_mul_f32_e32 v28, v15, v28
	v_exp_f32_e32 v29, v28
	v_pk_mul_f32 v[34:35], v[22:23], v[22:23]

.Lw3b57:
	v_add_f32_e32 v9, 1.0, v9
	v_rcp_f32_e32 v28, v9
	v_add_f32_e32 v9, 1.0, v29
	v_rcp_f32_e32 v29, v9
	v_fmamk_f32 v9, v34, 0xbdd2d3e8, v99
	v_mul_f32_e32 v9, v22, v9
	v_exp_f32_e32 v34, v9
	v_cvt_pk_f16_f32 v9, v24, v25
	v_fmamk_f32 v24, v35, 0xbdd2d3e8, v99
	v_pk_mul_f32 v[16:17], v[30:31], v[16:17] op_sel_hi:[0,1]
	v_mul_f32_e32 v24, v23, v24
	v_pk_fma_f32 v[16:17], v[42:43], v[16:17], v[50:51]
	v_pk_mul_f32 v[14:15], v[14:15], v[28:29]
	v_exp_f32_e32 v29, v24
	v_pk_mul_f32 v[24:25], v[16:17], v[16:17]
	v_cvt_pk_f16_f32 v14, v14, v15
	v_fmamk_f32 v24, v24, 0xbdd2d3e8, v99
	v_mul_f32_e32 v24, v16, v24
	v_exp_f32_e32 v24, v24
	v_add_f32_e32 v15, 1.0, v34
	v_rcp_f32_e32 v28, v15
	v_add_f32_e32 v15, 1.0, v29

.Lw3b58:
	v_rcp_f32_e32 v29, v15
	v_add_f32_e32 v15, 1.0, v24
	v_fmamk_f32 v24, v25, 0xbdd2d3e8, v99
	v_mul_f32_e32 v34, v17, v24
	v_pk_mul_f32 v[24:25], v[30:31], v[32:33] op_sel_hi:[0,1]
	v_pk_fma_f32 v[24:25], v[40:41], v[24:25], v[48:49]
	v_exp_f32_e32 v35, v34
	v_pk_mul_f32 v[32:33], v[24:25], v[24:25]
	v_rcp_f32_e32 v34, v15
	v_fmamk_f32 v32, v32, 0xbdd2d3e8, v99
	v_fmamk_f32 v33, v33, 0xbdd2d3e8, v99
	v_mul_f32_e32 v32, v24, v32
	v_mul_f32_e32 v33, v25, v33
	v_exp_f32_e32 v32, v32
	v_exp_f32_e32 v33, v33
	v_add_f32_e32 v15, 1.0, v35
	v_rcp_f32_e32 v35, v15
	v_add_f32_e32 v32, 1.0, v32
	v_add_f32_e32 v33, 1.0, v33
	v_rcp_f32_e32 v32, v32
	v_rcp_f32_e32 v33, v33
	v_pk_mul_f32 v[22:23], v[22:23], v[28:29]
	v_pk_mul_f32 v[16:17], v[16:17], v[34:35]

.Lw3b59:
	v_pk_mul_f32 v[24:25], v[24:25], v[32:33]
	s_nop 0
	v_cvt_pk_f16_f32 v16, v16, v17
	v_lshl_add_u32 v15, v31, 2, v101
	v_add_u32_e32 v48, 0x440, v15
	v_add_u32_e32 v42, 0x448, v15
	v_add_u32_e32 v46, 0x450, v15
	ds_read2_b32 v[32:33], v15 offset0:146 offset1:147
	ds_read2_b32 v[36:37], v15 offset0:150 offset1:151
	ds_read2_b32 v[38:39], v15 offset0:148 offset1:149
	ds_read2_b32 v[40:41], v15 offset0:144 offset1:145
	v_add_u32_e32 v15, 0x458, v15
	ds_read2_b32 v[42:43], v42 offset1:1
	ds_read2_b32 v[44:45], v15 offset1:1
	ds_read2_b32 v[46:47], v46 offset1:1
	ds_read2_b32 v[48:49], v48 offset1:1

.Lw3b60:
	v_cvt_pk_f16_f32 v15, v22, v23
	v_pk_mul_f32 v[12:13], v[30:31], v[12:13] op_sel_hi:[0,1]
	s_waitcnt lgkmcnt(0)
	v_pk_fma_f32 v[12:13], v[40:41], v[12:13], v[48:49]
	v_pk_mul_f32 v[18:19], v[30:31], v[18:19] op_sel_hi:[0,1]
	v_pk_mul_f32 v[22:23], v[12:13], v[12:13]
	v_pk_fma_f32 v[28:29], v[32:33], v[18:19], v[42:43]
	v_fmamk_f32 v17, v22, 0xbdd2d3e8, v99
	v_mul_f32_e32 v17, v12, v17
	v_fmamk_f32 v22, v23, 0xbdd2d3e8, v99
	v_exp_f32_e32 v17, v17
	v_mul_f32_e32 v22, v13, v22
	v_exp_f32_e32 v23, v22
	v_pk_mul_f32 v[18:19], v[28:29], v[28:29]
	v_add_f32_e32 v17, 1.0, v17
	v_rcp_f32_e32 v22, v17
	v_add_f32_e32 v17, 1.0, v23
	v_rcp_f32_e32 v23, v17
	v_fmamk_f32 v17, v18, 0xbdd2d3e8, v99
	v_pk_mul_f32 v[10:11], v[30:31], v[10:11] op_sel_hi:[0,1]

.Lw3b61:
	v_mul_f32_e32 v17, v28, v17
	v_pk_mul_f32 v[12:13], v[12:13], v[22:23]
	v_pk_fma_f32 v[10:11], v[36:37], v[10:11], v[44:45]
	v_cvt_pk_f16_f32 v18, v12, v13
	v_fmamk_f32 v12, v19, 0xbdd2d3e8, v99
	v_mul_f32_e32 v12, v29, v12
	v_exp_f32_e32 v19, v12
	v_pk_mul_f32 v[12:13], v[30:31], v[20:21] op_sel_hi:[0,1]
	v_pk_fma_f32 v[12:13], v[38:39], v[12:13], v[46:47]
	v_exp_f32_e32 v32, v17
	v_pk_mul_f32 v[20:21], v[12:13], v[12:13]
	v_add_f32_e32 v19, 1.0, v19
	v_fmamk_f32 v20, v20, 0xbdd2d3e8, v99
	v_mul_f32_e32 v20, v12, v20
	v_exp_f32_e32 v20, v20
	v_rcp_f32_e32 v23, v19
	v_cvt_pk_f16_f32 v17, v24, v25
	v_add_f32_e32 v22, 1.0, v32
	v_add_f32_e32 v19, 1.0, v20
	v_fmamk_f32 v20, v21, 0xbdd2d3e8, v99
	v_mul_f32_e32 v24, v13, v20

.Lw3b62:
	v_pk_mul_f32 v[20:21], v[10:11], v[10:11]
	v_exp_f32_e32 v25, v24
	v_fmamk_f32 v20, v20, 0xbdd2d3e8, v99
	v_fmamk_f32 v21, v21, 0xbdd2d3e8, v99
	v_mul_f32_e32 v20, v10, v20
	v_mul_f32_e32 v21, v11, v21
	v_exp_f32_e32 v20, v20
	v_exp_f32_e32 v21, v21
	v_rcp_f32_e32 v24, v19
	v_add_f32_e32 v19, 1.0, v25
	v_add_f32_e32 v20, 1.0, v20
	v_add_f32_e32 v21, 1.0, v21
	v_rcp_f32_e32 v20, v20
	v_rcp_f32_e32 v21, v21
	v_rcp_f32_e32 v25, v19
	v_rcp_f32_e32 v22, v22
	v_pk_mul_f32 v[10:11], v[10:11], v[20:21]
	s_nop 0
	v_pk_mul_f32 v[12:13], v[12:13], v[24:25]
	v_lshl_add_u32 v19, v31, 2, v101
	v_add_u32_e32 v21, 0x468, v19
	ds_read2_b32 v[32:33], v19 offset0:154 offset1:155
	ds_read2_b32 v[34:35], v19 offset0:158 offset1:159

.Lw3b63:
	ds_read2_b32 v[36:37], v19 offset0:156 offset1:157
	ds_read2_b32 v[38:39], v19 offset0:152 offset1:153
	v_add_u32_e32 v20, 0x460, v19
	v_add_u32_e32 v31, 0x470, v19
	v_add_u32_e32 v19, 0x478, v19
	ds_read2_b32 v[40:41], v21 offset1:1
	ds_read2_b32 v[42:43], v19 offset1:1
	ds_read2_b32 v[44:45], v31 offset1:1
	ds_read2_b32 v[46:47], v20 offset1:1
	v_pk_mul_f32 v[20:21], v[28:29], v[22:23]
	s_nop 0
	v_cvt_pk_f16_f32 v19, v20, v21
	v_cvt_pk_f16_f32 v20, v12, v13
	v_pk_mul_f32 v[4:5], v[30:31], v[4:5] op_sel_hi:[0,1]
	s_waitcnt lgkmcnt(0)
	v_pk_fma_f32 v[4:5], v[38:39], v[4:5], v[46:47]

.Lw3b64:
	v_cvt_pk_f16_f32 v21, v10, v11
	v_pk_mul_f32 v[12:13], v[4:5], v[4:5]
	v_pk_mul_f32 v[10:11], v[30:31], v[26:27] op_sel_hi:[0,1]
	v_fmamk_f32 v12, v12, 0xbdd2d3e8, v99
	v_fmamk_f32 v13, v13, 0xbdd2d3e8, v99
	v_mul_f32_e32 v12, v4, v12
	v_mul_f32_e32 v13, v5, v13
	v_exp_f32_e32 v12, v12
	v_exp_f32_e32 v13, v13
	v_pk_fma_f32 v[10:11], v[32:33], v[10:11], v[40:41]
	v_pk_mul_f32 v[0:1], v[30:31], v[0:1] op_sel_hi:[0,1]
	v_add_f32_e32 v12, 1.0, v12
	v_add_f32_e32 v13, 1.0, v13
	v_rcp_f32_e32 v12, v12
	v_rcp_f32_e32 v13, v13
	v_pk_fma_f32 v[0:1], v[36:37], v[0:1], v[44:45]
	v_pk_mul_f32 v[2:3], v[30:31], v[2:3] op_sel_hi:[0,1]
	v_pk_fma_f32 v[2:3], v[34:35], v[2:3], v[42:43]
	v_pk_mul_f32 v[4:5], v[4:5], v[12:13]
	v_pk_mul_f32 v[12:13], v[10:11], v[10:11]

.Lw3b65:
	v_cvt_pk_f16_f32 v24, v4, v5
	v_fmamk_f32 v12, v12, 0xbdd2d3e8, v99
	v_fmamk_f32 v13, v13, 0xbdd2d3e8, v99
	v_mul_f32_e32 v12, v10, v12
	v_mul_f32_e32 v13, v11, v13
	v_exp_f32_e32 v12, v12
	v_exp_f32_e32 v13, v13
	v_add_f32_e32 v4, 1.0, v12
	v_add_f32_e32 v5, 1.0, v13
	v_pk_mul_f32 v[12:13], v[0:1], v[0:1]
	v_rcp_f32_e32 v4, v4
	v_fmamk_f32 v12, v12, 0xbdd2d3e8, v99
	v_fmamk_f32 v13, v13, 0xbdd2d3e8, v99
	v_mul_f32_e32 v12, v0, v12
	v_mul_f32_e32 v13, v1, v13
	v_rcp_f32_e32 v5, v5
	v_exp_f32_e32 v12, v12
	v_exp_f32_e32 v13, v13
	v_pk_mul_f32 v[4:5], v[10:11], v[4:5]
	v_add_f32_e32 v10, 1.0, v12
	v_add_f32_e32 v11, 1.0, v13
	v_pk_mul_f32 v[12:13], v[2:3], v[2:3]

.Lw3b66:
	v_rcp_f32_e32 v10, v10
	v_fmamk_f32 v12, v12, 0xbdd2d3e8, v99
	v_fmamk_f32 v13, v13, 0xbdd2d3e8, v99
	v_mul_f32_e32 v12, v2, v12
	v_mul_f32_e32 v13, v3, v13
	v_exp_f32_e32 v12, v12
	v_exp_f32_e32 v13, v13
	v_rcp_f32_e32 v11, v11
	v_cvt_pk_f16_f32 v25, v4, v5
	v_add_f32_e32 v12, 1.0, v12
	v_add_f32_e32 v13, 1.0, v13
	v_rcp_f32_e32 v12, v12
	v_rcp_f32_e32 v13, v13
	v_pk_mul_f32 v[0:1], v[0:1], v[10:11]
	s_nop 0
	v_cvt_pk_f16_f32 v26, v0, v1
	v_pk_mul_f32 v[0:1], v[2:3], v[12:13]
	s_nop 0
	v_cvt_pk_f16_f32 v27, v0, v1
	ds_read_b128 v[0:3], v96 offset:1536
	ds_read_b128 v[10:13], v96 offset:1552
	ds_read_b128 v[30:33], v96 offset:1568

.Lw3b67:
	ds_read_b128 v[34:37], v96 offset:1584
	ds_read_b128 v[38:41], v96 offset:1600
	ds_read_b128 v[42:45], v96 offset:1616
	ds_read_b128 v[46:49], v96 offset:1632
	ds_read_b128 v[50:53], v96 offset:1648
	v_mov_b32_e32 v4, v77
	s_nop 0
	v_lshl_add_u32 v28, v4, 4, v102
	ds_read_b128 v[54:57], v28
	ds_read_b128 v[58:61], v28 offset:1024
	ds_read_b128 v[62:65], v28 offset:2048
	ds_read_b128 v[66:69], v28 offset:3072
	ds_read_b128 v[104:107], v28 offset:4096
	ds_read_b128 v[108:111], v28 offset:5120
	ds_read_b128 v[112:115], v28 offset:6144
	ds_read_b128 v[116:119], v28 offset:7168

.Lw3b68:
	s_waitcnt lgkmcnt(7)
	v_mfma_f32_16x16x32_f16 v[0:3], v[54:57], v[6:9], v[0:3]
	s_waitcnt lgkmcnt(6)
	v_mfma_f32_16x16x32_f16 v[10:13], v[58:61], v[6:9], v[10:13]
	s_waitcnt lgkmcnt(5)
	v_mfma_f32_16x16x32_f16 v[30:33], v[62:65], v[6:9], v[30:33]
	s_waitcnt lgkmcnt(4)
	v_mfma_f32_16x16x32_f16 v[34:37], v[66:69], v[6:9], v[34:37]
	ds_read_b128 v[54:57], v28 offset:8192
	ds_read_b128 v[58:61], v28 offset:9216
	ds_read_b128 v[62:65], v28 offset:10240
	ds_read_b128 v[66:69], v28 offset:11264
	s_waitcnt lgkmcnt(7)
	v_mfma_f32_16x16x32_f16 v[38:41], v[104:107], v[6:9], v[38:41]
	s_waitcnt lgkmcnt(6)
	v_mfma_f32_16x16x32_f16 v[42:45], v[108:111], v[6:9], v[42:45]
	s_waitcnt lgkmcnt(5)
	v_mfma_f32_16x16x32_f16 v[46:49], v[112:115], v[6:9], v[46:49]
	s_waitcnt lgkmcnt(4)
	v_mfma_f32_16x16x32_f16 v[4:7], v[116:119], v[6:9], v[50:53]

.Lw3b69:
	s_nop 2
	ds_read_b128 v[50:53], v28 offset:12288
	ds_read_b128 v[104:107], v28 offset:13312
	ds_read_b128 v[108:111], v28 offset:14336
	ds_read_b128 v[112:115], v28 offset:15360
	s_waitcnt lgkmcnt(7)
	v_mfma_f32_16x16x32_f16 v[0:3], v[54:57], v[14:17], v[0:3]
	s_waitcnt lgkmcnt(6)
	v_mfma_f32_16x16x32_f16 v[8:11], v[58:61], v[14:17], v[10:13]
	s_waitcnt lgkmcnt(5)
	v_mfma_f32_16x16x32_f16 v[30:33], v[62:65], v[14:17], v[30:33]
	s_waitcnt lgkmcnt(4)
	v_mfma_f32_16x16x32_f16 v[34:37], v[66:69], v[14:17], v[34:37]
	ds_read_b128 v[54:57], v28 offset:16384
	ds_read_b128 v[58:61], v28 offset:17408
	ds_read_b128 v[62:65], v28 offset:18432
	ds_read_b128 v[66:69], v28 offset:19456
	s_waitcnt lgkmcnt(7)

.Lw3b70:
	v_mfma_f32_16x16x32_f16 v[38:41], v[50:53], v[14:17], v[38:41]
	s_waitcnt lgkmcnt(6)
	v_mfma_f32_16x16x32_f16 v[42:45], v[104:107], v[14:17], v[42:45]
	s_waitcnt lgkmcnt(5)
	v_mfma_f32_16x16x32_f16 v[46:49], v[108:111], v[14:17], v[46:49]
	s_waitcnt lgkmcnt(4)
	v_mfma_f32_16x16x32_f16 v[4:7], v[112:115], v[14:17], v[4:7]
	ds_read_b128 v[12:15], v28 offset:20480
	ds_read_b128 v[50:53], v28 offset:21504
	ds_read_b128 v[104:107], v28 offset:22528
	ds_read_b128 v[108:111], v28 offset:23552
	s_waitcnt lgkmcnt(7)
	v_mfma_f32_16x16x32_f16 v[0:3], v[54:57], v[18:21], v[0:3]
	s_waitcnt lgkmcnt(6)
	v_mfma_f32_16x16x32_f16 v[8:11], v[58:61], v[18:21], v[8:11]
	s_waitcnt lgkmcnt(5)
	v_mfma_f32_16x16x32_f16 v[30:33], v[62:65], v[18:21], v[30:33]
	s_waitcnt lgkmcnt(4)
	v_mfma_f32_16x16x32_f16 v[34:37], v[66:69], v[18:21], v[34:37]

.Lw3b71:
	ds_read_b128 v[54:57], v28 offset:24576
	ds_read_b128 v[58:61], v28 offset:25600
	ds_read_b128 v[62:65], v28 offset:26624
	ds_read_b128 v[66:69], v28 offset:27648
	s_waitcnt lgkmcnt(7)
	v_mfma_f32_16x16x32_f16 v[12:15], v[12:15], v[18:21], v[38:41]
	s_waitcnt lgkmcnt(6)
	v_mfma_f32_16x16x32_f16 v[38:41], v[50:53], v[18:21], v[42:45]
	s_waitcnt lgkmcnt(5)
	v_mfma_f32_16x16x32_f16 v[42:45], v[104:107], v[18:21], v[46:49]
	s_waitcnt lgkmcnt(4)
	v_mfma_f32_16x16x32_f16 v[46:49], v[108:111], v[18:21], v[4:7]
	s_nop 2
	ds_read_b128 v[4:7], v28 offset:28672
	ds_read_b128 v[50:53], v28 offset:29696
	ds_read_b128 v[104:107], v28 offset:30720
	ds_read_b128 v[108:111], v28 offset:31744
	s_waitcnt lgkmcnt(7)
	v_mfma_f32_16x16x32_f16 v[54:57], v[54:57], v[24:27], v[0:3]

.Lw3b72:
	s_waitcnt lgkmcnt(6)
	v_mfma_f32_16x16x32_f16 v[58:61], v[58:61], v[24:27], v[8:11]
	s_waitcnt lgkmcnt(5)
	v_mfma_f32_16x16x32_f16 v[20:23], v[62:65], v[24:27], v[30:33]
	s_waitcnt lgkmcnt(4)
	v_mfma_f32_16x16x32_f16 v[16:19], v[66:69], v[24:27], v[34:37]
	s_waitcnt lgkmcnt(0)
	v_mfma_f32_16x16x32_f16 v[0:3], v[108:111], v[24:27], v[46:49]
	v_mfma_f32_16x16x32_f16 v[12:15], v[4:7], v[24:27], v[12:15]
	v_mfma_f32_16x16x32_f16 v[8:11], v[50:53], v[24:27], v[38:41]
	v_mfma_f32_16x16x32_f16 v[4:7], v[104:107], v[24:27], v[42:45]
	v_mul_f32_e32 v24, v54, v54
	v_fmamk_f32 v24, v24, 0xbdd2d3e8, v99
	v_mul_f32_e32 v24, v54, v24
	v_exp_f32_e32 v24, v24
	v_mul_f32_e32 v25, v55, v55
	v_mul_f32_e32 v26, v56, v56
	v_fmamk_f32 v25, v25, 0xbdd2d3e8, v99
	v_fmamk_f32 v26, v26, 0xbdd2d3e8, v99
	v_mul_f32_e32 v25, v55, v25

.Lw3b73:
	v_add_f32_e32 v24, 1.0, v24
	v_mul_f32_e32 v26, v56, v26
	v_rcp_f32_e32 v24, v24
	v_exp_f32_e32 v25, v25
	v_exp_f32_e32 v26, v26
	v_mul_f32_e32 v30, v57, v57
	v_mul_f32_e32 v31, v58, v58
	v_fmamk_f32 v30, v30, 0xbdd2d3e8, v99
	v_fmamk_f32 v31, v31, 0xbdd2d3e8, v99
	v_fma_mixlo_f16 v29, v54, v24, 0
	v_add_f32_e32 v24, 1.0, v25
	v_add_f32_e32 v25, 1.0, v26
	v_mul_f32_e32 v30, v57, v30
	v_mul_f32_e32 v31, v58, v31
	v_rcp_f32_e32 v24, v24
	v_rcp_f32_e32 v25, v25
	v_exp_f32_e32 v30, v30
	v_exp_f32_e32 v31, v31
	v_mov_b32_e32 v26, v55
	v_mov_b32_e32 v27, v56
	v_pk_mul_f32 v[24:25], v[26:27], v[24:25]
	v_add_f32_e32 v26, 1.0, v30
	v_add_f32_e32 v27, 1.0, v31
	v_rcp_f32_e32 v26, v26
	v_rcp_f32_e32 v27, v27
	v_cvt_pk_f16_f32 v25, v24, v25

.Lw3b74:
	v_pk_mov_b32 v[30:31], v[56:57], v[58:59] op_sel:[1,0]
	v_pack_b32_f16 v24, v29, v25
	v_pk_mul_f32 v[26:27], v[30:31], v[26:27]
	v_mul_f32_e32 v29, v59, v59
	v_mul_f32_e32 v30, v60, v60
	v_fmamk_f32 v29, v29, 0xbdd2d3e8, v99
	v_fmamk_f32 v30, v30, 0xbdd2d3e8, v99
	v_mul_f32_e32 v29, v59, v29
	v_mul_f32_e32 v30, v60, v30
	v_exp_f32_e32 v29, v29
	v_exp_f32_e32 v30, v30
	v_cvt_pk_f16_f32 v32, v26, v27
	v_mov_b32_e32 v31, v60
	v_add_f32_e32 v26, 1.0, v29
	v_add_f32_e32 v27, 1.0, v30
	v_rcp_f32_e32 v26, v26
	v_rcp_f32_e32 v27, v27
	v_mov_b32_e32 v30, v59
	v_alignbit_b32 v25, v32, v25, 16
	v_mul_f32_e32 v34, v20, v20
	v_pk_mul_f32 v[26:27], v[30:31], v[26:27]
	v_fmamk_f32 v34, v34, 0xbdd2d3e8, v99

.Lw3b75:
	v_cvt_pk_f16_f32 v27, v26, v27
	v_mul_f32_e32 v26, v61, v61
	v_fmamk_f32 v26, v26, 0xbdd2d3e8, v99
	v_mul_f32_e32 v26, v61, v26
	v_exp_f32_e32 v29, v26
	v_alignbit_b32 v26, v27, v32, 16
	ds_read_b128 v[30:33], v28 offset:32768
	v_mul_f32_e32 v34, v20, v34
	v_add_f32_e32 v29, 1.0, v29
	v_rcp_f32_e32 v29, v29
	v_lshrrev_b32_e32 v27, 16, v27
	v_exp_f32_e32 v38, v34
	ds_read_b128 v[34:37], v28 offset:33792
	v_fma_mixhi_f16 v27, v61, v29, 0
	v_add_f32_e32 v29, 1.0, v38
	s_waitcnt lgkmcnt(1)
	v_mfma_f32_16x16x32_f16 v[24:27], v[30:33], v[24:27], 0
	v_mul_f32_e32 v30, v21, v21
	v_fmamk_f32 v30, v30, 0xbdd2d3e8, v99
	v_mul_f32_e32 v31, v22, v22
	v_mul_f32_e32 v30, v21, v30
	v_fmamk_f32 v31, v31, 0xbdd2d3e8, v99

.Lw3b76:
	v_rcp_f32_e32 v29, v29
	v_exp_f32_e32 v30, v30
	v_mul_f32_e32 v31, v22, v31
	v_exp_f32_e32 v31, v31
	v_fma_mixlo_f16 v29, v20, v29, 0
	v_add_f32_e32 v20, 1.0, v30
	v_rcp_f32_e32 v30, v20
	v_add_f32_e32 v20, 1.0, v31
	v_rcp_f32_e32 v31, v20
	v_mov_b32_e32 v20, v21
	v_mov_b32_e32 v21, v22
	v_mul_f32_e32 v22, v23, v23
	v_fmamk_f32 v22, v22, 0xbdd2d3e8, v99
	v_mul_f32_e32 v32, v16, v16
	v_mul_f32_e32 v22, v23, v22
	v_fmamk_f32 v32, v32, 0xbdd2d3e8, v99
	v_exp_f32_e32 v22, v22
	v_mul_f32_e32 v32, v16, v32
	v_exp_f32_e32 v32, v32
	v_pk_mul_f32 v[20:21], v[20:21], v[30:31]
	v_add_f32_e32 v22, 1.0, v22
	v_rcp_f32_e32 v30, v22
	v_add_f32_e32 v22, 1.0, v32
	v_rcp_f32_e32 v31, v22
	v_pk_mov_b32 v[22:23], v[22:23], v[16:17] op_sel:[1,0]
	v_cvt_pk_f16_f32 v21, v20, v21

.Lw3b77:
	v_mul_f32_e32 v16, v17, v17
	v_pk_mul_f32 v[22:23], v[22:23], v[30:31]
	v_pack_b32_f16 v20, v29, v21
	v_cvt_pk_f16_f32 v29, v22, v23
	v_fmamk_f32 v16, v16, 0xbdd2d3e8, v99
	v_mul_f32_e32 v22, v18, v18
	v_mul_f32_e32 v16, v17, v16
	v_fmamk_f32 v22, v22, 0xbdd2d3e8, v99
	v_exp_f32_e32 v16, v16
	v_mul_f32_e32 v22, v18, v22
	v_exp_f32_e32 v23, v22
	v_alignbit_b32 v21, v29, v21, 16
	v_add_f32_e32 v16, 1.0, v16
	v_rcp_f32_e32 v22, v16
	v_add_f32_e32 v16, 1.0, v23
	v_rcp_f32_e32 v23, v16
	v_mul_f32_e32 v16, v19, v19
	v_fmamk_f32 v16, v16, 0xbdd2d3e8, v99
	v_mul_f32_e32 v16, v19, v16
	v_exp_f32_e32 v30, v16
	v_mov_b32_e32 v16, v17
	v_mov_b32_e32 v17, v18
	v_pk_mul_f32 v[16:17], v[16:17], v[22:23]

.Lw3b78:
	v_add_f32_e32 v18, 1.0, v30
	v_rcp_f32_e32 v18, v18
	v_cvt_pk_f16_f32 v16, v16, v17
	v_lshrrev_b32_e32 v23, 16, v16
	v_alignbit_b32 v22, v16, v29, 16
	v_fma_mixhi_f16 v23, v19, v18, 0
	s_waitcnt lgkmcnt(0)
	s_nop 0
	v_mfma_f32_16x16x32_f16 v[16:19], v[34:37], v[20:23], v[24:27]
	v_mul_f32_e32 v20, v12, v12
	v_fmamk_f32 v20, v20, 0xbdd2d3e8, v99
	v_mul_f32_e32 v20, v12, v20
	v_exp_f32_e32 v20, v20
	v_mul_f32_e32 v21, v13, v13
	v_fmamk_f32 v21, v21, 0xbdd2d3e8, v99
	v_mul_f32_e32 v22, v14, v14
	v_mul_f32_e32 v21, v13, v21
	v_add_f32_e32 v20, 1.0, v20
	v_fmamk_f32 v22, v22, 0xbdd2d3e8, v99
	v_rcp_f32_e32 v20, v20
	v_exp_f32_e32 v21, v21
	v_mul_f32_e32 v22, v14, v22
	v_exp_f32_e32 v22, v22

.Lw3b79:
	v_fma_mixlo_f16 v23, v12, v20, 0
	v_add_f32_e32 v12, 1.0, v21
	v_rcp_f32_e32 v20, v12
	v_add_f32_e32 v12, 1.0, v22
	v_rcp_f32_e32 v21, v12
	v_mov_b32_e32 v12, v13
	v_mov_b32_e32 v13, v14
	v_mul_f32_e32 v14, v15, v15
	v_fmamk_f32 v14, v14, 0xbdd2d3e8, v99
	v_mul_f32_e32 v22, v8, v8
	v_mul_f32_e32 v14, v15, v14
	v_fmamk_f32 v22, v22, 0xbdd2d3e8, v99
	v_exp_f32_e32 v14, v14
	v_mul_f32_e32 v22, v8, v22
	v_exp_f32_e32 v22, v22
	v_pk_mul_f32 v[12:13], v[12:13], v[20:21]
	v_add_f32_e32 v14, 1.0, v14
	v_rcp_f32_e32 v20, v14
	v_add_f32_e32 v14, 1.0, v22
	v_rcp_f32_e32 v21, v14
	v_pk_mov_b32 v[14:15], v[14:15], v[8:9] op_sel:[1,0]
	v_mul_f32_e32 v8, v9, v9
	v_fmamk_f32 v8, v8, 0xbdd2d3e8, v99
	v_pk_mul_f32 v[14:15], v[14:15], v[20:21]

.Lw3b80:
	v_mul_f32_e32 v20, v10, v10
	v_mul_f32_e32 v8, v9, v8
	v_fmamk_f32 v20, v20, 0xbdd2d3e8, v99
	v_exp_f32_e32 v8, v8
	v_mul_f32_e32 v20, v10, v20
	v_exp_f32_e32 v20, v20
	v_cvt_pk_f16_f32 v21, v14, v15
	v_add_f32_e32 v8, 1.0, v8
	v_rcp_f32_e32 v14, v8
	v_add_f32_e32 v8, 1.0, v20
	v_rcp_f32_e32 v15, v8
	v_mov_b32_e32 v8, v9
	v_mov_b32_e32 v9, v10
	v_cvt_pk_f16_f32 v13, v12, v13
	v_pk_mul_f32 v[8:9], v[8:9], v[14:15]
	v_pack_b32_f16 v12, v23, v13
	v_cvt_pk_f16_f32 v8, v8, v9
	v_mul_f32_e32 v9, v11, v11
	v_fmamk_f32 v9, v9, 0xbdd2d3e8, v99
	v_mul_f32_e32 v9, v11, v9
	v_exp_f32_e32 v9, v9
	v_alignbit_b32 v13, v21, v13, 16
	v_alignbit_b32 v14, v8, v21, 16

.Lw3b81:
	ds_read_b128 v[20:23], v28 offset:34816
	v_lshrrev_b32_e32 v15, 16, v8
	v_add_f32_e32 v8, 1.0, v9
	v_rcp_f32_e32 v8, v8
	v_mul_f32_e32 v9, v4, v4
	v_fmamk_f32 v9, v9, 0xbdd2d3e8, v99
	v_mul_f32_e32 v9, v4, v9
	v_exp_f32_e32 v24, v9
	v_fma_mixhi_f16 v15, v11, v8, 0
	ds_read_b128 v[8:11], v28 offset:35840
	s_waitcnt lgkmcnt(1)
	v_mfma_f32_16x16x32_f16 v[12:15], v[20:23], v[12:15], v[16:19]
	s_nop 2
	v_mul_f32_e32 v17, v5, v5
	v_fmamk_f32 v17, v17, 0xbdd2d3e8, v99
	v_mul_f32_e32 v18, v6, v6
	v_add_f32_e32 v16, 1.0, v24
	v_mul_f32_e32 v17, v5, v17
	v_fmamk_f32 v18, v18, 0xbdd2d3e8, v99
	v_rcp_f32_e32 v16, v16
	v_exp_f32_e32 v17, v17
	v_mul_f32_e32 v18, v6, v18
	v_exp_f32_e32 v18, v18

.Lw3b82:
	v_fma_mixlo_f16 v19, v4, v16, 0
	v_add_f32_e32 v4, 1.0, v17
	v_rcp_f32_e32 v16, v4
	v_add_f32_e32 v4, 1.0, v18
	v_rcp_f32_e32 v17, v4
	v_mov_b32_e32 v4, v5
	v_mov_b32_e32 v5, v6
	v_mul_f32_e32 v6, v7, v7
	v_fmamk_f32 v6, v6, 0xbdd2d3e8, v99
	v_mul_f32_e32 v18, v0, v0
	v_mul_f32_e32 v6, v7, v6
	v_fmamk_f32 v18, v18, 0xbdd2d3e8, v99
	v_exp_f32_e32 v6, v6
	v_mul_f32_e32 v18, v0, v18
	v_exp_f32_e32 v18, v18
	v_pk_mul_f32 v[4:5], v[4:5], v[16:17]
	v_add_f32_e32 v6, 1.0, v6
	v_rcp_f32_e32 v16, v6
	v_add_f32_e32 v6, 1.0, v18
	v_rcp_f32_e32 v17, v6
	v_pk_mov_b32 v[6:7], v[6:7], v[0:1] op_sel:[1,0]
	v_mul_f32_e32 v0, v1, v1
	v_fmamk_f32 v0, v0, 0xbdd2d3e8, v99
	v_pk_mul_f32 v[6:7], v[6:7], v[16:17]

.Lw3b83:
	v_mul_f32_e32 v0, v1, v0
	v_cvt_pk_f16_f32 v16, v6, v7
	v_mul_f32_e32 v6, v2, v2
	v_fmamk_f32 v6, v6, 0xbdd2d3e8, v99
	v_exp_f32_e32 v0, v0
	v_mul_f32_e32 v6, v2, v6
	v_exp_f32_e32 v7, v6
	v_cvt_pk_f16_f32 v5, v4, v5
	v_add_f32_e32 v0, 1.0, v0
	v_rcp_f32_e32 v6, v0
	v_add_f32_e32 v0, 1.0, v7
	v_rcp_f32_e32 v7, v0
	v_mul_f32_e32 v0, v3, v3
	v_fmamk_f32 v0, v0, 0xbdd2d3e8, v99
	v_mul_f32_e32 v0, v3, v0
	v_exp_f32_e32 v17, v0
	v_mov_b32_e32 v0, v1
	v_mov_b32_e32 v1, v2
	v_pk_mul_f32 v[0:1], v[0:1], v[6:7]
	v_add_f32_e32 v2, 1.0, v17
	v_rcp_f32_e32 v2, v2
	v_cvt_pk_f16_f32 v0, v0, v1
	v_lshrrev_b32_e32 v7, 16, v0
	v_pack_b32_f16 v4, v19, v5

.Lw3b84:
	v_alignbit_b32 v5, v16, v5, 16
	v_alignbit_b32 v6, v0, v16, 16
	v_fma_mixhi_f16 v7, v3, v2, 0
	s_waitcnt lgkmcnt(0)
	s_nop 0
	v_mfma_f32_16x16x32_f16 v[0:3], v[8:11], v[4:7], v[12:15]
	s_and_saveexec_b64 s[14:15], s[4:5]
	s_xor_b64 s[14:15], exec, s[14:15]
	s_cbranch_execz .LBB3_9
	s_load_dwordx2 s[20:21], s[16:17], 0x0
	s_nop 3
	v_or_b32_e32 v2, s10, v80
	v_ashrrev_i32_e32 v3, 31, v2
	v_lshl_add_u64 v[2:3], v[2:3], 3, s[6:7]
	s_waitcnt lgkmcnt(0)
	v_pk_add_f32 v[0:1], v[0:1], s[20:21]
	global_store_dwordx2 v[2:3], v[0:1], off
	s_branch .LBB3_9

	.amdhsa_kernel _Z10k_layer_a2ILi1ELi13EEvPKDF16_PKiS3_PK15HIP_vector_typeIjLj4EES7_PKfS9_S9_S9_S9_S9_PDF16_Pf
		.amdhsa_group_segment_fixed_size 162052
		.amdhsa_private_segment_fixed_size 0
		.amdhsa_kernarg_size 360
		.amdhsa_user_sgpr_count 2
		.amdhsa_user_sgpr_dispatch_ptr 0
		.amdhsa_user_sgpr_queue_ptr 0
		.amdhsa_user_sgpr_kernarg_segment_ptr 1
		.amdhsa_user_sgpr_dispatch_id 0
		.amdhsa_user_sgpr_kernarg_preload_length 0
		.amdhsa_user_sgpr_kernarg_preload_offset 0
		.amdhsa_user_sgpr_private_segment_size 0
		.amdhsa_uses_dynamic_stack 0
		.amdhsa_enable_private_segment 0
		.amdhsa_system_sgpr_workgroup_id_x 1
		.amdhsa_system_sgpr_workgroup_id_y 0
		.amdhsa_system_sgpr_workgroup_id_z 0
		.amdhsa_system_sgpr_workgroup_info 0
		.amdhsa_system_vgpr_workitem_id 0
		.amdhsa_next_free_vgpr 128
		.amdhsa_next_free_sgpr 96
		.amdhsa_accum_offset 128
		.amdhsa_reserve_vcc 1
		.amdhsa_float_round_mode_32 0
		.amdhsa_float_round_mode_16_64 0
		.amdhsa_float_denorm_mode_32 3
		.amdhsa_float_denorm_mode_16_64 3
		.amdhsa_dx10_clamp 1
		.amdhsa_ieee_mode 1
		.amdhsa_fp16_overflow 0
		.amdhsa_tg_split 0
		.amdhsa_exception_fp_ieee_invalid_op 0
		.amdhsa_exception_fp_denorm_src 0
		.amdhsa_exception_fp_ieee_div_zero 0
		.amdhsa_exception_fp_ieee_overflow 0
		.amdhsa_exception_fp_ieee_underflow 0
		.amdhsa_exception_fp_ieee_inexact 0
		.amdhsa_exception_int_div_zero 0
	.end_amdhsa_kernel

amdhsa.kernels:
  - .agpr_count:     0
    .args:
      - .actual_access:  read_only
        .address_space:  global
        .offset:         0
        .size:           8
        .value_kind:     global_buffer
      - .actual_access:  read_only
        .address_space:  global
        .offset:         8
        .size:           8
        .value_kind:     global_buffer
      - .actual_access:  write_only
        .address_space:  global
        .offset:         16
        .size:           8
        .value_kind:     global_buffer
      - .actual_access:  write_only
        .address_space:  global
        .offset:         24
        .size:           8
        .value_kind:     global_buffer
      - .actual_access:  write_only
        .address_space:  global
        .offset:         32
        .size:           8
        .value_kind:     global_buffer
      - .actual_access:  read_only
        .address_space:  global
        .offset:         40
        .size:           8
        .value_kind:     global_buffer
      - .actual_access:  read_only
        .address_space:  global
        .offset:         48
        .size:           8
        .value_kind:     global_buffer
      - .actual_access:  read_only
        .address_space:  global
        .offset:         56
        .size:           8
        .value_kind:     global_buffer
      - .actual_access:  write_only
        .address_space:  global
        .offset:         64
        .size:           8
        .value_kind:     global_buffer
      - .actual_access:  write_only
        .address_space:  global
        .offset:         72
        .size:           8
        .value_kind:     global_buffer
      - .actual_access:  read_only
        .address_space:  global
        .offset:         80
        .size:           8
        .value_kind:     global_buffer
      - .address_space:  global
        .offset:         88
        .size:           8
        .value_kind:     global_buffer
      - .actual_access:  write_only
        .address_space:  global
        .offset:         96
        .size:           8
        .value_kind:     global_buffer
    .group_segment_fixed_size: 34400
    .kernarg_segment_align: 8
    .kernarg_segment_size: 104
    .language:       OpenCL C
    .language_version:
      - 2
      - 0
    .max_flat_workgroup_size: 1024
    .name:           _Z7k_frontPKiS0_PiS1_PjPKfS4_S4_P15HIP_vector_typeIjLj4EES7_PKS5_IfLj4EES7_S7_
    .private_segment_fixed_size: 0
    .sgpr_count:     44
    .sgpr_spill_count: 0
    .symbol:         _Z7k_frontPKiS0_PiS1_PjPKfS4_S4_P15HIP_vector_typeIjLj4EES7_PKS5_IfLj4EES7_S7_.kd
    .uniform_work_group_size: 1
    .uses_dynamic_stack: false
    .vgpr_count:     44
    .vgpr_spill_count: 0
    .wavefront_size: 64
  - .agpr_count:     0
    .args:
      - .actual_access:  read_only
        .address_space:  global
        .offset:         0
        .size:           8
        .value_kind:     global_buffer
      - .actual_access:  read_only
        .address_space:  global
        .offset:         8
        .size:           8
        .value_kind:     global_buffer
      - .actual_access:  read_only
        .address_space:  global
        .offset:         16
        .size:           8
        .value_kind:     global_buffer
      - .actual_access:  write_only
        .address_space:  global
        .offset:         24
        .size:           8
        .value_kind:     global_buffer
      - .address_space:  global
        .offset:         32
        .size:           8
        .value_kind:     global_buffer
      - .actual_access:  read_only
        .address_space:  global
        .offset:         40
        .size:           8
        .value_kind:     global_buffer
      - .address_space:  global
        .offset:         48
        .size:           8
        .value_kind:     global_buffer
    .group_segment_fixed_size: 72624
    .kernarg_segment_align: 8
    .kernarg_segment_size: 56
    .language:       OpenCL C
    .language_version:
      - 2
      - 0
    .max_flat_workgroup_size: 1024
    .name:           _Z8k_bucketPKiS0_PKjPiS3_PK15HIP_vector_typeIfLj4EEPS4_IjLj4EE
    .private_segment_fixed_size: 0
    .sgpr_count:     80
    .sgpr_spill_count: 0
    .symbol:         _Z8k_bucketPKiS0_PKjPiS3_PK15HIP_vector_typeIfLj4EEPS4_IjLj4EE.kd
    .uniform_work_group_size: 1
    .uses_dynamic_stack: false
    .vgpr_count:     64
    .vgpr_spill_count: 0
    .wavefront_size: 64
  - .agpr_count:     0
    .args:
      - .actual_access:  read_only
        .address_space:  global
        .offset:         0
        .size:           8
        .value_kind:     global_buffer
      - .actual_access:  read_only
        .address_space:  global
        .offset:         8
        .size:           8
        .value_kind:     global_buffer
      - .actual_access:  read_only
        .address_space:  global
        .offset:         16
        .size:           8
        .value_kind:     global_buffer
      - .actual_access:  read_only
        .address_space:  global
        .offset:         24
        .size:           8
        .value_kind:     global_buffer
      - .actual_access:  read_only
        .address_space:  global
        .offset:         32
        .size:           8
        .value_kind:     global_buffer
      - .actual_access:  read_only
        .address_space:  global
        .offset:         40
        .size:           8
        .value_kind:     global_buffer
      - .actual_access:  read_only
        .address_space:  global
        .offset:         48
        .size:           8
        .value_kind:     global_buffer
      - .actual_access:  read_only
        .address_space:  global
        .offset:         56
        .size:           8
        .value_kind:     global_buffer
      - .actual_access:  read_only
        .address_space:  global
        .offset:         64
        .size:           8
        .value_kind:     global_buffer
      - .actual_access:  read_only
        .address_space:  global
        .offset:         72
        .size:           8
        .value_kind:     global_buffer
      - .actual_access:  read_only
        .address_space:  global
        .offset:         80
        .size:           8
        .value_kind:     global_buffer
      - .actual_access:  write_only
        .address_space:  global
        .offset:         88
        .size:           8
        .value_kind:     global_buffer
      - .actual_access:  read_only
        .address_space:  global
        .offset:         96
        .size:           8
        .value_kind:     global_buffer
      - .offset:         104
        .size:           4
        .value_kind:     hidden_block_count_x
      - .offset:         108
        .size:           4
        .value_kind:     hidden_block_count_y
      - .offset:         112
        .size:           4
        .value_kind:     hidden_block_count_z
      - .offset:         116
        .size:           2
        .value_kind:     hidden_group_size_x
      - .offset:         118
        .size:           2
        .value_kind:     hidden_group_size_y
      - .offset:         120
        .size:           2
        .value_kind:     hidden_group_size_z
      - .offset:         122
        .size:           2
        .value_kind:     hidden_remainder_x
      - .offset:         124
        .size:           2
        .value_kind:     hidden_remainder_y
      - .offset:         126
        .size:           2
        .value_kind:     hidden_remainder_z
      - .offset:         144
        .size:           8
        .value_kind:     hidden_global_offset_x
      - .offset:         152
        .size:           8
        .value_kind:     hidden_global_offset_y
      - .offset:         160
        .size:           8
        .value_kind:     hidden_global_offset_z
      - .offset:         168
        .size:           2
        .value_kind:     hidden_grid_dims
    .group_segment_fixed_size: 125188
    .kernarg_segment_align: 8
    .kernarg_segment_size: 360
    .language:       OpenCL C
    .language_version:
      - 2
      - 0
    .max_flat_workgroup_size: 832
    .name:           _Z10k_layer_a2ILi0ELi13EEvPKDF16_PKiS3_PK15HIP_vector_typeIjLj4EES7_PKfS9_S9_S9_S9_S9_PDF16_Pf
    .private_segment_fixed_size: 0
    .sgpr_count:     68
    .sgpr_spill_count: 0
    .symbol:         _Z10k_layer_a2ILi0ELi13EEvPKDF16_PKiS3_PK15HIP_vector_typeIjLj4EES7_PKfS9_S9_S9_S9_S9_PDF16_Pf.kd
    .uniform_work_group_size: 1
    .uses_dynamic_stack: false
    .vgpr_count:     128
    .vgpr_spill_count: 0
    .wavefront_size: 64
  - .agpr_count:     0
    .args:
      - .actual_access:  read_only
        .address_space:  global
        .offset:         0
        .size:           8
        .value_kind:     global_buffer
      - .actual_access:  read_only
        .address_space:  global
        .offset:         8
        .size:           8
        .value_kind:     global_buffer
      - .actual_access:  read_only
        .address_space:  global
        .offset:         16
        .size:           8
        .value_kind:     global_buffer
      - .actual_access:  read_only
        .address_space:  global
        .offset:         24
        .size:           8
        .value_kind:     global_buffer
      - .actual_access:  read_only
        .address_space:  global
        .offset:         32
        .size:           8
        .value_kind:     global_buffer
      - .actual_access:  read_only
        .address_space:  global
        .offset:         40
        .size:           8
        .value_kind:     global_buffer
      - .actual_access:  read_only
        .address_space:  global
        .offset:         48
        .size:           8
        .value_kind:     global_buffer
      - .actual_access:  read_only
        .address_space:  global
        .offset:         56
        .size:           8
        .value_kind:     global_buffer
      - .actual_access:  read_only
        .address_space:  global
        .offset:         64
        .size:           8
        .value_kind:     global_buffer
      - .actual_access:  read_only
        .address_space:  global
        .offset:         72
        .size:           8
        .value_kind:     global_buffer
      - .actual_access:  read_only
        .address_space:  global
        .offset:         80
        .size:           8
        .value_kind:     global_buffer
      - .actual_access:  read_only
        .address_space:  global
        .offset:         88
        .size:           8
        .value_kind:     global_buffer
      - .actual_access:  write_only
        .address_space:  global
        .offset:         96
        .size:           8
        .value_kind:     global_buffer
      - .offset:         104
        .size:           4
        .value_kind:     hidden_block_count_x
      - .offset:         108
        .size:           4
        .value_kind:     hidden_block_count_y
      - .offset:         112
        .size:           4
        .value_kind:     hidden_block_count_z
      - .offset:         116
        .size:           2
        .value_kind:     hidden_group_size_x
      - .offset:         118
        .size:           2
        .value_kind:     hidden_group_size_y
      - .offset:         120
        .size:           2
        .value_kind:     hidden_group_size_z
      - .offset:         122
        .size:           2
        .value_kind:     hidden_remainder_x
      - .offset:         124
        .size:           2
        .value_kind:     hidden_remainder_y
      - .offset:         126
        .size:           2
        .value_kind:     hidden_remainder_z
      - .offset:         144
        .size:           8
        .value_kind:     hidden_global_offset_x
      - .offset:         152
        .size:           8
        .value_kind:     hidden_global_offset_y
      - .offset:         160
        .size:           8
        .value_kind:     hidden_global_offset_z
      - .offset:         168
        .size:           2
        .value_kind:     hidden_grid_dims
    .group_segment_fixed_size: 162052
    .kernarg_segment_align: 8
    .kernarg_segment_size: 360
    .language:       OpenCL C
    .language_version:
      - 2
      - 0
    .max_flat_workgroup_size: 832
    .name:           _Z10k_layer_a2ILi1ELi13EEvPKDF16_PKiS3_PK15HIP_vector_typeIjLj4EES7_PKfS9_S9_S9_S9_S9_PDF16_Pf
    .private_segment_fixed_size: 0
    .sgpr_count:     68
    .sgpr_spill_count: 0
    .symbol:         _Z10k_layer_a2ILi1ELi13EEvPKDF16_PKiS3_PK15HIP_vector_typeIjLj4EES7_PKfS9_S9_S9_S9_S9_PDF16_Pf.kd
    .uniform_work_group_size: 1
    .uses_dynamic_stack: false
    .vgpr_count:     128
    .vgpr_spill_count: 0
    .wavefront_size: 64
